# conversion loops: wait for all outstanding VMEM (incl. previous item's stores) before issuing each item's 32 loads
# baseline (speedup 1.0000x reference)
.LBB0_72:
	s_ashr_i32 s0, s12, 8
	s_lshl_b32 s1, s13, 19
	s_lshl_b32 s24, s94, 3
	s_lshl_b32 s5, s5, 5
	s_mul_hi_i32 s9, s1, s0
	s_mul_i32 s1, s1, s0
	s_add_u32 s0, s6, s1
	s_addc_u32 s1, s7, s9
	s_lshl_b32 s6, s12, 5
	s_and_b32 s6, s6, 0x1fe0
	s_add_u32 s0, s0, s6
	s_mul_hi_i32 s7, s8, s5
	s_mul_i32 s6, s8, s5
	s_addc_u32 s1, s1, 0
	s_lshl_b64 s[6:7], s[6:7], 2
	s_add_u32 s6, s10, s6
	s_mul_i32 s26, s5, s13
	s_addc_u32 s7, s11, s7
	s_ashr_i32 s5, s4, 31
	s_lshl_b64 s[4:5], s[4:5], 2
	s_add_u32 s6, s6, s4
	s_addc_u32 s7, s7, s5
	v_mov_b32_e32 v39, 0
	v_lshlrev_b32_e32 v38, 2, v33
	s_mov_b32 s9, 0
	v_lshl_add_u64 v[2:3], s[6:7], 0, v[38:39]
	s_lshl_b32 s8, s8, 2
	v_lshl_add_u64 v[2:3], v[2:3], 0, s[8:9]
	v_lshl_add_u64 v[4:5], v[2:3], 0, s[8:9]
	v_lshl_add_u64 v[6:7], v[4:5], 0, s[8:9]
	v_lshl_add_u64 v[8:9], v[6:7], 0, s[8:9]
	v_lshl_add_u64 v[10:11], v[8:9], 0, s[8:9]
	v_lshl_add_u64 v[12:13], v[10:11], 0, s[8:9]
	v_lshl_add_u64 v[14:15], v[12:13], 0, s[8:9]
	v_lshl_add_u64 v[16:17], v[14:15], 0, s[8:9]
	v_lshl_add_u64 v[18:19], v[16:17], 0, s[8:9]
	v_lshl_add_u64 v[20:21], v[18:19], 0, s[8:9]
	v_lshl_add_u64 v[22:23], v[20:21], 0, s[8:9]
	v_lshl_add_u64 v[24:25], v[22:23], 0, s[8:9]
	v_lshl_add_u64 v[26:27], v[24:25], 0, s[8:9]
	v_lshl_add_u64 v[28:29], v[26:27], 0, s[8:9]
	v_lshl_add_u64 v[30:31], v[28:29], 0, s[8:9]
	v_lshl_add_u64 v[34:35], v[30:31], 0, s[8:9]
	v_lshl_add_u64 v[36:37], v[34:35], 0, s[8:9]
	v_lshl_add_u64 v[40:41], v[36:37], 0, s[8:9]
	v_lshl_add_u64 v[42:43], v[40:41], 0, s[8:9]
	v_lshl_add_u64 v[44:45], v[42:43], 0, s[8:9]
	v_lshl_add_u64 v[46:47], v[44:45], 0, s[8:9]
	v_lshl_add_u64 v[48:49], v[46:47], 0, s[8:9]
	v_lshl_add_u64 v[50:51], v[48:49], 0, s[8:9]
	v_lshl_add_u64 v[52:53], v[50:51], 0, s[8:9]
	v_lshl_add_u64 v[54:55], v[52:53], 0, s[8:9]
	v_lshl_add_u64 v[56:57], v[54:55], 0, s[8:9]
	v_lshl_add_u64 v[58:59], v[56:57], 0, s[8:9]
	v_lshl_add_u64 v[60:61], v[58:59], 0, s[8:9]
	v_lshl_add_u64 v[62:63], v[60:61], 0, s[8:9]
	v_lshl_add_u64 v[64:65], v[62:63], 0, s[8:9]
	v_lshl_add_u64 v[66:67], v[64:65], 0, s[8:9]
	s_waitcnt vmcnt(0)
	global_load_dword v1, v[2:3], off nt
	s_nop 0
	global_load_dword v2, v[4:5], off nt
	global_load_dword v3, v[6:7], off nt
	s_nop 0
	global_load_dword v4, v[8:9], off nt
	global_load_dword v5, v[10:11], off nt
	s_nop 0
	global_load_dword v8, v[12:13], off nt
	global_load_dword v7, v[14:15], off nt
	global_load_dword v10, v[16:17], off nt
	global_load_dword v9, v[18:19], off nt
	s_nop 0
	global_load_dword v12, v[20:21], off nt
	global_load_dword v11, v[22:23], off nt
	global_load_dword v14, v[24:25], off nt
	global_load_dword v13, v[26:27], off nt
	global_load_dword v16, v[28:29], off nt
	global_load_dword v15, v[30:31], off nt
	global_load_dword v18, v[34:35], off nt
	global_load_dword v17, v[36:37], off nt
	global_load_dword v20, v[40:41], off nt
	global_load_dword v19, v[42:43], off nt
	global_load_dword v22, v[44:45], off nt
	global_load_dword v21, v[46:47], off nt
	global_load_dword v24, v[48:49], off nt
	global_load_dword v23, v[50:51], off nt
	global_load_dword v26, v[52:53], off nt
	global_load_dword v25, v[54:55], off nt
	global_load_dword v28, v[56:57], off nt
	global_load_dword v27, v[58:59], off nt
	global_load_dword v30, v[60:61], off nt
	global_load_dword v29, v[62:63], off nt
	global_load_dword v32, v[64:65], off nt
	global_load_dword v31, v[66:67], off nt
	global_load_dword v6, v38, s[6:7] nt
	s_add_i32 s14, s43, s24
	s_cmpk_gt_i32 s14, 0x1fff
	s_mov_b64 s[4:5], s[0:1]
	s_mov_b32 s44, s26
	s_mov_b32 s27, s25
	s_waitcnt lgkmcnt(0)
	v_mov_b32_e32 v76, v73
	s_cbranch_scc1 .LBB0_90
	s_cmpk_lt_i32 s14, 0x1800
	s_cselect_b64 s[4:5], -1, 0
	s_cmpk_gt_i32 s14, 0x17ff
	s_cbranch_scc1 .LBB0_77
	s_mul_hi_i32 s6, s14, 0x2aaaaaab
	s_lshr_b32 s7, s6, 31
	s_ashr_i32 s6, s6, 4
	s_add_i32 s7, s6, s7
	s_mul_i32 s6, s7, 0x60
	s_sub_i32 s10, s14, s6
	s_lshl_b32 s6, s10, 6
	s_add_u32 s8, s96, 0x800000
	s_addc_u32 s9, s97, 0
	s_cmp_gt_i32 s10, 31
	s_cbranch_scc0 .LBB0_79
	s_lshl_b32 s12, s10, 7
	s_cmp_gt_u32 s10, 63
	s_cbranch_scc0 .LBB0_80
	s_and_b32 s10, s12, 0x3f00
	s_and_b32 s11, s6, 64
	s_or_b32 s10, s10, s11
	s_xor_b32 s16, s10, 0x2080
	s_mov_b64 s[10:11], 0
	s_branch .LBB0_81

.LBB0_89:
	s_ashr_i32 s4, s16, 8
	s_lshl_b32 s5, s15, 19
	s_lshl_b32 s13, s7, 5
	s_mul_hi_i32 s7, s5, s4
	s_mul_i32 s5, s5, s4
	s_add_u32 s4, s8, s5
	s_addc_u32 s5, s9, s7
	s_lshl_b32 s7, s16, 5
	s_and_b32 s7, s7, 0x1fe0
	s_add_u32 s4, s4, s7
	s_mul_hi_i32 s17, s12, s13
	s_mul_i32 s16, s12, s13
	s_addc_u32 s5, s5, 0
	s_lshl_b64 s[16:17], s[16:17], 2
	s_add_u32 s8, s10, s16
	s_addc_u32 s10, s11, s17
	s_ashr_i32 s7, s6, 31
	s_lshl_b64 s[6:7], s[6:7], 2
	s_add_u32 s6, s8, s6
	s_addc_u32 s7, s10, s7
	v_mov_b32_e32 v39, 0
	s_mov_b32 s9, 0
	v_lshl_add_u64 v[34:35], s[6:7], 0, v[38:39]
	s_lshl_b32 s8, s12, 2
	v_lshl_add_u64 v[34:35], v[34:35], 0, s[8:9]
	v_lshl_add_u64 v[36:37], v[34:35], 0, s[8:9]
	v_lshl_add_u64 v[40:41], v[36:37], 0, s[8:9]
	v_lshl_add_u64 v[42:43], v[40:41], 0, s[8:9]
	v_lshl_add_u64 v[44:45], v[42:43], 0, s[8:9]
	v_lshl_add_u64 v[46:47], v[44:45], 0, s[8:9]
	v_lshl_add_u64 v[48:49], v[46:47], 0, s[8:9]
	s_waitcnt vmcnt(0)
	global_load_dword v77, v38, s[6:7] nt
	global_load_dword v78, v[34:35], off nt
	global_load_dword v79, v[36:37], off nt
	global_load_dword v80, v[40:41], off nt
	global_load_dword v81, v[42:43], off nt
	global_load_dword v82, v[44:45], off nt
	global_load_dword v83, v[46:47], off nt
	global_load_dword v84, v[48:49], off nt
	v_lshl_add_u64 v[34:35], v[48:49], 0, s[8:9]
	global_load_dword v85, v[34:35], off nt
	v_lshl_add_u64 v[34:35], v[34:35], 0, s[8:9]
	global_load_dword v86, v[34:35], off nt
	v_lshl_add_u64 v[34:35], v[34:35], 0, s[8:9]
	global_load_dword v87, v[34:35], off nt
	v_lshl_add_u64 v[34:35], v[34:35], 0, s[8:9]
	global_load_dword v88, v[34:35], off nt
	v_lshl_add_u64 v[34:35], v[34:35], 0, s[8:9]
	global_load_dword v89, v[34:35], off nt
	v_lshl_add_u64 v[34:35], v[34:35], 0, s[8:9]
	global_load_dword v90, v[34:35], off nt
	v_lshl_add_u64 v[34:35], v[34:35], 0, s[8:9]
	global_load_dword v93, v[34:35], off nt
	v_lshl_add_u64 v[34:35], v[34:35], 0, s[8:9]
	global_load_dword v94, v[34:35], off nt
	v_lshl_add_u64 v[34:35], v[34:35], 0, s[8:9]
	global_load_dword v95, v[34:35], off nt
	v_lshl_add_u64 v[34:35], v[34:35], 0, s[8:9]
	global_load_dword v96, v[34:35], off nt
	v_lshl_add_u64 v[34:35], v[34:35], 0, s[8:9]
	global_load_dword v97, v[34:35], off nt
	v_lshl_add_u64 v[34:35], v[34:35], 0, s[8:9]
	global_load_dword v98, v[34:35], off nt
	v_lshl_add_u64 v[34:35], v[34:35], 0, s[8:9]
	global_load_dword v99, v[34:35], off nt
	v_lshl_add_u64 v[34:35], v[34:35], 0, s[8:9]
	global_load_dword v100, v[34:35], off nt
	v_lshl_add_u64 v[34:35], v[34:35], 0, s[8:9]
	global_load_dword v101, v[34:35], off nt
	v_lshl_add_u64 v[34:35], v[34:35], 0, s[8:9]
	global_load_dword v102, v[34:35], off nt
	v_lshl_add_u64 v[34:35], v[34:35], 0, s[8:9]
	global_load_dword v103, v[34:35], off nt
	v_lshl_add_u64 v[34:35], v[34:35], 0, s[8:9]
	global_load_dword v104, v[34:35], off nt
	v_lshl_add_u64 v[34:35], v[34:35], 0, s[8:9]
	global_load_dword v105, v[34:35], off nt
	v_lshl_add_u64 v[34:35], v[34:35], 0, s[8:9]
	global_load_dword v106, v[34:35], off nt
	v_lshl_add_u64 v[34:35], v[34:35], 0, s[8:9]
	global_load_dword v107, v[34:35], off nt
	v_lshl_add_u64 v[34:35], v[34:35], 0, s[8:9]
	global_load_dword v108, v[34:35], off nt
	v_lshl_add_u64 v[34:35], v[34:35], 0, s[8:9]
	global_load_dword v109, v[34:35], off nt
	v_lshl_add_u64 v[34:35], v[34:35], 0, s[8:9]
	global_load_dword v110, v[34:35], off nt
	s_mul_i32 s44, s13, s15

.LBB0_108:
	s_lshl_b32 s21, s10, 5
	s_ashr_i32 s10, s17, 8
	s_lshl_b32 s12, s46, 19
	s_mul_hi_i32 s13, s12, s10
	s_mul_i32 s12, s12, s10
	s_add_u32 s10, s22, s12
	s_addc_u32 s13, s23, s13
	s_lshl_b32 s12, s17, 5
	s_and_b32 s12, s12, 0x1fe0
	s_add_u32 s12, s10, s12
	s_mul_hi_i32 s23, s20, s21
	s_mul_i32 s22, s20, s21
	s_addc_u32 s13, s13, 0
	s_lshl_b64 s[22:23], s[22:23], 2
	s_add_u32 s10, s18, s22
	s_addc_u32 s18, s19, s23
	s_ashr_i32 s17, s16, 31
	s_lshl_b64 s[16:17], s[16:17], 2
	s_add_u32 s16, s10, s16
	s_addc_u32 s17, s18, s17
	v_lshl_add_u64 v[34:35], s[16:17], 0, v[38:39]
	s_lshl_b32 s10, s20, 2
	v_lshl_add_u64 v[34:35], v[34:35], 0, s[10:11]
	v_lshl_add_u64 v[36:37], v[34:35], 0, s[10:11]
	s_waitcnt vmcnt(25)
	v_lshl_add_u64 v[46:47], v[36:37], 0, s[10:11]
	s_waitcnt vmcnt(22)
	v_lshl_add_u64 v[48:49], v[46:47], 0, s[10:11]
	s_waitcnt vmcnt(21)
	v_lshl_add_u64 v[50:51], v[48:49], 0, s[10:11]
	s_waitcnt vmcnt(18)
	v_lshl_add_u64 v[52:53], v[50:51], 0, s[10:11]
	s_waitcnt vmcnt(17)
	v_lshl_add_u64 v[54:55], v[52:53], 0, s[10:11]
	s_waitcnt vmcnt(0)
	global_load_dword v42, v38, s[16:17] nt
	global_load_dword v44, v[34:35], off nt
	global_load_dword v33, v[36:37], off nt
	global_load_dword v43, v[46:47], off nt
	s_nop 0
	global_load_dword v46, v[48:49], off nt
	s_nop 0
	global_load_dword v48, v[50:51], off nt
	global_load_dword v45, v[52:53], off nt
	global_load_dword v47, v[54:55], off nt
	v_lshl_add_u64 v[34:35], v[54:55], 0, s[10:11]
	global_load_dword v50, v[34:35], off nt
	v_lshl_add_u64 v[34:35], v[34:35], 0, s[10:11]
	global_load_dword v52, v[34:35], off nt
	v_lshl_add_u64 v[34:35], v[34:35], 0, s[10:11]
	global_load_dword v49, v[34:35], off nt
	v_lshl_add_u64 v[34:35], v[34:35], 0, s[10:11]
	global_load_dword v51, v[34:35], off nt
	v_lshl_add_u64 v[34:35], v[34:35], 0, s[10:11]
	global_load_dword v54, v[34:35], off nt
	v_lshl_add_u64 v[34:35], v[34:35], 0, s[10:11]
	global_load_dword v56, v[34:35], off nt
	v_lshl_add_u64 v[34:35], v[34:35], 0, s[10:11]
	global_load_dword v53, v[34:35], off nt
	v_lshl_add_u64 v[34:35], v[34:35], 0, s[10:11]
	global_load_dword v55, v[34:35], off nt
	v_lshl_add_u64 v[34:35], v[34:35], 0, s[10:11]
	global_load_dword v58, v[34:35], off nt
	v_lshl_add_u64 v[34:35], v[34:35], 0, s[10:11]
	global_load_dword v60, v[34:35], off nt
	v_lshl_add_u64 v[34:35], v[34:35], 0, s[10:11]
	global_load_dword v57, v[34:35], off nt
	v_lshl_add_u64 v[34:35], v[34:35], 0, s[10:11]
	global_load_dword v59, v[34:35], off nt
	v_lshl_add_u64 v[34:35], v[34:35], 0, s[10:11]
	global_load_dword v62, v[34:35], off nt
	v_lshl_add_u64 v[34:35], v[34:35], 0, s[10:11]
	global_load_dword v64, v[34:35], off nt
	v_lshl_add_u64 v[34:35], v[34:35], 0, s[10:11]
	global_load_dword v61, v[34:35], off nt
	v_lshl_add_u64 v[34:35], v[34:35], 0, s[10:11]
	global_load_dword v63, v[34:35], off nt
	v_lshl_add_u64 v[34:35], v[34:35], 0, s[10:11]
	global_load_dword v66, v[34:35], off nt
	v_lshl_add_u64 v[34:35], v[34:35], 0, s[10:11]
	global_load_dword v68, v[34:35], off nt
	v_lshl_add_u64 v[34:35], v[34:35], 0, s[10:11]
	global_load_dword v65, v[34:35], off nt
	v_lshl_add_u64 v[34:35], v[34:35], 0, s[10:11]
	global_load_dword v67, v[34:35], off nt
	v_lshl_add_u64 v[34:35], v[34:35], 0, s[10:11]
	global_load_dword v70, v[34:35], off nt
	v_lshl_add_u64 v[34:35], v[34:35], 0, s[10:11]
	global_load_dword v72, v[34:35], off nt
	v_lshl_add_u64 v[34:35], v[34:35], 0, s[10:11]
	global_load_dword v69, v[34:35], off nt
	v_lshl_add_u64 v[34:35], v[34:35], 0, s[10:11]
	global_load_dword v71, v[34:35], off nt
	s_mul_i32 s46, s21, s46

.LBB0_135:
	s_ashr_i32 s0, s17, 8
	s_lshl_b32 s1, s48, 19
	s_lshl_b32 s10, s10, 5
	s_mul_hi_i32 s21, s1, s0
	s_mul_i32 s1, s1, s0
	s_add_u32 s0, s22, s1
	s_addc_u32 s1, s23, s21
	s_lshl_b32 s17, s17, 5
	s_and_b32 s17, s17, 0x1fe0
	s_add_u32 s0, s0, s17
	s_mul_hi_i32 s23, s20, s10
	s_mul_i32 s22, s20, s10
	s_addc_u32 s1, s1, 0
	s_lshl_b64 s[22:23], s[22:23], 2
	s_mul_i32 s26, s10, s48
	s_add_u32 s10, s18, s22
	s_addc_u32 s18, s19, s23
	s_ashr_i32 s17, s16, 31
	s_lshl_b64 s[16:17], s[16:17], 2
	s_add_u32 s16, s10, s16
	s_addc_u32 s17, s18, s17
	s_waitcnt vmcnt(30)
	v_lshl_add_u64 v[2:3], s[16:17], 0, v[38:39]
	s_lshl_b32 s10, s20, 2
	v_lshl_add_u64 v[2:3], v[2:3], 0, s[10:11]
	s_waitcnt vmcnt(28)
	v_lshl_add_u64 v[4:5], v[2:3], 0, s[10:11]
	s_waitcnt vmcnt(0)
	global_load_dword v6, v38, s[16:17] nt
	global_load_dword v1, v[2:3], off nt
	s_nop 0
	global_load_dword v2, v[4:5], off nt
	v_lshl_add_u64 v[4:5], v[4:5], 0, s[10:11]
	s_waitcnt vmcnt(27)
	v_lshl_add_u64 v[8:9], v[4:5], 0, s[10:11]
	global_load_dword v3, v[4:5], off nt
	s_nop 0
	global_load_dword v4, v[8:9], off nt
	v_lshl_add_u64 v[8:9], v[8:9], 0, s[10:11]
	s_waitcnt vmcnt(27)
	v_lshl_add_u64 v[10:11], v[8:9], 0, s[10:11]
	global_load_dword v5, v[8:9], off nt
	s_nop 0
	global_load_dword v8, v[10:11], off nt
	v_lshl_add_u64 v[10:11], v[10:11], 0, s[10:11]
	s_waitcnt vmcnt(27)
	v_lshl_add_u64 v[12:13], v[10:11], 0, s[10:11]
	global_load_dword v7, v[10:11], off nt
	s_nop 0
	global_load_dword v10, v[12:13], off nt
	v_lshl_add_u64 v[12:13], v[12:13], 0, s[10:11]
	s_waitcnt vmcnt(27)
	v_lshl_add_u64 v[14:15], v[12:13], 0, s[10:11]
	global_load_dword v9, v[12:13], off nt
	s_nop 0
	global_load_dword v12, v[14:15], off nt
	v_lshl_add_u64 v[14:15], v[14:15], 0, s[10:11]
	s_waitcnt vmcnt(27)
	v_lshl_add_u64 v[16:17], v[14:15], 0, s[10:11]
	global_load_dword v11, v[14:15], off nt
	s_nop 0
	global_load_dword v14, v[16:17], off nt
	v_lshl_add_u64 v[16:17], v[16:17], 0, s[10:11]
	s_waitcnt vmcnt(27)
	v_lshl_add_u64 v[18:19], v[16:17], 0, s[10:11]
	global_load_dword v13, v[16:17], off nt
	s_nop 0
	global_load_dword v16, v[18:19], off nt
	v_lshl_add_u64 v[18:19], v[18:19], 0, s[10:11]
	s_waitcnt vmcnt(27)
	v_lshl_add_u64 v[20:21], v[18:19], 0, s[10:11]
	global_load_dword v15, v[18:19], off nt
	s_nop 0
	global_load_dword v18, v[20:21], off nt
	v_lshl_add_u64 v[20:21], v[20:21], 0, s[10:11]
	s_waitcnt vmcnt(27)
	v_lshl_add_u64 v[22:23], v[20:21], 0, s[10:11]
	global_load_dword v17, v[20:21], off nt
	s_nop 0
	global_load_dword v20, v[22:23], off nt
	v_lshl_add_u64 v[22:23], v[22:23], 0, s[10:11]
	s_waitcnt vmcnt(27)
	v_lshl_add_u64 v[24:25], v[22:23], 0, s[10:11]
	global_load_dword v19, v[22:23], off nt
	s_nop 0
	global_load_dword v22, v[24:25], off nt
	v_lshl_add_u64 v[24:25], v[24:25], 0, s[10:11]
	s_waitcnt vmcnt(27)
	v_lshl_add_u64 v[26:27], v[24:25], 0, s[10:11]
	global_load_dword v21, v[24:25], off nt
	s_nop 0
	global_load_dword v24, v[26:27], off nt
	v_lshl_add_u64 v[26:27], v[26:27], 0, s[10:11]
	s_waitcnt vmcnt(27)
	v_lshl_add_u64 v[28:29], v[26:27], 0, s[10:11]
	global_load_dword v23, v[26:27], off nt
	s_nop 0
	global_load_dword v26, v[28:29], off nt
	v_lshl_add_u64 v[28:29], v[28:29], 0, s[10:11]
	s_waitcnt vmcnt(27)
	v_lshl_add_u64 v[30:31], v[28:29], 0, s[10:11]
	global_load_dword v25, v[28:29], off nt
	s_nop 0
	global_load_dword v28, v[30:31], off nt
	v_lshl_add_u64 v[30:31], v[30:31], 0, s[10:11]
	v_lshl_add_u64 v[34:35], v[30:31], 0, s[10:11]
	global_load_dword v27, v[30:31], off nt
	s_nop 0
	global_load_dword v30, v[34:35], off nt
	v_lshl_add_u64 v[34:35], v[34:35], 0, s[10:11]
	global_load_dword v29, v[34:35], off nt
	v_lshl_add_u64 v[34:35], v[34:35], 0, s[10:11]
	global_load_dword v32, v[34:35], off nt
	v_lshl_add_u64 v[34:35], v[34:35], 0, s[10:11]
	global_load_dword v31, v[34:35], off nt

.LBB0_162:
	s_ashr_i32 s4, s23, 8
	s_lshl_b32 s5, s22, 19
	s_lshl_b32 s19, s15, 5
	s_mul_hi_i32 s10, s5, s4
	s_mul_i32 s5, s5, s4
	s_add_u32 s4, s20, s5
	s_addc_u32 s5, s21, s10
	s_lshl_b32 s10, s23, 5
	s_and_b32 s10, s10, 0x1fe0
	s_add_u32 s4, s4, s10
	s_mul_hi_i32 s21, s18, s19
	s_mul_i32 s20, s18, s19
	s_addc_u32 s5, s5, 0
	s_lshl_b64 s[20:21], s[20:21], 2
	s_add_u32 s10, s16, s20
	s_addc_u32 s16, s17, s21
	s_ashr_i32 s15, s14, 31
	s_lshl_b64 s[14:15], s[14:15], 2
	s_add_u32 s14, s10, s14
	s_addc_u32 s15, s16, s15
	v_lshl_add_u64 v[34:35], s[14:15], 0, v[38:39]
	s_lshl_b32 s10, s18, 2
	v_lshl_add_u64 v[34:35], v[34:35], 0, s[10:11]
	v_lshl_add_u64 v[36:37], v[34:35], 0, s[10:11]
	v_lshl_add_u64 v[74:75], v[36:37], 0, s[10:11]
	s_waitcnt vmcnt(27)
	v_lshl_add_u64 v[82:83], v[74:75], 0, s[10:11]
	s_waitcnt vmcnt(25)
	v_lshl_add_u64 v[84:85], v[82:83], 0, s[10:11]
	s_waitcnt vmcnt(23)
	v_lshl_add_u64 v[86:87], v[84:85], 0, s[10:11]
	s_waitcnt vmcnt(21)
	v_lshl_add_u64 v[88:89], v[86:87], 0, s[10:11]
	s_waitcnt vmcnt(0)
	global_load_dword v77, v38, s[14:15] nt
	global_load_dword v78, v[34:35], off nt
	global_load_dword v79, v[36:37], off nt
	global_load_dword v80, v[74:75], off nt
	global_load_dword v81, v[82:83], off nt
	s_nop 0
	global_load_dword v82, v[84:85], off nt
	global_load_dword v83, v[86:87], off nt
	s_nop 0
	global_load_dword v84, v[88:89], off nt
	v_lshl_add_u64 v[34:35], v[88:89], 0, s[10:11]
	global_load_dword v85, v[34:35], off nt
	v_lshl_add_u64 v[34:35], v[34:35], 0, s[10:11]
	global_load_dword v86, v[34:35], off nt
	v_lshl_add_u64 v[34:35], v[34:35], 0, s[10:11]
	global_load_dword v87, v[34:35], off nt
	v_lshl_add_u64 v[34:35], v[34:35], 0, s[10:11]
	global_load_dword v88, v[34:35], off nt
	v_lshl_add_u64 v[34:35], v[34:35], 0, s[10:11]
	global_load_dword v89, v[34:35], off nt
	v_lshl_add_u64 v[34:35], v[34:35], 0, s[10:11]
	global_load_dword v90, v[34:35], off nt
	v_lshl_add_u64 v[34:35], v[34:35], 0, s[10:11]
	global_load_dword v93, v[34:35], off nt
	v_lshl_add_u64 v[34:35], v[34:35], 0, s[10:11]
	global_load_dword v94, v[34:35], off nt
	v_lshl_add_u64 v[34:35], v[34:35], 0, s[10:11]
	global_load_dword v95, v[34:35], off nt
	v_lshl_add_u64 v[34:35], v[34:35], 0, s[10:11]
	global_load_dword v96, v[34:35], off nt
	v_lshl_add_u64 v[34:35], v[34:35], 0, s[10:11]
	global_load_dword v97, v[34:35], off nt
	v_lshl_add_u64 v[34:35], v[34:35], 0, s[10:11]
	global_load_dword v98, v[34:35], off nt
	v_lshl_add_u64 v[34:35], v[34:35], 0, s[10:11]
	global_load_dword v99, v[34:35], off nt
	v_lshl_add_u64 v[34:35], v[34:35], 0, s[10:11]
	global_load_dword v100, v[34:35], off nt
	v_lshl_add_u64 v[34:35], v[34:35], 0, s[10:11]
	global_load_dword v101, v[34:35], off nt
	v_lshl_add_u64 v[34:35], v[34:35], 0, s[10:11]
	global_load_dword v102, v[34:35], off nt
	v_lshl_add_u64 v[34:35], v[34:35], 0, s[10:11]
	global_load_dword v103, v[34:35], off nt
	v_lshl_add_u64 v[34:35], v[34:35], 0, s[10:11]
	global_load_dword v104, v[34:35], off nt
	v_lshl_add_u64 v[34:35], v[34:35], 0, s[10:11]
	global_load_dword v105, v[34:35], off nt
	v_lshl_add_u64 v[34:35], v[34:35], 0, s[10:11]
	global_load_dword v106, v[34:35], off nt
	v_lshl_add_u64 v[34:35], v[34:35], 0, s[10:11]
	global_load_dword v107, v[34:35], off nt
	v_lshl_add_u64 v[34:35], v[34:35], 0, s[10:11]
	global_load_dword v108, v[34:35], off nt
	v_lshl_add_u64 v[34:35], v[34:35], 0, s[10:11]
	global_load_dword v109, v[34:35], off nt
	v_lshl_add_u64 v[34:35], v[34:35], 0, s[10:11]
	global_load_dword v110, v[34:35], off nt
	s_mul_i32 s44, s19, s22

.LBB0_362:
	s_ashr_i32 s16, s25, 8
	s_ashr_i32 s17, s16, 31
	s_mul_i32 s19, s16, s19
	s_mul_hi_u32 s20, s16, s18
	s_add_i32 s19, s20, s19
	s_mul_i32 s17, s17, s18
	s_add_i32 s17, s19, s17
	s_mul_i32 s16, s16, s18
	s_lshl_b32 s26, s94, 3
	s_lshl_b32 s3, s3, 5
	s_lshl_b64 s[16:17], s[16:17], 8
	s_add_u32 s14, s16, s14
	s_addc_u32 s15, s17, s15
	s_mul_i32 s15, s15, s27
	s_mul_hi_u32 s16, s14, s27
	s_add_i32 s16, s16, s15
	s_mul_i32 s14, s14, s27
	s_add_u32 s0, s0, s14
	s_addc_u32 s1, s1, s16
	s_lshl_b32 s14, s25, 5
	s_and_b32 s14, s14, 0x1fe0
	s_add_u32 s0, s0, s14
	s_addc_u32 s1, s1, 0
	s_ashr_i32 s14, s3, 31
	s_mul_i32 s14, s12, s14
	s_mul_hi_u32 s15, s12, s3
	s_add_i32 s14, s15, s14
	s_mul_i32 s15, s13, s3
	s_add_i32 s15, s14, s15
	s_mul_i32 s14, s12, s3
	s_lshl_b64 s[14:15], s[14:15], 2
	s_add_u32 s10, s10, s14
	s_mul_i32 s52, s3, s27
	s_addc_u32 s11, s11, s15
	s_ashr_i32 s3, s2, 31
	s_lshl_b64 s[2:3], s[2:3], 2
	v_and_b32_e32 v38, 63, v2
	s_add_u32 s2, s10, s2
	v_mov_b32_e32 v39, 0
	s_addc_u32 s3, s11, s3
	v_lshlrev_b32_e32 v40, 2, v38
	v_mov_b32_e32 v41, v39
	v_lshl_add_u64 v[2:3], s[2:3], 0, v[40:41]
	s_lshl_b64 s[10:11], s[12:13], 2
	v_lshl_add_u64 v[2:3], v[2:3], 0, s[10:11]
	v_lshl_add_u64 v[4:5], v[2:3], 0, s[10:11]
	v_lshl_add_u64 v[6:7], v[4:5], 0, s[10:11]
	v_lshl_add_u64 v[8:9], v[6:7], 0, s[10:11]
	v_lshl_add_u64 v[10:11], v[8:9], 0, s[10:11]
	v_lshl_add_u64 v[12:13], v[10:11], 0, s[10:11]
	v_lshl_add_u64 v[14:15], v[12:13], 0, s[10:11]
	v_lshl_add_u64 v[16:17], v[14:15], 0, s[10:11]
	v_lshl_add_u64 v[18:19], v[16:17], 0, s[10:11]
	v_lshl_add_u64 v[20:21], v[18:19], 0, s[10:11]
	v_lshl_add_u64 v[22:23], v[20:21], 0, s[10:11]
	v_lshl_add_u64 v[24:25], v[22:23], 0, s[10:11]
	v_lshl_add_u64 v[26:27], v[24:25], 0, s[10:11]
	v_lshl_add_u64 v[28:29], v[26:27], 0, s[10:11]
	v_lshl_add_u64 v[30:31], v[28:29], 0, s[10:11]
	v_lshl_add_u64 v[32:33], v[30:31], 0, s[10:11]
	v_lshl_add_u64 v[34:35], v[32:33], 0, s[10:11]
	v_lshl_add_u64 v[36:37], v[34:35], 0, s[10:11]
	v_lshl_add_u64 v[42:43], v[36:37], 0, s[10:11]
	v_lshl_add_u64 v[44:45], v[42:43], 0, s[10:11]
	v_lshl_add_u64 v[46:47], v[44:45], 0, s[10:11]
	v_lshl_add_u64 v[48:49], v[46:47], 0, s[10:11]
	v_lshl_add_u64 v[50:51], v[48:49], 0, s[10:11]
	v_lshl_add_u64 v[52:53], v[50:51], 0, s[10:11]
	v_lshl_add_u64 v[54:55], v[52:53], 0, s[10:11]
	v_lshl_add_u64 v[56:57], v[54:55], 0, s[10:11]
	v_lshl_add_u64 v[58:59], v[56:57], 0, s[10:11]
	v_lshl_add_u64 v[60:61], v[58:59], 0, s[10:11]
	v_lshl_add_u64 v[62:63], v[60:61], 0, s[10:11]
	v_lshl_add_u64 v[64:65], v[62:63], 0, s[10:11]
	v_lshl_add_u64 v[66:67], v[64:65], 0, s[10:11]
	s_waitcnt vmcnt(0)
	global_load_dword v1, v[2:3], off nt
	s_nop 0
	global_load_dword v2, v[4:5], off nt
	global_load_dword v3, v[6:7], off nt
	s_nop 0
	global_load_dword v4, v[8:9], off nt
	global_load_dword v5, v[10:11], off nt
	global_load_dword v6, v[12:13], off nt
	global_load_dword v7, v[14:15], off nt
	s_nop 0
	global_load_dword v8, v[16:17], off nt
	global_load_dword v9, v[18:19], off nt
	global_load_dword v10, v[20:21], off nt
	global_load_dword v11, v[22:23], off nt
	global_load_dword v12, v[24:25], off nt
	global_load_dword v13, v[26:27], off nt
	global_load_dword v14, v[28:29], off nt
	global_load_dword v15, v[30:31], off nt
	global_load_dword v16, v[32:33], off nt
	global_load_dword v17, v[34:35], off nt
	global_load_dword v18, v[36:37], off nt
	global_load_dword v19, v[42:43], off nt
	global_load_dword v20, v[44:45], off nt
	global_load_dword v21, v[46:47], off nt
	global_load_dword v22, v[48:49], off nt
	global_load_dword v23, v[50:51], off nt
	global_load_dword v24, v[52:53], off nt
	global_load_dword v25, v[54:55], off nt
	global_load_dword v26, v[56:57], off nt
	global_load_dword v27, v[58:59], off nt
	global_load_dword v28, v[60:61], off nt
	global_load_dword v29, v[62:63], off nt
	global_load_dword v30, v[64:65], off nt
	global_load_dword v31, v[66:67], off nt
	global_load_dword v32, v40, s[2:3] nt
	s_add_i32 s27, s24, s26
	s_cmp_gt_i32 s27, 0xa7ff
	s_mov_b64 s[22:23], s[0:1]
	s_mov_b32 s72, s52
	s_mov_b32 s51, s49
	s_waitcnt lgkmcnt(0)
	v_mov_b32_e32 v79, v73
	s_mov_b32 s53, s50
	s_cbranch_scc1 .LBB0_411
	s_cmpk_gt_i32 s27, 0x17ff
	s_cbranch_scc0 .LBB0_371
	s_cmpk_gt_u32 s27, 0x1fff
	s_cbranch_scc0 .LBB0_374
	s_cmpk_gt_u32 s27, 0x35ff
	s_cbranch_scc0 .LBB0_375
	s_cmpk_gt_u32 s27, 0x4bff
	s_cbranch_scc0 .LBB0_376
	s_cmpk_gt_u32 s27, 0x61ff
	s_cbranch_scc0 .LBB0_377
	s_cmpk_gt_u32 s27, 0x79ff
	s_cbranch_scc0 .LBB0_378
	s_cmpk_gt_u32 s27, 0x81ff
	s_cbranch_scc0 .LBB0_379
	s_add_i32 s2, s27, 0x7e00
	s_and_b32 s10, s2, 0xffff
	s_add_i32 s3, s27, 0x6200
	s_cmpk_lt_u32 s10, 0x1c00
	s_cselect_b32 s2, s2, s3
	s_bfe_u32 s3, s2, 0xc0004
	s_mulk_i32 s3, 0x2493
	s_lshr_b32 s3, s3, 16
	s_mul_i32 s11, s3, 0x70
	s_sub_i32 s14, s2, s11
	s_lshl_b32 s15, s14, 6
	s_and_b32 s2, s15, 0xffc0
	s_cmpk_gt_u32 s10, 0x1bff
	s_cselect_b32 s10, 0x3800000, 0
	s_cselect_b32 s16, 0x1c00000, 0
	s_add_u32 s10, s64, s10
	s_addc_u32 s11, s65, 0
	s_add_u32 s12, s96, 0x8a00000
	s_addc_u32 s13, s97, 0
	s_lshl_b32 s14, s14, 7
	s_and_b32 s14, s14, 0x3f00
	s_and_b32 s15, s15, 64
	s_mov_b32 s17, 0
	s_or_b32 s28, s14, s15
	s_mov_b64 s[14:15], 0
	s_branch .LBB0_380

.LBB0_410:
	s_lshl_b32 s24, s3, 5
	s_ashr_i32 s3, s28, 8
	s_ashr_i32 s18, s3, 31
	s_mul_i32 s19, s3, s21
	s_mul_hi_u32 s21, s3, s20
	s_add_i32 s19, s21, s19
	s_mul_i32 s18, s18, s20
	s_add_i32 s19, s19, s18
	s_mul_i32 s18, s3, s20
	s_lshl_b64 s[18:19], s[18:19], 8
	s_add_u32 s3, s18, s16
	s_addc_u32 s16, s19, s17
	s_mul_i32 s16, s16, s30
	s_mul_hi_u32 s17, s3, s30
	s_add_i32 s17, s17, s16
	s_mul_i32 s3, s3, s30
	s_add_u32 s3, s12, s3
	s_addc_u32 s12, s13, s17
	s_lshl_b32 s13, s28, 5
	s_and_b32 s13, s13, 0x1fe0
	s_add_u32 s22, s3, s13
	s_addc_u32 s23, s12, 0
	s_ashr_i32 s3, s24, 31
	s_mul_i32 s3, s14, s3
	s_mul_hi_u32 s12, s14, s24
	s_add_i32 s3, s12, s3
	s_mul_i32 s12, s15, s24
	s_add_i32 s13, s3, s12
	s_mul_i32 s12, s14, s24
	s_lshl_b64 s[12:13], s[12:13], 2
	s_add_u32 s10, s10, s12
	s_addc_u32 s11, s11, s13
	s_ashr_i32 s3, s2, 31
	s_lshl_b64 s[2:3], s[2:3], 2
	s_add_u32 s2, s10, s2
	s_addc_u32 s3, s11, s3
	v_mov_b32_e32 v41, 0
	v_lshl_add_u64 v[34:35], s[2:3], 0, v[40:41]
	s_waitcnt vmcnt(0)
	global_load_dword v80, v40, s[2:3] nt
	s_lshl_b64 s[2:3], s[14:15], 2
	v_lshl_add_u64 v[34:35], v[34:35], 0, s[2:3]
	v_lshl_add_u64 v[36:37], v[34:35], 0, s[2:3]
	v_lshl_add_u64 v[42:43], v[36:37], 0, s[2:3]
	v_lshl_add_u64 v[44:45], v[42:43], 0, s[2:3]
	v_lshl_add_u64 v[46:47], v[44:45], 0, s[2:3]
	v_lshl_add_u64 v[48:49], v[46:47], 0, s[2:3]
	v_lshl_add_u64 v[50:51], v[48:49], 0, s[2:3]
	global_load_dword v81, v[34:35], off nt
	global_load_dword v82, v[36:37], off nt
	global_load_dword v83, v[42:43], off nt
	global_load_dword v84, v[44:45], off nt
	global_load_dword v85, v[46:47], off nt
	global_load_dword v86, v[48:49], off nt
	global_load_dword v87, v[50:51], off nt
	v_lshl_add_u64 v[34:35], v[50:51], 0, s[2:3]
	global_load_dword v88, v[34:35], off nt
	v_lshl_add_u64 v[34:35], v[34:35], 0, s[2:3]
	global_load_dword v89, v[34:35], off nt
	v_lshl_add_u64 v[34:35], v[34:35], 0, s[2:3]
	global_load_dword v90, v[34:35], off nt
	v_lshl_add_u64 v[34:35], v[34:35], 0, s[2:3]
	global_load_dword v91, v[34:35], off nt
	v_lshl_add_u64 v[34:35], v[34:35], 0, s[2:3]
	global_load_dword v92, v[34:35], off nt
	v_lshl_add_u64 v[34:35], v[34:35], 0, s[2:3]
	global_load_dword v93, v[34:35], off nt
	v_lshl_add_u64 v[34:35], v[34:35], 0, s[2:3]
	global_load_dword v94, v[34:35], off nt
	v_lshl_add_u64 v[34:35], v[34:35], 0, s[2:3]
	global_load_dword v95, v[34:35], off nt
	v_lshl_add_u64 v[34:35], v[34:35], 0, s[2:3]
	global_load_dword v96, v[34:35], off nt
	v_lshl_add_u64 v[34:35], v[34:35], 0, s[2:3]
	global_load_dword v97, v[34:35], off nt
	v_lshl_add_u64 v[34:35], v[34:35], 0, s[2:3]
	global_load_dword v98, v[34:35], off nt
	v_lshl_add_u64 v[34:35], v[34:35], 0, s[2:3]
	global_load_dword v99, v[34:35], off nt
	v_lshl_add_u64 v[34:35], v[34:35], 0, s[2:3]
	global_load_dword v100, v[34:35], off nt
	v_lshl_add_u64 v[34:35], v[34:35], 0, s[2:3]
	global_load_dword v101, v[34:35], off nt
	v_lshl_add_u64 v[34:35], v[34:35], 0, s[2:3]
	global_load_dword v102, v[34:35], off nt
	v_lshl_add_u64 v[34:35], v[34:35], 0, s[2:3]
	global_load_dword v103, v[34:35], off nt
	v_lshl_add_u64 v[34:35], v[34:35], 0, s[2:3]
	global_load_dword v104, v[34:35], off nt
	v_lshl_add_u64 v[34:35], v[34:35], 0, s[2:3]
	global_load_dword v105, v[34:35], off nt
	v_lshl_add_u64 v[34:35], v[34:35], 0, s[2:3]
	global_load_dword v106, v[34:35], off nt
	v_lshl_add_u64 v[34:35], v[34:35], 0, s[2:3]
	global_load_dword v107, v[34:35], off nt
	v_lshl_add_u64 v[34:35], v[34:35], 0, s[2:3]
	global_load_dword v108, v[34:35], off nt
	v_lshl_add_u64 v[34:35], v[34:35], 0, s[2:3]
	global_load_dword v109, v[34:35], off nt
	v_lshl_add_u64 v[34:35], v[34:35], 0, s[2:3]
	global_load_dword v110, v[34:35], off nt
	v_lshl_add_u64 v[34:35], v[34:35], 0, s[2:3]
	global_load_dword v111, v[34:35], off nt
	s_mul_i32 s72, s24, s30

.LBB0_452:
	s_lshl_b32 s20, s29, 5
	s_ashr_i32 s29, s73, 8
	s_ashr_i32 s36, s29, 31
	s_mul_i32 s37, s29, s41
	s_mul_hi_u32 s41, s29, s40
	s_add_i32 s37, s41, s37
	s_mul_i32 s36, s36, s40
	s_add_i32 s37, s37, s36
	s_mul_i32 s36, s29, s40
	s_lshl_b64 s[36:37], s[36:37], 8
	s_add_u32 s24, s36, s24
	s_addc_u32 s25, s37, s25
	s_mul_i32 s25, s25, s76
	s_mul_hi_u32 s29, s24, s76
	s_add_i32 s29, s29, s25
	s_mul_i32 s24, s24, s76
	s_add_u32 s24, s38, s24
	s_addc_u32 s25, s39, s29
	s_lshl_b32 s29, s73, 5
	s_and_b32 s29, s29, 0x1fe0
	s_add_u32 s24, s24, s29
	s_addc_u32 s25, s25, 0
	s_ashr_i32 s29, s20, 31
	s_mul_i32 s29, s34, s29
	s_mul_hi_u32 s36, s34, s20
	s_add_i32 s29, s36, s29
	s_mul_i32 s36, s35, s20
	s_add_i32 s37, s29, s36
	s_mul_i32 s36, s34, s20
	s_lshl_b64 s[36:37], s[36:37], 2
	s_add_u32 s30, s30, s36
	s_addc_u32 s31, s31, s37
	s_ashr_i32 s29, s28, 31
	s_lshl_b64 s[28:29], s[28:29], 2
	s_add_u32 s28, s30, s28
	s_addc_u32 s29, s31, s29
	v_lshl_add_u64 v[34:35], s[28:29], 0, v[40:41]
	s_waitcnt vmcnt(0)
	global_load_dword v42, v40, s[28:29] nt
	s_lshl_b64 s[28:29], s[34:35], 2
	v_lshl_add_u64 v[34:35], v[34:35], 0, s[28:29]
	v_lshl_add_u64 v[36:37], v[34:35], 0, s[28:29]
	s_waitcnt vmcnt(26)
	v_lshl_add_u64 v[46:47], v[36:37], 0, s[28:29]
	s_waitcnt vmcnt(23)
	v_lshl_add_u64 v[48:49], v[46:47], 0, s[28:29]
	s_waitcnt vmcnt(22)
	v_lshl_add_u64 v[50:51], v[48:49], 0, s[28:29]
	s_waitcnt vmcnt(19)
	v_lshl_add_u64 v[52:53], v[50:51], 0, s[28:29]
	s_waitcnt vmcnt(18)
	v_lshl_add_u64 v[54:55], v[52:53], 0, s[28:29]
	global_load_dword v44, v[34:35], off nt
	global_load_dword v33, v[36:37], off nt
	global_load_dword v43, v[46:47], off nt
	s_nop 0
	global_load_dword v46, v[48:49], off nt
	s_nop 0
	global_load_dword v48, v[50:51], off nt
	global_load_dword v45, v[52:53], off nt
	global_load_dword v47, v[54:55], off nt
	v_lshl_add_u64 v[34:35], v[54:55], 0, s[28:29]
	global_load_dword v50, v[34:35], off nt
	v_lshl_add_u64 v[34:35], v[34:35], 0, s[28:29]
	global_load_dword v52, v[34:35], off nt
	v_lshl_add_u64 v[34:35], v[34:35], 0, s[28:29]
	global_load_dword v49, v[34:35], off nt
	v_lshl_add_u64 v[34:35], v[34:35], 0, s[28:29]
	global_load_dword v51, v[34:35], off nt
	v_lshl_add_u64 v[34:35], v[34:35], 0, s[28:29]
	global_load_dword v54, v[34:35], off nt
	v_lshl_add_u64 v[34:35], v[34:35], 0, s[28:29]
	global_load_dword v56, v[34:35], off nt
	v_lshl_add_u64 v[34:35], v[34:35], 0, s[28:29]
	global_load_dword v53, v[34:35], off nt
	v_lshl_add_u64 v[34:35], v[34:35], 0, s[28:29]
	global_load_dword v55, v[34:35], off nt
	v_lshl_add_u64 v[34:35], v[34:35], 0, s[28:29]
	global_load_dword v58, v[34:35], off nt
	v_lshl_add_u64 v[34:35], v[34:35], 0, s[28:29]
	global_load_dword v60, v[34:35], off nt
	v_lshl_add_u64 v[34:35], v[34:35], 0, s[28:29]
	global_load_dword v57, v[34:35], off nt
	v_lshl_add_u64 v[34:35], v[34:35], 0, s[28:29]
	global_load_dword v59, v[34:35], off nt
	v_lshl_add_u64 v[34:35], v[34:35], 0, s[28:29]
	global_load_dword v62, v[34:35], off nt
	v_lshl_add_u64 v[34:35], v[34:35], 0, s[28:29]
	global_load_dword v64, v[34:35], off nt
	v_lshl_add_u64 v[34:35], v[34:35], 0, s[28:29]
	global_load_dword v61, v[34:35], off nt
	v_lshl_add_u64 v[34:35], v[34:35], 0, s[28:29]
	global_load_dword v63, v[34:35], off nt
	v_lshl_add_u64 v[34:35], v[34:35], 0, s[28:29]
	global_load_dword v66, v[34:35], off nt
	v_lshl_add_u64 v[34:35], v[34:35], 0, s[28:29]
	global_load_dword v68, v[34:35], off nt
	v_lshl_add_u64 v[34:35], v[34:35], 0, s[28:29]
	global_load_dword v65, v[34:35], off nt
	v_lshl_add_u64 v[34:35], v[34:35], 0, s[28:29]
	global_load_dword v67, v[34:35], off nt
	v_lshl_add_u64 v[34:35], v[34:35], 0, s[28:29]
	global_load_dword v70, v[34:35], off nt
	v_lshl_add_u64 v[34:35], v[34:35], 0, s[28:29]
	global_load_dword v72, v[34:35], off nt
	v_lshl_add_u64 v[34:35], v[34:35], 0, s[28:29]
	global_load_dword v69, v[34:35], off nt
	v_lshl_add_u64 v[34:35], v[34:35], 0, s[28:29]
	global_load_dword v71, v[34:35], off nt
	s_mul_i32 s73, s20, s76

.LBB0_510:
	s_lshl_b32 s20, s29, 5
	s_ashr_i32 s29, s75, 8
	s_ashr_i32 s36, s29, 31
	s_mul_i32 s37, s29, s41
	s_mul_hi_u32 s41, s29, s40
	s_add_i32 s37, s41, s37
	s_mul_i32 s36, s36, s40
	s_add_i32 s37, s37, s36
	s_mul_i32 s36, s29, s40
	s_lshl_b64 s[36:37], s[36:37], 8
	s_add_u32 s0, s36, s0
	s_addc_u32 s1, s37, s1
	s_mul_i32 s1, s1, s77
	s_mul_hi_u32 s29, s0, s77
	s_add_i32 s29, s29, s1
	s_mul_i32 s0, s0, s77
	s_add_u32 s0, s38, s0
	s_addc_u32 s1, s39, s29
	s_lshl_b32 s29, s75, 5
	s_and_b32 s29, s29, 0x1fe0
	s_add_u32 s0, s0, s29
	s_addc_u32 s1, s1, 0
	s_ashr_i32 s29, s20, 31
	s_mul_i32 s29, s34, s29
	s_mul_hi_u32 s36, s34, s20
	s_add_i32 s29, s36, s29
	s_mul_i32 s36, s35, s20
	s_add_i32 s37, s29, s36
	s_mul_i32 s36, s34, s20
	s_lshl_b64 s[36:37], s[36:37], 2
	s_mul_i32 s52, s20, s77
	s_add_u32 s20, s30, s36
	s_addc_u32 s30, s31, s37
	s_ashr_i32 s29, s28, 31
	s_lshl_b64 s[28:29], s[28:29], 2
	s_add_u32 s28, s20, s28
	s_addc_u32 s29, s30, s29
	s_waitcnt vmcnt(30)
	v_lshl_add_u64 v[2:3], s[28:29], 0, v[40:41]
	s_lshl_b64 s[30:31], s[34:35], 2
	v_lshl_add_u64 v[2:3], v[2:3], 0, s[30:31]
	s_waitcnt vmcnt(28)
	v_lshl_add_u64 v[4:5], v[2:3], 0, s[30:31]
	s_waitcnt vmcnt(26)
	v_lshl_add_u64 v[6:7], v[4:5], 0, s[30:31]
	s_waitcnt vmcnt(24)
	v_lshl_add_u64 v[8:9], v[6:7], 0, s[30:31]
	s_waitcnt vmcnt(22)
	v_lshl_add_u64 v[10:11], v[8:9], 0, s[30:31]
	s_waitcnt vmcnt(20)
	v_lshl_add_u64 v[12:13], v[10:11], 0, s[30:31]
	s_waitcnt vmcnt(18)
	v_lshl_add_u64 v[14:15], v[12:13], 0, s[30:31]
	s_waitcnt vmcnt(16)
	v_lshl_add_u64 v[16:17], v[14:15], 0, s[30:31]
	s_waitcnt vmcnt(14)
	v_lshl_add_u64 v[18:19], v[16:17], 0, s[30:31]
	s_waitcnt vmcnt(12)
	v_lshl_add_u64 v[20:21], v[18:19], 0, s[30:31]
	s_waitcnt vmcnt(10)
	v_lshl_add_u64 v[22:23], v[20:21], 0, s[30:31]
	s_waitcnt vmcnt(8)
	v_lshl_add_u64 v[24:25], v[22:23], 0, s[30:31]
	s_waitcnt vmcnt(6)
	v_lshl_add_u64 v[26:27], v[24:25], 0, s[30:31]
	s_waitcnt vmcnt(4)
	v_lshl_add_u64 v[28:29], v[26:27], 0, s[30:31]
	s_waitcnt vmcnt(2)
	v_lshl_add_u64 v[30:31], v[28:29], 0, s[30:31]
	v_lshl_add_u64 v[34:35], v[30:31], 0, s[30:31]
	v_lshl_add_u64 v[36:37], v[34:35], 0, s[30:31]
	v_lshl_add_u64 v[74:75], v[36:37], 0, s[30:31]
	v_lshl_add_u64 v[114:115], v[74:75], 0, s[30:31]
	v_lshl_add_u64 v[116:117], v[114:115], 0, s[30:31]
	v_lshl_add_u64 v[118:119], v[116:117], 0, s[30:31]
	v_lshl_add_u64 v[120:121], v[118:119], 0, s[30:31]
	v_lshl_add_u64 v[122:123], v[120:121], 0, s[30:31]
	v_lshl_add_u64 v[124:125], v[122:123], 0, s[30:31]
	v_lshl_add_u64 v[126:127], v[124:125], 0, s[30:31]
	v_lshl_add_u64 v[128:129], v[126:127], 0, s[30:31]
	v_lshl_add_u64 v[130:131], v[128:129], 0, s[30:31]
	v_lshl_add_u64 v[132:133], v[130:131], 0, s[30:31]
	v_lshl_add_u64 v[134:135], v[132:133], 0, s[30:31]
	v_lshl_add_u64 v[136:137], v[134:135], 0, s[30:31]
	v_lshl_add_u64 v[138:139], v[136:137], 0, s[30:31]
	s_waitcnt vmcnt(0)
	global_load_dword v1, v[2:3], off nt
	s_nop 0
	global_load_dword v2, v[4:5], off nt
	global_load_dword v3, v[6:7], off nt
	s_nop 0
	global_load_dword v4, v[8:9], off nt
	global_load_dword v5, v[10:11], off nt
	global_load_dword v6, v[12:13], off nt
	global_load_dword v7, v[14:15], off nt
	s_nop 0
	global_load_dword v8, v[16:17], off nt
	global_load_dword v9, v[18:19], off nt
	global_load_dword v10, v[20:21], off nt
	global_load_dword v11, v[22:23], off nt
	global_load_dword v12, v[24:25], off nt
	global_load_dword v13, v[26:27], off nt
	global_load_dword v14, v[28:29], off nt
	global_load_dword v15, v[30:31], off nt
	global_load_dword v16, v[34:35], off nt
	global_load_dword v17, v[36:37], off nt
	global_load_dword v18, v[74:75], off nt
	global_load_dword v19, v[114:115], off nt
	global_load_dword v20, v[116:117], off nt
	global_load_dword v21, v[118:119], off nt
	global_load_dword v22, v[120:121], off nt
	global_load_dword v23, v[122:123], off nt
	global_load_dword v24, v[124:125], off nt
	global_load_dword v25, v[126:127], off nt
	global_load_dword v26, v[128:129], off nt
	global_load_dword v27, v[130:131], off nt
	global_load_dword v28, v[132:133], off nt
	global_load_dword v29, v[134:135], off nt
	global_load_dword v30, v[136:137], off nt
	global_load_dword v31, v[138:139], off nt
	global_load_dword v32, v40, s[28:29] nt

.LBB0_567:
	s_ashr_i32 s27, s72, 8
	s_ashr_i32 s34, s27, 31
	s_mul_i32 s35, s27, s39
	s_mul_hi_u32 s39, s27, s38
	s_add_i32 s35, s39, s35
	s_mul_i32 s34, s34, s38
	s_add_i32 s35, s35, s34
	s_mul_i32 s34, s27, s38
	s_lshl_b32 s20, s44, 5
	s_lshl_b64 s[34:35], s[34:35], 8
	s_add_u32 s22, s34, s22
	s_addc_u32 s23, s35, s23
	s_mul_i32 s23, s23, s74
	s_mul_hi_u32 s27, s22, s74
	s_add_i32 s27, s27, s23
	s_mul_i32 s22, s22, s74
	s_add_u32 s22, s36, s22
	s_addc_u32 s23, s37, s27
	s_lshl_b32 s27, s72, 5
	s_and_b32 s27, s27, 0x1fe0
	s_add_u32 s22, s22, s27
	s_addc_u32 s23, s23, 0
	s_ashr_i32 s27, s20, 31
	s_mul_i32 s27, s30, s27
	s_mul_hi_u32 s34, s30, s20
	s_add_i32 s27, s34, s27
	s_mul_i32 s34, s31, s20
	s_add_i32 s35, s27, s34
	s_mul_i32 s34, s30, s20
	s_lshl_b64 s[34:35], s[34:35], 2
	s_add_u32 s28, s28, s34
	s_addc_u32 s29, s29, s35
	s_ashr_i32 s27, s26, 31
	s_lshl_b64 s[26:27], s[26:27], 2
	s_add_u32 s26, s28, s26
	s_addc_u32 s27, s29, s27
	v_lshl_add_u64 v[34:35], s[26:27], 0, v[40:41]
	s_waitcnt vmcnt(0)
	global_load_dword v80, v40, s[26:27] nt
	s_lshl_b64 s[26:27], s[30:31], 2
	v_lshl_add_u64 v[34:35], v[34:35], 0, s[26:27]
	v_lshl_add_u64 v[36:37], v[34:35], 0, s[26:27]
	v_lshl_add_u64 v[74:75], v[36:37], 0, s[26:27]
	s_waitcnt vmcnt(29)
	v_lshl_add_u64 v[84:85], v[74:75], 0, s[26:27]
	s_waitcnt vmcnt(27)
	v_lshl_add_u64 v[86:87], v[84:85], 0, s[26:27]
	s_waitcnt vmcnt(25)
	v_lshl_add_u64 v[88:89], v[86:87], 0, s[26:27]
	s_waitcnt vmcnt(23)
	v_lshl_add_u64 v[90:91], v[88:89], 0, s[26:27]
	global_load_dword v81, v[34:35], off nt
	global_load_dword v82, v[36:37], off nt
	global_load_dword v83, v[74:75], off nt
	s_nop 0
	global_load_dword v84, v[84:85], off nt
	s_nop 0
	global_load_dword v85, v[86:87], off nt
	s_nop 0
	global_load_dword v86, v[88:89], off nt
	global_load_dword v87, v[90:91], off nt
	v_lshl_add_u64 v[34:35], v[90:91], 0, s[26:27]
	global_load_dword v88, v[34:35], off nt
	v_lshl_add_u64 v[34:35], v[34:35], 0, s[26:27]
	global_load_dword v89, v[34:35], off nt
	v_lshl_add_u64 v[34:35], v[34:35], 0, s[26:27]
	global_load_dword v90, v[34:35], off nt
	v_lshl_add_u64 v[34:35], v[34:35], 0, s[26:27]
	global_load_dword v91, v[34:35], off nt
	v_lshl_add_u64 v[34:35], v[34:35], 0, s[26:27]
	global_load_dword v92, v[34:35], off nt
	v_lshl_add_u64 v[34:35], v[34:35], 0, s[26:27]
	global_load_dword v93, v[34:35], off nt
	v_lshl_add_u64 v[34:35], v[34:35], 0, s[26:27]
	global_load_dword v94, v[34:35], off nt
	v_lshl_add_u64 v[34:35], v[34:35], 0, s[26:27]
	global_load_dword v95, v[34:35], off nt
	v_lshl_add_u64 v[34:35], v[34:35], 0, s[26:27]
	global_load_dword v96, v[34:35], off nt
	v_lshl_add_u64 v[34:35], v[34:35], 0, s[26:27]
	global_load_dword v97, v[34:35], off nt
	v_lshl_add_u64 v[34:35], v[34:35], 0, s[26:27]
	global_load_dword v98, v[34:35], off nt
	v_lshl_add_u64 v[34:35], v[34:35], 0, s[26:27]
	global_load_dword v99, v[34:35], off nt
	v_lshl_add_u64 v[34:35], v[34:35], 0, s[26:27]
	global_load_dword v100, v[34:35], off nt
	v_lshl_add_u64 v[34:35], v[34:35], 0, s[26:27]
	global_load_dword v101, v[34:35], off nt
	v_lshl_add_u64 v[34:35], v[34:35], 0, s[26:27]
	global_load_dword v102, v[34:35], off nt
	v_lshl_add_u64 v[34:35], v[34:35], 0, s[26:27]
	global_load_dword v103, v[34:35], off nt
	v_lshl_add_u64 v[34:35], v[34:35], 0, s[26:27]
	global_load_dword v104, v[34:35], off nt
	v_lshl_add_u64 v[34:35], v[34:35], 0, s[26:27]
	global_load_dword v105, v[34:35], off nt
	v_lshl_add_u64 v[34:35], v[34:35], 0, s[26:27]
	global_load_dword v106, v[34:35], off nt
	v_lshl_add_u64 v[34:35], v[34:35], 0, s[26:27]
	global_load_dword v107, v[34:35], off nt
	v_lshl_add_u64 v[34:35], v[34:35], 0, s[26:27]
	global_load_dword v108, v[34:35], off nt
	v_lshl_add_u64 v[34:35], v[34:35], 0, s[26:27]
	global_load_dword v109, v[34:35], off nt
	v_lshl_add_u64 v[34:35], v[34:35], 0, s[26:27]
	global_load_dword v110, v[34:35], off nt
	v_lshl_add_u64 v[34:35], v[34:35], 0, s[26:27]
	global_load_dword v111, v[34:35], off nt
	s_mul_i32 s72, s20, s74

.LBB0_813:
	s_ashr_i32 s12, s21, 8
	s_ashr_i32 s13, s12, 31
	s_mul_i32 s15, s12, s15
	s_mul_hi_u32 s16, s12, s14
	s_add_i32 s15, s16, s15
	s_mul_i32 s13, s13, s14
	s_add_i32 s13, s15, s13
	s_mul_i32 s12, s12, s14
	s_lshl_b32 s22, s94, 3
	s_lshl_b32 s3, s3, 5
	s_lshl_b64 s[12:13], s[12:13], 8
	s_add_u32 s10, s12, s10
	s_addc_u32 s11, s13, s11
	s_mul_i32 s11, s11, s23
	s_mul_hi_u32 s12, s10, s23
	s_add_i32 s12, s12, s11
	s_mul_i32 s10, s10, s23
	s_add_u32 s0, s0, s10
	s_addc_u32 s1, s1, s12
	s_lshl_b32 s10, s21, 5
	s_and_b32 s10, s10, 0x1fe0
	s_add_u32 s0, s0, s10
	s_addc_u32 s1, s1, 0
	s_ashr_i32 s10, s3, 31
	s_mul_i32 s10, s8, s10
	s_mul_hi_u32 s11, s8, s3
	s_add_i32 s10, s11, s10
	s_mul_i32 s11, s9, s3
	s_add_i32 s11, s10, s11
	s_mul_i32 s10, s8, s3
	s_lshl_b64 s[10:11], s[10:11], 2
	s_add_u32 s4, s4, s10
	s_mul_i32 s51, s3, s23
	s_addc_u32 s5, s5, s11
	s_ashr_i32 s3, s2, 31
	s_lshl_b64 s[2:3], s[2:3], 2
	v_and_b32_e32 v38, 63, v2
	s_add_u32 s2, s4, s2
	v_mov_b32_e32 v39, 0
	s_addc_u32 s3, s5, s3
	v_lshlrev_b32_e32 v40, 2, v38
	v_mov_b32_e32 v41, v39
	v_lshl_add_u64 v[2:3], s[2:3], 0, v[40:41]
	s_lshl_b64 s[4:5], s[8:9], 2
	v_lshl_add_u64 v[2:3], v[2:3], 0, s[4:5]
	v_lshl_add_u64 v[4:5], v[2:3], 0, s[4:5]
	v_lshl_add_u64 v[6:7], v[4:5], 0, s[4:5]
	v_lshl_add_u64 v[8:9], v[6:7], 0, s[4:5]
	v_lshl_add_u64 v[10:11], v[8:9], 0, s[4:5]
	v_lshl_add_u64 v[12:13], v[10:11], 0, s[4:5]
	v_lshl_add_u64 v[14:15], v[12:13], 0, s[4:5]
	v_lshl_add_u64 v[16:17], v[14:15], 0, s[4:5]
	v_lshl_add_u64 v[18:19], v[16:17], 0, s[4:5]
	v_lshl_add_u64 v[20:21], v[18:19], 0, s[4:5]
	v_lshl_add_u64 v[22:23], v[20:21], 0, s[4:5]
	v_lshl_add_u64 v[24:25], v[22:23], 0, s[4:5]
	v_lshl_add_u64 v[26:27], v[24:25], 0, s[4:5]
	v_lshl_add_u64 v[28:29], v[26:27], 0, s[4:5]
	v_lshl_add_u64 v[30:31], v[28:29], 0, s[4:5]
	v_lshl_add_u64 v[32:33], v[30:31], 0, s[4:5]
	v_lshl_add_u64 v[34:35], v[32:33], 0, s[4:5]
	v_lshl_add_u64 v[36:37], v[34:35], 0, s[4:5]
	v_lshl_add_u64 v[42:43], v[36:37], 0, s[4:5]
	v_lshl_add_u64 v[44:45], v[42:43], 0, s[4:5]
	v_lshl_add_u64 v[46:47], v[44:45], 0, s[4:5]
	v_lshl_add_u64 v[48:49], v[46:47], 0, s[4:5]
	v_lshl_add_u64 v[50:51], v[48:49], 0, s[4:5]
	v_lshl_add_u64 v[52:53], v[50:51], 0, s[4:5]
	v_lshl_add_u64 v[54:55], v[52:53], 0, s[4:5]
	v_lshl_add_u64 v[56:57], v[54:55], 0, s[4:5]
	v_lshl_add_u64 v[58:59], v[56:57], 0, s[4:5]
	v_lshl_add_u64 v[60:61], v[58:59], 0, s[4:5]
	v_lshl_add_u64 v[62:63], v[60:61], 0, s[4:5]
	v_lshl_add_u64 v[64:65], v[62:63], 0, s[4:5]
	v_lshl_add_u64 v[66:67], v[64:65], 0, s[4:5]
	s_waitcnt vmcnt(0)
	global_load_dword v1, v[2:3], off nt
	s_nop 0
	global_load_dword v2, v[4:5], off nt
	global_load_dword v3, v[6:7], off nt
	s_nop 0
	global_load_dword v4, v[8:9], off nt
	global_load_dword v5, v[10:11], off nt
	global_load_dword v6, v[12:13], off nt
	global_load_dword v7, v[14:15], off nt
	s_nop 0
	global_load_dword v8, v[16:17], off nt
	global_load_dword v9, v[18:19], off nt
	global_load_dword v10, v[20:21], off nt
	global_load_dword v11, v[22:23], off nt
	global_load_dword v12, v[24:25], off nt
	global_load_dword v13, v[26:27], off nt
	global_load_dword v14, v[28:29], off nt
	global_load_dword v15, v[30:31], off nt
	global_load_dword v16, v[32:33], off nt
	global_load_dword v17, v[34:35], off nt
	global_load_dword v18, v[36:37], off nt
	global_load_dword v19, v[42:43], off nt
	global_load_dword v20, v[44:45], off nt
	global_load_dword v21, v[46:47], off nt
	global_load_dword v22, v[48:49], off nt
	global_load_dword v23, v[50:51], off nt
	global_load_dword v24, v[52:53], off nt
	global_load_dword v25, v[54:55], off nt
	global_load_dword v26, v[56:57], off nt
	global_load_dword v27, v[58:59], off nt
	global_load_dword v28, v[60:61], off nt
	global_load_dword v29, v[62:63], off nt
	global_load_dword v30, v[64:65], off nt
	global_load_dword v31, v[66:67], off nt
	global_load_dword v32, v40, s[2:3] nt
	s_add_i32 s23, s20, s22
	s_cmp_gt_i32 s23, 0xffff
	s_mov_b64 s[18:19], s[0:1]
	s_mov_b32 s71, s51
	s_mov_b32 s50, s48
	s_waitcnt lgkmcnt(0)
	v_mov_b32_e32 v79, v73
	s_mov_b32 s52, s49
	s_cbranch_scc1 .LBB0_862
	s_cmpk_gt_i32 s23, 0x17ff
	s_cbranch_scc0 .LBB0_822
	s_cmpk_gt_u32 s23, 0x1fff
	s_cbranch_scc0 .LBB0_825
	s_cmpk_gt_u32 s23, 0x35ff
	s_cbranch_scc0 .LBB0_826
	s_cmpk_gt_u32 s23, 0x4bff
	s_cbranch_scc0 .LBB0_827
	s_cmpk_gt_u32 s23, 0x61ff
	s_cbranch_scc0 .LBB0_828
	s_cmpk_gt_u32 s23, 0x79ff
	s_cbranch_scc0 .LBB0_829
	s_cmpk_gt_u32 s23, 0x81ff
	s_cbranch_scc0 .LBB0_830
	s_add_i32 s2, s23, 0x7e00
	s_bfe_u32 s3, s2, 0x6000a
	s_mulk_i32 s3, 0x2493
	s_lshr_b32 s10, s3, 16
	s_mul_i32 s3, s10, 0x1c00
	s_sub_i32 s2, s2, s3
	s_bfe_u32 s3, s2, 0xc0004
	s_mulk_i32 s3, 0x2493
	s_lshr_b32 s3, s3, 16
	s_mul_i32 s4, s3, 0x70
	s_sub_i32 s11, s2, s4
	s_lshl_b32 s14, s11, 6
	s_and_b32 s2, s14, 0xffc0
	s_mul_i32 s4, s10, 0x3800000
	s_add_u32 s4, s64, s4
	s_addc_u32 s5, s65, 0
	s_add_u32 s8, s96, 0x8a00000
	s_addc_u32 s9, s97, 0
	s_mul_i32 s12, s10, 0x1c00000
	s_lshl_b32 s10, s11, 7
	s_and_b32 s10, s10, 0x3f00
	s_and_b32 s11, s14, 64
	s_mov_b32 s13, 0
	s_or_b32 s24, s10, s11
	s_mov_b64 s[10:11], 0
	s_branch .LBB0_831

.LBB0_861:
	s_lshl_b32 s20, s3, 5
	s_ashr_i32 s3, s24, 8
	s_ashr_i32 s14, s3, 31
	s_mul_i32 s15, s3, s17
	s_mul_hi_u32 s17, s3, s16
	s_add_i32 s15, s17, s15
	s_mul_i32 s14, s14, s16
	s_add_i32 s15, s15, s14
	s_mul_i32 s14, s3, s16
	s_lshl_b64 s[14:15], s[14:15], 8
	s_add_u32 s3, s14, s12
	s_addc_u32 s12, s15, s13
	s_mul_i32 s12, s12, s26
	s_mul_hi_u32 s13, s3, s26
	s_add_i32 s13, s13, s12
	s_mul_i32 s3, s3, s26
	s_add_u32 s3, s8, s3
	s_addc_u32 s8, s9, s13
	s_lshl_b32 s9, s24, 5
	s_and_b32 s9, s9, 0x1fe0
	s_add_u32 s18, s3, s9
	s_addc_u32 s19, s8, 0
	s_ashr_i32 s3, s20, 31
	s_mul_i32 s3, s10, s3
	s_mul_hi_u32 s8, s10, s20
	s_add_i32 s3, s8, s3
	s_mul_i32 s8, s11, s20
	s_add_i32 s9, s3, s8
	s_mul_i32 s8, s10, s20
	s_lshl_b64 s[8:9], s[8:9], 2
	s_add_u32 s4, s4, s8
	s_addc_u32 s5, s5, s9
	s_ashr_i32 s3, s2, 31
	s_lshl_b64 s[2:3], s[2:3], 2
	s_add_u32 s2, s4, s2
	s_addc_u32 s3, s5, s3
	v_mov_b32_e32 v41, 0
	v_lshl_add_u64 v[34:35], s[2:3], 0, v[40:41]
	s_waitcnt vmcnt(0)
	global_load_dword v80, v40, s[2:3] nt
	s_lshl_b64 s[2:3], s[10:11], 2
	v_lshl_add_u64 v[34:35], v[34:35], 0, s[2:3]
	v_lshl_add_u64 v[36:37], v[34:35], 0, s[2:3]
	v_lshl_add_u64 v[42:43], v[36:37], 0, s[2:3]
	v_lshl_add_u64 v[44:45], v[42:43], 0, s[2:3]
	v_lshl_add_u64 v[46:47], v[44:45], 0, s[2:3]
	v_lshl_add_u64 v[48:49], v[46:47], 0, s[2:3]
	v_lshl_add_u64 v[50:51], v[48:49], 0, s[2:3]
	global_load_dword v81, v[34:35], off nt
	global_load_dword v82, v[36:37], off nt
	global_load_dword v83, v[42:43], off nt
	global_load_dword v84, v[44:45], off nt
	global_load_dword v85, v[46:47], off nt
	global_load_dword v86, v[48:49], off nt
	global_load_dword v87, v[50:51], off nt
	v_lshl_add_u64 v[34:35], v[50:51], 0, s[2:3]
	global_load_dword v88, v[34:35], off nt
	v_lshl_add_u64 v[34:35], v[34:35], 0, s[2:3]
	global_load_dword v89, v[34:35], off nt
	v_lshl_add_u64 v[34:35], v[34:35], 0, s[2:3]
	global_load_dword v90, v[34:35], off nt
	v_lshl_add_u64 v[34:35], v[34:35], 0, s[2:3]
	global_load_dword v91, v[34:35], off nt
	v_lshl_add_u64 v[34:35], v[34:35], 0, s[2:3]
	global_load_dword v92, v[34:35], off nt
	v_lshl_add_u64 v[34:35], v[34:35], 0, s[2:3]
	global_load_dword v93, v[34:35], off nt
	v_lshl_add_u64 v[34:35], v[34:35], 0, s[2:3]
	global_load_dword v94, v[34:35], off nt
	v_lshl_add_u64 v[34:35], v[34:35], 0, s[2:3]
	global_load_dword v95, v[34:35], off nt
	v_lshl_add_u64 v[34:35], v[34:35], 0, s[2:3]
	global_load_dword v96, v[34:35], off nt
	v_lshl_add_u64 v[34:35], v[34:35], 0, s[2:3]
	global_load_dword v97, v[34:35], off nt
	v_lshl_add_u64 v[34:35], v[34:35], 0, s[2:3]
	global_load_dword v98, v[34:35], off nt
	v_lshl_add_u64 v[34:35], v[34:35], 0, s[2:3]
	global_load_dword v99, v[34:35], off nt
	v_lshl_add_u64 v[34:35], v[34:35], 0, s[2:3]
	global_load_dword v100, v[34:35], off nt
	v_lshl_add_u64 v[34:35], v[34:35], 0, s[2:3]
	global_load_dword v101, v[34:35], off nt
	v_lshl_add_u64 v[34:35], v[34:35], 0, s[2:3]
	global_load_dword v102, v[34:35], off nt
	v_lshl_add_u64 v[34:35], v[34:35], 0, s[2:3]
	global_load_dword v103, v[34:35], off nt
	v_lshl_add_u64 v[34:35], v[34:35], 0, s[2:3]
	global_load_dword v104, v[34:35], off nt
	v_lshl_add_u64 v[34:35], v[34:35], 0, s[2:3]
	global_load_dword v105, v[34:35], off nt
	v_lshl_add_u64 v[34:35], v[34:35], 0, s[2:3]
	global_load_dword v106, v[34:35], off nt
	v_lshl_add_u64 v[34:35], v[34:35], 0, s[2:3]
	global_load_dword v107, v[34:35], off nt
	v_lshl_add_u64 v[34:35], v[34:35], 0, s[2:3]
	global_load_dword v108, v[34:35], off nt
	v_lshl_add_u64 v[34:35], v[34:35], 0, s[2:3]
	global_load_dword v109, v[34:35], off nt
	v_lshl_add_u64 v[34:35], v[34:35], 0, s[2:3]
	global_load_dword v110, v[34:35], off nt
	v_lshl_add_u64 v[34:35], v[34:35], 0, s[2:3]
	global_load_dword v111, v[34:35], off nt
	s_mul_i32 s71, s20, s26

.LBB0_903:
	s_lshl_b32 s16, s25, 5
	s_ashr_i32 s25, s72, 8
	s_ashr_i32 s30, s25, 31
	s_mul_i32 s31, s25, s37
	s_mul_hi_u32 s37, s25, s36
	s_add_i32 s31, s37, s31
	s_mul_i32 s30, s30, s36
	s_add_i32 s31, s31, s30
	s_mul_i32 s30, s25, s36
	s_lshl_b64 s[30:31], s[30:31], 8
	s_add_u32 s20, s30, s20
	s_addc_u32 s21, s31, s21
	s_mul_i32 s21, s21, s75
	s_mul_hi_u32 s25, s20, s75
	s_add_i32 s25, s25, s21
	s_mul_i32 s20, s20, s75
	s_add_u32 s20, s34, s20
	s_addc_u32 s21, s35, s25
	s_lshl_b32 s25, s72, 5
	s_and_b32 s25, s25, 0x1fe0
	s_add_u32 s20, s20, s25
	s_addc_u32 s21, s21, 0
	s_ashr_i32 s25, s16, 31
	s_mul_i32 s25, s28, s25
	s_mul_hi_u32 s30, s28, s16
	s_add_i32 s25, s30, s25
	s_mul_i32 s30, s29, s16
	s_add_i32 s31, s25, s30
	s_mul_i32 s30, s28, s16
	s_lshl_b64 s[30:31], s[30:31], 2
	s_add_u32 s26, s26, s30
	s_addc_u32 s27, s27, s31
	s_ashr_i32 s25, s24, 31
	s_lshl_b64 s[24:25], s[24:25], 2
	s_add_u32 s24, s26, s24
	s_addc_u32 s25, s27, s25
	v_lshl_add_u64 v[34:35], s[24:25], 0, v[40:41]
	s_waitcnt vmcnt(0)
	global_load_dword v42, v40, s[24:25] nt
	s_lshl_b64 s[24:25], s[28:29], 2
	v_lshl_add_u64 v[34:35], v[34:35], 0, s[24:25]
	v_lshl_add_u64 v[36:37], v[34:35], 0, s[24:25]
	s_waitcnt vmcnt(26)
	v_lshl_add_u64 v[46:47], v[36:37], 0, s[24:25]
	s_waitcnt vmcnt(23)
	v_lshl_add_u64 v[48:49], v[46:47], 0, s[24:25]
	s_waitcnt vmcnt(22)
	v_lshl_add_u64 v[50:51], v[48:49], 0, s[24:25]
	s_waitcnt vmcnt(19)
	v_lshl_add_u64 v[52:53], v[50:51], 0, s[24:25]
	s_waitcnt vmcnt(18)
	v_lshl_add_u64 v[54:55], v[52:53], 0, s[24:25]
	global_load_dword v44, v[34:35], off nt
	global_load_dword v33, v[36:37], off nt
	global_load_dword v43, v[46:47], off nt
	s_nop 0
	global_load_dword v46, v[48:49], off nt
	s_nop 0
	global_load_dword v48, v[50:51], off nt
	global_load_dword v45, v[52:53], off nt
	global_load_dword v47, v[54:55], off nt
	v_lshl_add_u64 v[34:35], v[54:55], 0, s[24:25]
	global_load_dword v50, v[34:35], off nt
	v_lshl_add_u64 v[34:35], v[34:35], 0, s[24:25]
	global_load_dword v52, v[34:35], off nt
	v_lshl_add_u64 v[34:35], v[34:35], 0, s[24:25]
	global_load_dword v49, v[34:35], off nt
	v_lshl_add_u64 v[34:35], v[34:35], 0, s[24:25]
	global_load_dword v51, v[34:35], off nt
	v_lshl_add_u64 v[34:35], v[34:35], 0, s[24:25]
	global_load_dword v54, v[34:35], off nt
	v_lshl_add_u64 v[34:35], v[34:35], 0, s[24:25]
	global_load_dword v56, v[34:35], off nt
	v_lshl_add_u64 v[34:35], v[34:35], 0, s[24:25]
	global_load_dword v53, v[34:35], off nt
	v_lshl_add_u64 v[34:35], v[34:35], 0, s[24:25]
	global_load_dword v55, v[34:35], off nt
	v_lshl_add_u64 v[34:35], v[34:35], 0, s[24:25]
	global_load_dword v58, v[34:35], off nt
	v_lshl_add_u64 v[34:35], v[34:35], 0, s[24:25]
	global_load_dword v60, v[34:35], off nt
	v_lshl_add_u64 v[34:35], v[34:35], 0, s[24:25]
	global_load_dword v57, v[34:35], off nt
	v_lshl_add_u64 v[34:35], v[34:35], 0, s[24:25]
	global_load_dword v59, v[34:35], off nt
	v_lshl_add_u64 v[34:35], v[34:35], 0, s[24:25]
	global_load_dword v62, v[34:35], off nt
	v_lshl_add_u64 v[34:35], v[34:35], 0, s[24:25]
	global_load_dword v64, v[34:35], off nt
	v_lshl_add_u64 v[34:35], v[34:35], 0, s[24:25]
	global_load_dword v61, v[34:35], off nt
	v_lshl_add_u64 v[34:35], v[34:35], 0, s[24:25]
	global_load_dword v63, v[34:35], off nt
	v_lshl_add_u64 v[34:35], v[34:35], 0, s[24:25]
	global_load_dword v66, v[34:35], off nt
	v_lshl_add_u64 v[34:35], v[34:35], 0, s[24:25]
	global_load_dword v68, v[34:35], off nt
	v_lshl_add_u64 v[34:35], v[34:35], 0, s[24:25]
	global_load_dword v65, v[34:35], off nt
	v_lshl_add_u64 v[34:35], v[34:35], 0, s[24:25]
	global_load_dword v67, v[34:35], off nt
	v_lshl_add_u64 v[34:35], v[34:35], 0, s[24:25]
	global_load_dword v70, v[34:35], off nt
	v_lshl_add_u64 v[34:35], v[34:35], 0, s[24:25]
	global_load_dword v72, v[34:35], off nt
	v_lshl_add_u64 v[34:35], v[34:35], 0, s[24:25]
	global_load_dword v69, v[34:35], off nt
	v_lshl_add_u64 v[34:35], v[34:35], 0, s[24:25]
	global_load_dword v71, v[34:35], off nt
	s_mul_i32 s72, s16, s75

.LBB0_961:
	s_lshl_b32 s16, s25, 5
	s_ashr_i32 s25, s74, 8
	s_ashr_i32 s30, s25, 31
	s_mul_i32 s31, s25, s37
	s_mul_hi_u32 s37, s25, s36
	s_add_i32 s31, s37, s31
	s_mul_i32 s30, s30, s36
	s_add_i32 s31, s31, s30
	s_mul_i32 s30, s25, s36
	s_lshl_b64 s[30:31], s[30:31], 8
	s_add_u32 s0, s30, s0
	s_addc_u32 s1, s31, s1
	s_mul_i32 s1, s1, s76
	s_mul_hi_u32 s25, s0, s76
	s_add_i32 s25, s25, s1
	s_mul_i32 s0, s0, s76
	s_add_u32 s0, s34, s0
	s_addc_u32 s1, s35, s25
	s_lshl_b32 s25, s74, 5
	s_and_b32 s25, s25, 0x1fe0
	s_add_u32 s0, s0, s25
	s_addc_u32 s1, s1, 0
	s_ashr_i32 s25, s16, 31
	s_mul_i32 s25, s28, s25
	s_mul_hi_u32 s30, s28, s16
	s_add_i32 s25, s30, s25
	s_mul_i32 s30, s29, s16
	s_add_i32 s31, s25, s30
	s_mul_i32 s30, s28, s16
	s_lshl_b64 s[30:31], s[30:31], 2
	s_mul_i32 s51, s16, s76
	s_add_u32 s16, s26, s30
	s_addc_u32 s26, s27, s31
	s_ashr_i32 s25, s24, 31
	s_lshl_b64 s[24:25], s[24:25], 2
	s_add_u32 s24, s16, s24
	s_addc_u32 s25, s26, s25
	s_waitcnt vmcnt(30)
	v_lshl_add_u64 v[2:3], s[24:25], 0, v[40:41]
	s_lshl_b64 s[26:27], s[28:29], 2
	v_lshl_add_u64 v[2:3], v[2:3], 0, s[26:27]
	s_waitcnt vmcnt(28)
	v_lshl_add_u64 v[4:5], v[2:3], 0, s[26:27]
	s_waitcnt vmcnt(26)
	v_lshl_add_u64 v[6:7], v[4:5], 0, s[26:27]
	s_waitcnt vmcnt(24)
	v_lshl_add_u64 v[8:9], v[6:7], 0, s[26:27]
	s_waitcnt vmcnt(22)
	v_lshl_add_u64 v[10:11], v[8:9], 0, s[26:27]
	s_waitcnt vmcnt(20)
	v_lshl_add_u64 v[12:13], v[10:11], 0, s[26:27]
	s_waitcnt vmcnt(18)
	v_lshl_add_u64 v[14:15], v[12:13], 0, s[26:27]
	s_waitcnt vmcnt(16)
	v_lshl_add_u64 v[16:17], v[14:15], 0, s[26:27]
	s_waitcnt vmcnt(14)
	v_lshl_add_u64 v[18:19], v[16:17], 0, s[26:27]
	s_waitcnt vmcnt(12)
	v_lshl_add_u64 v[20:21], v[18:19], 0, s[26:27]
	s_waitcnt vmcnt(10)
	v_lshl_add_u64 v[22:23], v[20:21], 0, s[26:27]
	s_waitcnt vmcnt(8)
	v_lshl_add_u64 v[24:25], v[22:23], 0, s[26:27]
	s_waitcnt vmcnt(6)
	v_lshl_add_u64 v[26:27], v[24:25], 0, s[26:27]
	s_waitcnt vmcnt(4)
	v_lshl_add_u64 v[28:29], v[26:27], 0, s[26:27]
	s_waitcnt vmcnt(2)
	v_lshl_add_u64 v[30:31], v[28:29], 0, s[26:27]
	v_lshl_add_u64 v[34:35], v[30:31], 0, s[26:27]
	v_lshl_add_u64 v[36:37], v[34:35], 0, s[26:27]
	v_lshl_add_u64 v[74:75], v[36:37], 0, s[26:27]
	v_lshl_add_u64 v[114:115], v[74:75], 0, s[26:27]
	v_lshl_add_u64 v[116:117], v[114:115], 0, s[26:27]
	v_lshl_add_u64 v[118:119], v[116:117], 0, s[26:27]
	v_lshl_add_u64 v[120:121], v[118:119], 0, s[26:27]
	v_lshl_add_u64 v[122:123], v[120:121], 0, s[26:27]
	v_lshl_add_u64 v[124:125], v[122:123], 0, s[26:27]
	v_lshl_add_u64 v[126:127], v[124:125], 0, s[26:27]
	v_lshl_add_u64 v[128:129], v[126:127], 0, s[26:27]
	v_lshl_add_u64 v[130:131], v[128:129], 0, s[26:27]
	v_lshl_add_u64 v[132:133], v[130:131], 0, s[26:27]
	v_lshl_add_u64 v[134:135], v[132:133], 0, s[26:27]
	v_lshl_add_u64 v[136:137], v[134:135], 0, s[26:27]
	v_lshl_add_u64 v[138:139], v[136:137], 0, s[26:27]
	s_waitcnt vmcnt(0)
	global_load_dword v1, v[2:3], off nt
	s_nop 0
	global_load_dword v2, v[4:5], off nt
	global_load_dword v3, v[6:7], off nt
	s_nop 0
	global_load_dword v4, v[8:9], off nt
	global_load_dword v5, v[10:11], off nt
	global_load_dword v6, v[12:13], off nt
	global_load_dword v7, v[14:15], off nt
	s_nop 0
	global_load_dword v8, v[16:17], off nt
	global_load_dword v9, v[18:19], off nt
	global_load_dword v10, v[20:21], off nt
	global_load_dword v11, v[22:23], off nt
	global_load_dword v12, v[24:25], off nt
	global_load_dword v13, v[26:27], off nt
	global_load_dword v14, v[28:29], off nt
	global_load_dword v15, v[30:31], off nt
	global_load_dword v16, v[34:35], off nt
	global_load_dword v17, v[36:37], off nt
	global_load_dword v18, v[74:75], off nt
	global_load_dword v19, v[114:115], off nt
	global_load_dword v20, v[116:117], off nt
	global_load_dword v21, v[118:119], off nt
	global_load_dword v22, v[120:121], off nt
	global_load_dword v23, v[122:123], off nt
	global_load_dword v24, v[124:125], off nt
	global_load_dword v25, v[126:127], off nt
	global_load_dword v26, v[128:129], off nt
	global_load_dword v27, v[130:131], off nt
	global_load_dword v28, v[132:133], off nt
	global_load_dword v29, v[134:135], off nt
	global_load_dword v30, v[136:137], off nt
	global_load_dword v31, v[138:139], off nt
	global_load_dword v32, v40, s[24:25] nt

.LBB0_1018:
	s_ashr_i32 s23, s71, 8
	s_ashr_i32 s28, s23, 31
	s_mul_i32 s29, s23, s35
	s_mul_hi_u32 s35, s23, s34
	s_add_i32 s29, s35, s29
	s_mul_i32 s28, s28, s34
	s_add_i32 s29, s29, s28
	s_mul_i32 s28, s23, s34
	s_lshl_b32 s16, s40, 5
	s_lshl_b64 s[28:29], s[28:29], 8
	s_add_u32 s18, s28, s18
	s_addc_u32 s19, s29, s19
	s_mul_i32 s19, s19, s73
	s_mul_hi_u32 s23, s18, s73
	s_add_i32 s23, s23, s19
	s_mul_i32 s18, s18, s73
	s_add_u32 s18, s30, s18
	s_addc_u32 s19, s31, s23
	s_lshl_b32 s23, s71, 5
	s_and_b32 s23, s23, 0x1fe0
	s_add_u32 s18, s18, s23
	s_addc_u32 s19, s19, 0
	s_ashr_i32 s23, s16, 31
	s_mul_i32 s23, s26, s23
	s_mul_hi_u32 s28, s26, s16
	s_add_i32 s23, s28, s23
	s_mul_i32 s28, s27, s16
	s_add_i32 s29, s23, s28
	s_mul_i32 s28, s26, s16
	s_lshl_b64 s[28:29], s[28:29], 2
	s_add_u32 s24, s24, s28
	s_addc_u32 s25, s25, s29
	s_ashr_i32 s23, s22, 31
	s_lshl_b64 s[22:23], s[22:23], 2
	s_add_u32 s22, s24, s22
	s_addc_u32 s23, s25, s23
	v_lshl_add_u64 v[34:35], s[22:23], 0, v[40:41]
	s_waitcnt vmcnt(0)
	global_load_dword v80, v40, s[22:23] nt
	s_lshl_b64 s[22:23], s[26:27], 2
	v_lshl_add_u64 v[34:35], v[34:35], 0, s[22:23]
	v_lshl_add_u64 v[36:37], v[34:35], 0, s[22:23]
	v_lshl_add_u64 v[74:75], v[36:37], 0, s[22:23]
	s_waitcnt vmcnt(29)
	v_lshl_add_u64 v[84:85], v[74:75], 0, s[22:23]
	s_waitcnt vmcnt(27)
	v_lshl_add_u64 v[86:87], v[84:85], 0, s[22:23]
	s_waitcnt vmcnt(25)
	v_lshl_add_u64 v[88:89], v[86:87], 0, s[22:23]
	s_waitcnt vmcnt(23)
	v_lshl_add_u64 v[90:91], v[88:89], 0, s[22:23]
	global_load_dword v81, v[34:35], off nt
	global_load_dword v82, v[36:37], off nt
	global_load_dword v83, v[74:75], off nt
	s_nop 0
	global_load_dword v84, v[84:85], off nt
	s_nop 0
	global_load_dword v85, v[86:87], off nt
	s_nop 0
	global_load_dword v86, v[88:89], off nt
	global_load_dword v87, v[90:91], off nt
	v_lshl_add_u64 v[34:35], v[90:91], 0, s[22:23]
	global_load_dword v88, v[34:35], off nt
	v_lshl_add_u64 v[34:35], v[34:35], 0, s[22:23]
	global_load_dword v89, v[34:35], off nt
	v_lshl_add_u64 v[34:35], v[34:35], 0, s[22:23]
	global_load_dword v90, v[34:35], off nt
	v_lshl_add_u64 v[34:35], v[34:35], 0, s[22:23]
	global_load_dword v91, v[34:35], off nt
	v_lshl_add_u64 v[34:35], v[34:35], 0, s[22:23]
	global_load_dword v92, v[34:35], off nt
	v_lshl_add_u64 v[34:35], v[34:35], 0, s[22:23]
	global_load_dword v93, v[34:35], off nt
	v_lshl_add_u64 v[34:35], v[34:35], 0, s[22:23]
	global_load_dword v94, v[34:35], off nt
	v_lshl_add_u64 v[34:35], v[34:35], 0, s[22:23]
	global_load_dword v95, v[34:35], off nt
	v_lshl_add_u64 v[34:35], v[34:35], 0, s[22:23]
	global_load_dword v96, v[34:35], off nt
	v_lshl_add_u64 v[34:35], v[34:35], 0, s[22:23]
	global_load_dword v97, v[34:35], off nt
	v_lshl_add_u64 v[34:35], v[34:35], 0, s[22:23]
	global_load_dword v98, v[34:35], off nt
	v_lshl_add_u64 v[34:35], v[34:35], 0, s[22:23]
	global_load_dword v99, v[34:35], off nt
	v_lshl_add_u64 v[34:35], v[34:35], 0, s[22:23]
	global_load_dword v100, v[34:35], off nt
	v_lshl_add_u64 v[34:35], v[34:35], 0, s[22:23]
	global_load_dword v101, v[34:35], off nt
	v_lshl_add_u64 v[34:35], v[34:35], 0, s[22:23]
	global_load_dword v102, v[34:35], off nt
	v_lshl_add_u64 v[34:35], v[34:35], 0, s[22:23]
	global_load_dword v103, v[34:35], off nt
	v_lshl_add_u64 v[34:35], v[34:35], 0, s[22:23]
	global_load_dword v104, v[34:35], off nt
	v_lshl_add_u64 v[34:35], v[34:35], 0, s[22:23]
	global_load_dword v105, v[34:35], off nt
	v_lshl_add_u64 v[34:35], v[34:35], 0, s[22:23]
	global_load_dword v106, v[34:35], off nt
	v_lshl_add_u64 v[34:35], v[34:35], 0, s[22:23]
	global_load_dword v107, v[34:35], off nt
	v_lshl_add_u64 v[34:35], v[34:35], 0, s[22:23]
	global_load_dword v108, v[34:35], off nt
	v_lshl_add_u64 v[34:35], v[34:35], 0, s[22:23]
	global_load_dword v109, v[34:35], off nt
	v_lshl_add_u64 v[34:35], v[34:35], 0, s[22:23]
	global_load_dword v110, v[34:35], off nt
	v_lshl_add_u64 v[34:35], v[34:35], 0, s[22:23]
	global_load_dword v111, v[34:35], off nt
	s_mul_i32 s71, s16, s73

.LBB0_1257:
	s_ashr_i32 s12, s21, 8
	s_ashr_i32 s13, s12, 31
	s_mul_i32 s15, s12, s15
	s_mul_hi_u32 s16, s12, s14
	s_add_i32 s15, s16, s15
	s_mul_i32 s13, s13, s14
	s_add_i32 s13, s15, s13
	s_mul_i32 s12, s12, s14
	s_lshl_b32 s22, s94, 3
	s_lshl_b32 s3, s3, 5
	s_lshl_b64 s[12:13], s[12:13], 8
	s_add_u32 s8, s12, s8
	s_addc_u32 s9, s13, s9
	s_mul_i32 s9, s9, s23
	s_mul_hi_u32 s12, s8, s23
	s_add_i32 s12, s12, s9
	s_mul_i32 s8, s8, s23
	s_add_u32 s0, s0, s8
	s_addc_u32 s1, s1, s12
	s_lshl_b32 s8, s21, 5
	s_and_b32 s8, s8, 0x1fe0
	s_add_u32 s0, s0, s8
	s_addc_u32 s1, s1, 0
	s_ashr_i32 s8, s3, 31
	s_mul_i32 s8, s10, s8
	s_mul_hi_u32 s9, s10, s3
	s_add_i32 s8, s9, s8
	s_mul_i32 s9, s11, s3
	s_add_i32 s9, s8, s9
	s_mul_i32 s8, s10, s3
	s_lshl_b64 s[8:9], s[8:9], 2
	s_add_u32 s4, s4, s8
	s_mul_i32 s50, s3, s23
	s_addc_u32 s5, s5, s9
	s_ashr_i32 s3, s2, 31
	s_lshl_b64 s[2:3], s[2:3], 2
	v_and_b32_e32 v38, 63, v2
	s_add_u32 s2, s4, s2
	v_mov_b32_e32 v39, 0
	s_addc_u32 s3, s5, s3
	v_lshlrev_b32_e32 v40, 2, v38
	v_mov_b32_e32 v41, v39
	v_lshl_add_u64 v[2:3], s[2:3], 0, v[40:41]
	s_lshl_b64 s[4:5], s[10:11], 2
	v_lshl_add_u64 v[2:3], v[2:3], 0, s[4:5]
	v_lshl_add_u64 v[4:5], v[2:3], 0, s[4:5]
	v_lshl_add_u64 v[6:7], v[4:5], 0, s[4:5]
	v_lshl_add_u64 v[8:9], v[6:7], 0, s[4:5]
	v_lshl_add_u64 v[10:11], v[8:9], 0, s[4:5]
	v_lshl_add_u64 v[12:13], v[10:11], 0, s[4:5]
	v_lshl_add_u64 v[14:15], v[12:13], 0, s[4:5]
	v_lshl_add_u64 v[16:17], v[14:15], 0, s[4:5]
	v_lshl_add_u64 v[18:19], v[16:17], 0, s[4:5]
	v_lshl_add_u64 v[20:21], v[18:19], 0, s[4:5]
	v_lshl_add_u64 v[22:23], v[20:21], 0, s[4:5]
	v_lshl_add_u64 v[24:25], v[22:23], 0, s[4:5]
	v_lshl_add_u64 v[26:27], v[24:25], 0, s[4:5]
	v_lshl_add_u64 v[28:29], v[26:27], 0, s[4:5]
	v_lshl_add_u64 v[30:31], v[28:29], 0, s[4:5]
	v_lshl_add_u64 v[32:33], v[30:31], 0, s[4:5]
	v_lshl_add_u64 v[34:35], v[32:33], 0, s[4:5]
	v_lshl_add_u64 v[36:37], v[34:35], 0, s[4:5]
	v_lshl_add_u64 v[42:43], v[36:37], 0, s[4:5]
	v_lshl_add_u64 v[44:45], v[42:43], 0, s[4:5]
	v_lshl_add_u64 v[46:47], v[44:45], 0, s[4:5]
	v_lshl_add_u64 v[48:49], v[46:47], 0, s[4:5]
	v_lshl_add_u64 v[50:51], v[48:49], 0, s[4:5]
	v_lshl_add_u64 v[52:53], v[50:51], 0, s[4:5]
	v_lshl_add_u64 v[54:55], v[52:53], 0, s[4:5]
	v_lshl_add_u64 v[56:57], v[54:55], 0, s[4:5]
	v_lshl_add_u64 v[58:59], v[56:57], 0, s[4:5]
	v_lshl_add_u64 v[60:61], v[58:59], 0, s[4:5]
	v_lshl_add_u64 v[62:63], v[60:61], 0, s[4:5]
	v_lshl_add_u64 v[64:65], v[62:63], 0, s[4:5]
	v_lshl_add_u64 v[66:67], v[64:65], 0, s[4:5]
	s_waitcnt vmcnt(0)
	global_load_dword v1, v[2:3], off nt
	s_nop 0
	global_load_dword v2, v[4:5], off nt
	global_load_dword v3, v[6:7], off nt
	s_nop 0
	global_load_dword v4, v[8:9], off nt
	global_load_dword v5, v[10:11], off nt
	global_load_dword v6, v[12:13], off nt
	global_load_dword v7, v[14:15], off nt
	s_nop 0
	global_load_dword v8, v[16:17], off nt
	global_load_dword v9, v[18:19], off nt
	global_load_dword v10, v[20:21], off nt
	global_load_dword v11, v[22:23], off nt
	global_load_dword v12, v[24:25], off nt
	global_load_dword v13, v[26:27], off nt
	global_load_dword v14, v[28:29], off nt
	global_load_dword v15, v[30:31], off nt
	global_load_dword v16, v[32:33], off nt
	global_load_dword v17, v[34:35], off nt
	global_load_dword v18, v[36:37], off nt
	global_load_dword v19, v[42:43], off nt
	global_load_dword v20, v[44:45], off nt
	global_load_dword v21, v[46:47], off nt
	global_load_dword v22, v[48:49], off nt
	global_load_dword v23, v[50:51], off nt
	global_load_dword v24, v[52:53], off nt
	global_load_dword v25, v[54:55], off nt
	global_load_dword v26, v[56:57], off nt
	global_load_dword v27, v[58:59], off nt
	global_load_dword v28, v[60:61], off nt
	global_load_dword v29, v[62:63], off nt
	global_load_dword v30, v[64:65], off nt
	global_load_dword v31, v[66:67], off nt
	global_load_dword v32, v40, s[2:3] nt
	s_add_i32 s23, s20, s22
	s_cmp_gt_i32 s23, 0x1c7ff
	s_mov_b64 s[18:19], s[0:1]
	s_mov_b32 s70, s50
	s_mov_b32 s49, s47
	s_waitcnt lgkmcnt(0)
	v_mov_b32_e32 v79, v73
	s_mov_b32 s51, s48
	s_cbranch_scc1 .LBB0_1311
	s_cmpk_gt_i32 s23, 0x17ff
	s_cbranch_scc0 .LBB0_1267
	s_cmpk_gt_u32 s23, 0x1fff
	s_cbranch_scc0 .LBB0_1270
	s_cmpk_gt_u32 s23, 0x35ff
	s_cbranch_scc0 .LBB0_1271
	s_cmpk_gt_u32 s23, 0x4bff
	s_cbranch_scc0 .LBB0_1272
	s_cmpk_gt_u32 s23, 0x61ff
	s_cbranch_scc0 .LBB0_1273
	s_cmpk_gt_u32 s23, 0x79ff
	s_cbranch_scc0 .LBB0_1274
	s_cmpk_gt_u32 s23, 0x81ff
	s_cbranch_scc0 .LBB0_1275
	s_add_u32 s8, s96, 0x8a00000
	s_addc_u32 s9, s97, 0
	s_cmp_gt_u32 s23, 0x161ff
	s_cbranch_scc0 .LBB0_1276
	s_add_i32 s2, s23, 0x9e00
	s_bfe_u32 s3, s2, 0x6000a
	s_mulk_i32 s3, 0x2493
	s_lshr_b32 s10, s3, 16
	s_mul_i32 s3, s10, 0x1c00
	s_sub_i32 s2, s2, s3
	s_bfe_u32 s3, s2, 0xc0004
	s_mulk_i32 s3, 0x2493
	s_lshr_b32 s3, s3, 16
	s_mul_i32 s4, s3, 0x70
	s_sub_i32 s2, s2, s4
	s_lshl_b32 s12, s2, 6
	s_and_b32 s2, s12, 0xffc0
	s_mul_i32 s4, s10, 0x3800000
	s_add_u32 s4, s66, s4
	s_addc_u32 s5, s67, 0
	s_lshl_b32 s13, s2, 1
	s_and_b32 s12, s12, 64
	s_or_b32 s12, s13, s12
	s_mov_b32 s11, 0
	s_mul_i32 s10, s10, 0x1c00000
	s_or_b32 s24, s12, 0x80
	s_mov_b64 s[12:13], 0
	s_branch .LBB0_1277

.LBB0_1310:
	s_lshl_b32 s20, s3, 5
	s_ashr_i32 s3, s24, 8
	s_ashr_i32 s14, s3, 31
	s_mul_i32 s15, s3, s17
	s_mul_hi_u32 s17, s3, s16
	s_add_i32 s15, s17, s15
	s_mul_i32 s14, s14, s16
	s_add_i32 s15, s15, s14
	s_mul_i32 s14, s3, s16
	s_lshl_b64 s[14:15], s[14:15], 8
	s_add_u32 s3, s14, s10
	s_addc_u32 s10, s15, s11
	s_mul_i32 s10, s10, s26
	s_mul_hi_u32 s11, s3, s26
	s_add_i32 s11, s11, s10
	s_mul_i32 s3, s3, s26
	s_add_u32 s3, s8, s3
	s_addc_u32 s8, s9, s11
	s_lshl_b32 s9, s24, 5
	s_and_b32 s9, s9, 0x1fe0
	s_add_u32 s18, s3, s9
	s_addc_u32 s19, s8, 0
	s_ashr_i32 s3, s20, 31
	s_mul_i32 s3, s12, s3
	s_mul_hi_u32 s8, s12, s20
	s_add_i32 s3, s8, s3
	s_mul_i32 s8, s13, s20
	s_add_i32 s9, s3, s8
	s_mul_i32 s8, s12, s20
	s_lshl_b64 s[8:9], s[8:9], 2
	s_add_u32 s4, s4, s8
	s_addc_u32 s5, s5, s9
	s_ashr_i32 s3, s2, 31
	s_lshl_b64 s[2:3], s[2:3], 2
	s_add_u32 s2, s4, s2
	s_addc_u32 s3, s5, s3
	v_mov_b32_e32 v41, 0
	v_lshl_add_u64 v[34:35], s[2:3], 0, v[40:41]
	s_waitcnt vmcnt(0)
	global_load_dword v80, v40, s[2:3] nt
	s_lshl_b64 s[2:3], s[12:13], 2
	v_lshl_add_u64 v[34:35], v[34:35], 0, s[2:3]
	v_lshl_add_u64 v[36:37], v[34:35], 0, s[2:3]
	v_lshl_add_u64 v[42:43], v[36:37], 0, s[2:3]
	v_lshl_add_u64 v[44:45], v[42:43], 0, s[2:3]
	v_lshl_add_u64 v[46:47], v[44:45], 0, s[2:3]
	v_lshl_add_u64 v[48:49], v[46:47], 0, s[2:3]
	v_lshl_add_u64 v[50:51], v[48:49], 0, s[2:3]
	global_load_dword v81, v[34:35], off nt
	global_load_dword v82, v[36:37], off nt
	global_load_dword v83, v[42:43], off nt
	global_load_dword v84, v[44:45], off nt
	global_load_dword v85, v[46:47], off nt
	global_load_dword v86, v[48:49], off nt
	global_load_dword v87, v[50:51], off nt
	v_lshl_add_u64 v[34:35], v[50:51], 0, s[2:3]
	global_load_dword v88, v[34:35], off nt
	v_lshl_add_u64 v[34:35], v[34:35], 0, s[2:3]
	global_load_dword v89, v[34:35], off nt
	v_lshl_add_u64 v[34:35], v[34:35], 0, s[2:3]
	global_load_dword v90, v[34:35], off nt
	v_lshl_add_u64 v[34:35], v[34:35], 0, s[2:3]
	global_load_dword v91, v[34:35], off nt
	v_lshl_add_u64 v[34:35], v[34:35], 0, s[2:3]
	global_load_dword v92, v[34:35], off nt
	v_lshl_add_u64 v[34:35], v[34:35], 0, s[2:3]
	global_load_dword v93, v[34:35], off nt
	v_lshl_add_u64 v[34:35], v[34:35], 0, s[2:3]
	global_load_dword v94, v[34:35], off nt
	v_lshl_add_u64 v[34:35], v[34:35], 0, s[2:3]
	global_load_dword v95, v[34:35], off nt
	v_lshl_add_u64 v[34:35], v[34:35], 0, s[2:3]
	global_load_dword v96, v[34:35], off nt
	v_lshl_add_u64 v[34:35], v[34:35], 0, s[2:3]
	global_load_dword v97, v[34:35], off nt
	v_lshl_add_u64 v[34:35], v[34:35], 0, s[2:3]
	global_load_dword v98, v[34:35], off nt
	v_lshl_add_u64 v[34:35], v[34:35], 0, s[2:3]
	global_load_dword v99, v[34:35], off nt
	v_lshl_add_u64 v[34:35], v[34:35], 0, s[2:3]
	global_load_dword v100, v[34:35], off nt
	v_lshl_add_u64 v[34:35], v[34:35], 0, s[2:3]
	global_load_dword v101, v[34:35], off nt
	v_lshl_add_u64 v[34:35], v[34:35], 0, s[2:3]
	global_load_dword v102, v[34:35], off nt
	v_lshl_add_u64 v[34:35], v[34:35], 0, s[2:3]
	global_load_dword v103, v[34:35], off nt
	v_lshl_add_u64 v[34:35], v[34:35], 0, s[2:3]
	global_load_dword v104, v[34:35], off nt
	v_lshl_add_u64 v[34:35], v[34:35], 0, s[2:3]
	global_load_dword v105, v[34:35], off nt
	v_lshl_add_u64 v[34:35], v[34:35], 0, s[2:3]
	global_load_dword v106, v[34:35], off nt
	v_lshl_add_u64 v[34:35], v[34:35], 0, s[2:3]
	global_load_dword v107, v[34:35], off nt
	v_lshl_add_u64 v[34:35], v[34:35], 0, s[2:3]
	global_load_dword v108, v[34:35], off nt
	v_lshl_add_u64 v[34:35], v[34:35], 0, s[2:3]
	global_load_dword v109, v[34:35], off nt
	v_lshl_add_u64 v[34:35], v[34:35], 0, s[2:3]
	global_load_dword v110, v[34:35], off nt
	v_lshl_add_u64 v[34:35], v[34:35], 0, s[2:3]
	global_load_dword v111, v[34:35], off nt
	s_mul_i32 s70, s20, s26

.LBB0_1356:
	s_lshl_b32 s38, s25, 5
	s_ashr_i32 s25, s71, 8
	s_ashr_i32 s30, s25, 31
	s_mul_i32 s31, s25, s37
	s_mul_hi_u32 s37, s25, s36
	s_add_i32 s31, s37, s31
	s_mul_i32 s30, s30, s36
	s_add_i32 s31, s31, s30
	s_mul_i32 s30, s25, s36
	s_lshl_b64 s[30:31], s[30:31], 8
	s_add_u32 s20, s30, s20
	s_addc_u32 s21, s31, s21
	s_mul_i32 s21, s21, s16
	s_mul_hi_u32 s25, s20, s16
	s_add_i32 s25, s25, s21
	s_mul_i32 s20, s20, s16
	s_add_u32 s20, s34, s20
	s_addc_u32 s21, s35, s25
	s_lshl_b32 s25, s71, 5
	s_and_b32 s25, s25, 0x1fe0
	s_add_u32 s20, s20, s25
	s_addc_u32 s21, s21, 0
	s_ashr_i32 s25, s38, 31
	s_mul_i32 s25, s28, s25
	s_mul_hi_u32 s30, s28, s38
	s_add_i32 s25, s30, s25
	s_mul_i32 s30, s29, s38
	s_add_i32 s31, s25, s30
	s_mul_i32 s30, s28, s38
	s_lshl_b64 s[30:31], s[30:31], 2
	s_add_u32 s26, s26, s30
	s_addc_u32 s27, s27, s31
	s_ashr_i32 s25, s24, 31
	s_lshl_b64 s[24:25], s[24:25], 2
	s_add_u32 s24, s26, s24
	s_addc_u32 s25, s27, s25
	v_lshl_add_u64 v[34:35], s[24:25], 0, v[40:41]
	s_waitcnt vmcnt(0)
	global_load_dword v42, v40, s[24:25] nt
	s_lshl_b64 s[24:25], s[28:29], 2
	v_lshl_add_u64 v[34:35], v[34:35], 0, s[24:25]
	v_lshl_add_u64 v[36:37], v[34:35], 0, s[24:25]
	s_waitcnt vmcnt(26)
	v_lshl_add_u64 v[46:47], v[36:37], 0, s[24:25]
	s_waitcnt vmcnt(23)
	v_lshl_add_u64 v[48:49], v[46:47], 0, s[24:25]
	s_waitcnt vmcnt(22)
	v_lshl_add_u64 v[50:51], v[48:49], 0, s[24:25]
	s_waitcnt vmcnt(19)
	v_lshl_add_u64 v[52:53], v[50:51], 0, s[24:25]
	s_waitcnt vmcnt(18)
	v_lshl_add_u64 v[54:55], v[52:53], 0, s[24:25]
	global_load_dword v44, v[34:35], off nt
	global_load_dword v33, v[36:37], off nt
	global_load_dword v43, v[46:47], off nt
	s_nop 0
	global_load_dword v46, v[48:49], off nt
	s_nop 0
	global_load_dword v48, v[50:51], off nt
	global_load_dword v45, v[52:53], off nt
	global_load_dword v47, v[54:55], off nt
	v_lshl_add_u64 v[34:35], v[54:55], 0, s[24:25]
	global_load_dword v50, v[34:35], off nt
	v_lshl_add_u64 v[34:35], v[34:35], 0, s[24:25]
	global_load_dword v52, v[34:35], off nt
	v_lshl_add_u64 v[34:35], v[34:35], 0, s[24:25]
	global_load_dword v49, v[34:35], off nt
	v_lshl_add_u64 v[34:35], v[34:35], 0, s[24:25]
	global_load_dword v51, v[34:35], off nt
	v_lshl_add_u64 v[34:35], v[34:35], 0, s[24:25]
	global_load_dword v54, v[34:35], off nt
	v_lshl_add_u64 v[34:35], v[34:35], 0, s[24:25]
	global_load_dword v56, v[34:35], off nt
	v_lshl_add_u64 v[34:35], v[34:35], 0, s[24:25]
	global_load_dword v53, v[34:35], off nt
	v_lshl_add_u64 v[34:35], v[34:35], 0, s[24:25]
	global_load_dword v55, v[34:35], off nt
	v_lshl_add_u64 v[34:35], v[34:35], 0, s[24:25]
	global_load_dword v58, v[34:35], off nt
	v_lshl_add_u64 v[34:35], v[34:35], 0, s[24:25]
	global_load_dword v60, v[34:35], off nt
	v_lshl_add_u64 v[34:35], v[34:35], 0, s[24:25]
	global_load_dword v57, v[34:35], off nt
	v_lshl_add_u64 v[34:35], v[34:35], 0, s[24:25]
	global_load_dword v59, v[34:35], off nt
	v_lshl_add_u64 v[34:35], v[34:35], 0, s[24:25]
	global_load_dword v62, v[34:35], off nt
	v_lshl_add_u64 v[34:35], v[34:35], 0, s[24:25]
	global_load_dword v64, v[34:35], off nt
	v_lshl_add_u64 v[34:35], v[34:35], 0, s[24:25]
	global_load_dword v61, v[34:35], off nt
	v_lshl_add_u64 v[34:35], v[34:35], 0, s[24:25]
	global_load_dword v63, v[34:35], off nt
	v_lshl_add_u64 v[34:35], v[34:35], 0, s[24:25]
	global_load_dword v66, v[34:35], off nt
	v_lshl_add_u64 v[34:35], v[34:35], 0, s[24:25]
	global_load_dword v68, v[34:35], off nt
	v_lshl_add_u64 v[34:35], v[34:35], 0, s[24:25]
	global_load_dword v65, v[34:35], off nt
	v_lshl_add_u64 v[34:35], v[34:35], 0, s[24:25]
	global_load_dword v67, v[34:35], off nt
	v_lshl_add_u64 v[34:35], v[34:35], 0, s[24:25]
	global_load_dword v70, v[34:35], off nt
	v_lshl_add_u64 v[34:35], v[34:35], 0, s[24:25]
	global_load_dword v72, v[34:35], off nt
	v_lshl_add_u64 v[34:35], v[34:35], 0, s[24:25]
	global_load_dword v69, v[34:35], off nt
	v_lshl_add_u64 v[34:35], v[34:35], 0, s[24:25]
	global_load_dword v71, v[34:35], off nt
	s_mul_i32 s71, s38, s16

.LBB0_1418:
	s_ashr_i32 s30, s74, 8
	s_ashr_i32 s31, s30, 31
	s_mul_i32 s37, s30, s37
	s_mul_hi_u32 s38, s30, s36
	s_add_i32 s37, s38, s37
	s_mul_i32 s31, s31, s36
	s_add_i32 s31, s37, s31
	s_mul_i32 s30, s30, s36
	s_lshl_b32 s25, s25, 5
	s_lshl_b64 s[30:31], s[30:31], 8
	s_add_u32 s0, s30, s0
	s_addc_u32 s1, s31, s1
	s_mul_i32 s1, s1, s16
	s_mul_hi_u32 s30, s0, s16
	s_add_i32 s30, s30, s1
	s_mul_i32 s0, s0, s16
	s_add_u32 s0, s34, s0
	s_mul_i32 s50, s25, s16
	s_addc_u32 s1, s35, s30
	s_lshl_b32 s16, s74, 5
	s_and_b32 s16, s16, 0x1fe0
	s_add_u32 s0, s0, s16
	s_addc_u32 s1, s1, 0
	s_ashr_i32 s16, s25, 31
	s_mul_i32 s16, s28, s16
	s_mul_hi_u32 s30, s28, s25
	s_add_i32 s16, s30, s16
	s_mul_i32 s30, s29, s25
	s_add_i32 s31, s16, s30
	s_mul_i32 s30, s28, s25
	s_lshl_b64 s[30:31], s[30:31], 2
	s_add_u32 s16, s26, s30
	s_addc_u32 s26, s27, s31
	s_ashr_i32 s25, s24, 31
	s_lshl_b64 s[24:25], s[24:25], 2
	s_add_u32 s24, s16, s24
	s_addc_u32 s25, s26, s25
	s_waitcnt vmcnt(30)
	v_lshl_add_u64 v[2:3], s[24:25], 0, v[40:41]
	s_lshl_b64 s[26:27], s[28:29], 2
	v_lshl_add_u64 v[2:3], v[2:3], 0, s[26:27]
	s_waitcnt vmcnt(28)
	v_lshl_add_u64 v[4:5], v[2:3], 0, s[26:27]
	s_waitcnt vmcnt(26)
	v_lshl_add_u64 v[6:7], v[4:5], 0, s[26:27]
	s_waitcnt vmcnt(24)
	v_lshl_add_u64 v[8:9], v[6:7], 0, s[26:27]
	s_waitcnt vmcnt(22)
	v_lshl_add_u64 v[10:11], v[8:9], 0, s[26:27]
	s_waitcnt vmcnt(20)
	v_lshl_add_u64 v[12:13], v[10:11], 0, s[26:27]
	s_waitcnt vmcnt(18)
	v_lshl_add_u64 v[14:15], v[12:13], 0, s[26:27]
	s_waitcnt vmcnt(16)
	v_lshl_add_u64 v[16:17], v[14:15], 0, s[26:27]
	s_waitcnt vmcnt(14)
	v_lshl_add_u64 v[18:19], v[16:17], 0, s[26:27]
	s_waitcnt vmcnt(12)
	v_lshl_add_u64 v[20:21], v[18:19], 0, s[26:27]
	s_waitcnt vmcnt(10)
	v_lshl_add_u64 v[22:23], v[20:21], 0, s[26:27]
	s_waitcnt vmcnt(8)
	v_lshl_add_u64 v[24:25], v[22:23], 0, s[26:27]
	s_waitcnt vmcnt(6)
	v_lshl_add_u64 v[26:27], v[24:25], 0, s[26:27]
	s_waitcnt vmcnt(4)
	v_lshl_add_u64 v[28:29], v[26:27], 0, s[26:27]
	s_waitcnt vmcnt(2)
	v_lshl_add_u64 v[30:31], v[28:29], 0, s[26:27]
	v_lshl_add_u64 v[34:35], v[30:31], 0, s[26:27]
	v_lshl_add_u64 v[36:37], v[34:35], 0, s[26:27]
	v_lshl_add_u64 v[74:75], v[36:37], 0, s[26:27]
	v_lshl_add_u64 v[114:115], v[74:75], 0, s[26:27]
	v_lshl_add_u64 v[116:117], v[114:115], 0, s[26:27]
	v_lshl_add_u64 v[118:119], v[116:117], 0, s[26:27]
	v_lshl_add_u64 v[120:121], v[118:119], 0, s[26:27]
	v_lshl_add_u64 v[122:123], v[120:121], 0, s[26:27]
	v_lshl_add_u64 v[124:125], v[122:123], 0, s[26:27]
	v_lshl_add_u64 v[126:127], v[124:125], 0, s[26:27]
	v_lshl_add_u64 v[128:129], v[126:127], 0, s[26:27]
	v_lshl_add_u64 v[130:131], v[128:129], 0, s[26:27]
	v_lshl_add_u64 v[132:133], v[130:131], 0, s[26:27]
	v_lshl_add_u64 v[134:135], v[132:133], 0, s[26:27]
	v_lshl_add_u64 v[136:137], v[134:135], 0, s[26:27]
	v_lshl_add_u64 v[138:139], v[136:137], 0, s[26:27]
	s_waitcnt vmcnt(0)
	global_load_dword v1, v[2:3], off nt
	s_nop 0
	global_load_dword v2, v[4:5], off nt
	global_load_dword v3, v[6:7], off nt
	s_nop 0
	global_load_dword v4, v[8:9], off nt
	global_load_dword v5, v[10:11], off nt
	global_load_dword v6, v[12:13], off nt
	global_load_dword v7, v[14:15], off nt
	s_nop 0
	global_load_dword v8, v[16:17], off nt
	global_load_dword v9, v[18:19], off nt
	global_load_dword v10, v[20:21], off nt
	global_load_dword v11, v[22:23], off nt
	global_load_dword v12, v[24:25], off nt
	global_load_dword v13, v[26:27], off nt
	global_load_dword v14, v[28:29], off nt
	global_load_dword v15, v[30:31], off nt
	global_load_dword v16, v[34:35], off nt
	global_load_dword v17, v[36:37], off nt
	global_load_dword v18, v[74:75], off nt
	global_load_dword v19, v[114:115], off nt
	global_load_dword v20, v[116:117], off nt
	global_load_dword v21, v[118:119], off nt
	global_load_dword v22, v[120:121], off nt
	global_load_dword v23, v[122:123], off nt
	global_load_dword v24, v[124:125], off nt
	global_load_dword v25, v[126:127], off nt
	global_load_dword v26, v[128:129], off nt
	global_load_dword v27, v[130:131], off nt
	global_load_dword v28, v[132:133], off nt
	global_load_dword v29, v[134:135], off nt
	global_load_dword v30, v[136:137], off nt
	global_load_dword v31, v[138:139], off nt
	global_load_dword v32, v40, s[24:25] nt

.LBB0_1479:
	s_ashr_i32 s23, s70, 8
	s_ashr_i32 s28, s23, 31
	s_mul_i32 s29, s23, s35
	s_mul_hi_u32 s35, s23, s34
	s_add_i32 s29, s35, s29
	s_mul_i32 s28, s28, s34
	s_add_i32 s29, s29, s28
	s_mul_i32 s28, s23, s34
	s_lshl_b32 s36, s40, 5
	s_lshl_b64 s[28:29], s[28:29], 8
	s_add_u32 s18, s28, s18
	s_addc_u32 s19, s29, s19
	s_mul_i32 s19, s19, s16
	s_mul_hi_u32 s23, s18, s16
	s_add_i32 s23, s23, s19
	s_mul_i32 s18, s18, s16
	s_add_u32 s18, s30, s18
	s_addc_u32 s19, s31, s23
	s_lshl_b32 s23, s70, 5
	s_and_b32 s23, s23, 0x1fe0
	s_add_u32 s18, s18, s23
	s_addc_u32 s19, s19, 0
	s_ashr_i32 s23, s36, 31
	s_mul_i32 s23, s26, s23
	s_mul_hi_u32 s28, s26, s36
	s_add_i32 s23, s28, s23
	s_mul_i32 s28, s27, s36
	s_add_i32 s29, s23, s28
	s_mul_i32 s28, s26, s36
	s_lshl_b64 s[28:29], s[28:29], 2
	s_add_u32 s24, s24, s28
	s_addc_u32 s25, s25, s29
	s_ashr_i32 s23, s22, 31
	s_lshl_b64 s[22:23], s[22:23], 2
	s_add_u32 s22, s24, s22
	s_addc_u32 s23, s25, s23
	v_lshl_add_u64 v[34:35], s[22:23], 0, v[40:41]
	s_waitcnt vmcnt(0)
	global_load_dword v80, v40, s[22:23] nt
	s_lshl_b64 s[22:23], s[26:27], 2
	v_lshl_add_u64 v[34:35], v[34:35], 0, s[22:23]
	v_lshl_add_u64 v[36:37], v[34:35], 0, s[22:23]
	v_lshl_add_u64 v[74:75], v[36:37], 0, s[22:23]
	s_waitcnt vmcnt(29)
	v_lshl_add_u64 v[84:85], v[74:75], 0, s[22:23]
	s_waitcnt vmcnt(27)
	v_lshl_add_u64 v[86:87], v[84:85], 0, s[22:23]
	s_waitcnt vmcnt(25)
	v_lshl_add_u64 v[88:89], v[86:87], 0, s[22:23]
	s_waitcnt vmcnt(23)
	v_lshl_add_u64 v[90:91], v[88:89], 0, s[22:23]
	global_load_dword v81, v[34:35], off nt
	global_load_dword v82, v[36:37], off nt
	global_load_dword v83, v[74:75], off nt
	s_nop 0
	global_load_dword v84, v[84:85], off nt
	s_nop 0
	global_load_dword v85, v[86:87], off nt
	s_nop 0
	global_load_dword v86, v[88:89], off nt
	global_load_dword v87, v[90:91], off nt
	v_lshl_add_u64 v[34:35], v[90:91], 0, s[22:23]
	global_load_dword v88, v[34:35], off nt
	v_lshl_add_u64 v[34:35], v[34:35], 0, s[22:23]
	global_load_dword v89, v[34:35], off nt
	v_lshl_add_u64 v[34:35], v[34:35], 0, s[22:23]
	global_load_dword v90, v[34:35], off nt
	v_lshl_add_u64 v[34:35], v[34:35], 0, s[22:23]
	global_load_dword v91, v[34:35], off nt
	v_lshl_add_u64 v[34:35], v[34:35], 0, s[22:23]
	global_load_dword v92, v[34:35], off nt
	v_lshl_add_u64 v[34:35], v[34:35], 0, s[22:23]
	global_load_dword v93, v[34:35], off nt
	v_lshl_add_u64 v[34:35], v[34:35], 0, s[22:23]
	global_load_dword v94, v[34:35], off nt
	v_lshl_add_u64 v[34:35], v[34:35], 0, s[22:23]
	global_load_dword v95, v[34:35], off nt
	v_lshl_add_u64 v[34:35], v[34:35], 0, s[22:23]
	global_load_dword v96, v[34:35], off nt
	v_lshl_add_u64 v[34:35], v[34:35], 0, s[22:23]
	global_load_dword v97, v[34:35], off nt
	v_lshl_add_u64 v[34:35], v[34:35], 0, s[22:23]
	global_load_dword v98, v[34:35], off nt
	v_lshl_add_u64 v[34:35], v[34:35], 0, s[22:23]
	global_load_dword v99, v[34:35], off nt
	v_lshl_add_u64 v[34:35], v[34:35], 0, s[22:23]
	global_load_dword v100, v[34:35], off nt
	v_lshl_add_u64 v[34:35], v[34:35], 0, s[22:23]
	global_load_dword v101, v[34:35], off nt
	v_lshl_add_u64 v[34:35], v[34:35], 0, s[22:23]
	global_load_dword v102, v[34:35], off nt
	v_lshl_add_u64 v[34:35], v[34:35], 0, s[22:23]
	global_load_dword v103, v[34:35], off nt
	v_lshl_add_u64 v[34:35], v[34:35], 0, s[22:23]
	global_load_dword v104, v[34:35], off nt
	v_lshl_add_u64 v[34:35], v[34:35], 0, s[22:23]
	global_load_dword v105, v[34:35], off nt
	v_lshl_add_u64 v[34:35], v[34:35], 0, s[22:23]
	global_load_dword v106, v[34:35], off nt
	v_lshl_add_u64 v[34:35], v[34:35], 0, s[22:23]
	global_load_dword v107, v[34:35], off nt
	v_lshl_add_u64 v[34:35], v[34:35], 0, s[22:23]
	global_load_dword v108, v[34:35], off nt
	v_lshl_add_u64 v[34:35], v[34:35], 0, s[22:23]
	global_load_dword v109, v[34:35], off nt
	v_lshl_add_u64 v[34:35], v[34:35], 0, s[22:23]
	global_load_dword v110, v[34:35], off nt
	v_lshl_add_u64 v[34:35], v[34:35], 0, s[22:23]
	global_load_dword v111, v[34:35], off nt
	s_mul_i32 s70, s36, s16

.LBB0_1661:
	s_ashr_i32 s14, s21, 8
	s_ashr_i32 s15, s14, 31
	s_mul_i32 s13, s14, s13
	s_mul_hi_u32 s16, s14, s12
	s_add_i32 s13, s16, s13
	s_mul_i32 s15, s15, s12
	s_add_i32 s13, s13, s15
	s_mul_i32 s12, s14, s12
	s_lshl_b32 s22, s94, 3
	s_lshl_b32 s3, s3, 5
	s_lshl_b64 s[12:13], s[12:13], 8
	s_add_u32 s10, s12, s10
	s_addc_u32 s11, s13, s11
	s_mul_i32 s11, s11, s23
	s_mul_hi_u32 s12, s10, s23
	s_add_i32 s12, s12, s11
	s_mul_i32 s10, s10, s23
	s_add_u32 s0, s0, s10
	s_addc_u32 s1, s1, s12
	s_lshl_b32 s10, s21, 5
	s_and_b32 s10, s10, 0x1fe0
	s_add_u32 s0, s0, s10
	s_addc_u32 s1, s1, 0
	s_ashr_i32 s10, s3, 31
	s_mul_i32 s10, s8, s10
	s_mul_hi_u32 s11, s8, s3
	s_add_i32 s10, s11, s10
	s_mul_i32 s11, s9, s3
	s_add_i32 s11, s10, s11
	s_mul_i32 s10, s8, s3
	s_lshl_b64 s[10:11], s[10:11], 2
	s_add_u32 s4, s4, s10
	s_mul_i32 s53, s3, s23
	s_addc_u32 s5, s5, s11
	s_ashr_i32 s3, s2, 31
	s_lshl_b64 s[2:3], s[2:3], 2
	v_and_b32_e32 v38, 63, v2
	s_add_u32 s2, s4, s2
	v_mov_b32_e32 v39, 0
	s_addc_u32 s3, s5, s3
	v_lshlrev_b32_e32 v40, 2, v38
	v_mov_b32_e32 v41, v39
	v_lshl_add_u64 v[2:3], s[2:3], 0, v[40:41]
	s_lshl_b64 s[4:5], s[8:9], 2
	v_lshl_add_u64 v[2:3], v[2:3], 0, s[4:5]
	v_lshl_add_u64 v[4:5], v[2:3], 0, s[4:5]
	v_lshl_add_u64 v[6:7], v[4:5], 0, s[4:5]
	v_lshl_add_u64 v[8:9], v[6:7], 0, s[4:5]
	v_lshl_add_u64 v[10:11], v[8:9], 0, s[4:5]
	v_lshl_add_u64 v[12:13], v[10:11], 0, s[4:5]
	v_lshl_add_u64 v[14:15], v[12:13], 0, s[4:5]
	v_lshl_add_u64 v[16:17], v[14:15], 0, s[4:5]
	v_lshl_add_u64 v[18:19], v[16:17], 0, s[4:5]
	v_lshl_add_u64 v[20:21], v[18:19], 0, s[4:5]
	v_lshl_add_u64 v[22:23], v[20:21], 0, s[4:5]
	v_lshl_add_u64 v[24:25], v[22:23], 0, s[4:5]
	v_lshl_add_u64 v[26:27], v[24:25], 0, s[4:5]
	v_lshl_add_u64 v[28:29], v[26:27], 0, s[4:5]
	v_lshl_add_u64 v[30:31], v[28:29], 0, s[4:5]
	v_lshl_add_u64 v[32:33], v[30:31], 0, s[4:5]
	v_lshl_add_u64 v[34:35], v[32:33], 0, s[4:5]
	v_lshl_add_u64 v[36:37], v[34:35], 0, s[4:5]
	v_lshl_add_u64 v[42:43], v[36:37], 0, s[4:5]
	v_lshl_add_u64 v[44:45], v[42:43], 0, s[4:5]
	v_lshl_add_u64 v[46:47], v[44:45], 0, s[4:5]
	v_lshl_add_u64 v[48:49], v[46:47], 0, s[4:5]
	v_lshl_add_u64 v[50:51], v[48:49], 0, s[4:5]
	v_lshl_add_u64 v[52:53], v[50:51], 0, s[4:5]
	v_lshl_add_u64 v[54:55], v[52:53], 0, s[4:5]
	v_lshl_add_u64 v[56:57], v[54:55], 0, s[4:5]
	v_lshl_add_u64 v[58:59], v[56:57], 0, s[4:5]
	v_lshl_add_u64 v[60:61], v[58:59], 0, s[4:5]
	v_lshl_add_u64 v[62:63], v[60:61], 0, s[4:5]
	v_lshl_add_u64 v[64:65], v[62:63], 0, s[4:5]
	v_lshl_add_u64 v[66:67], v[64:65], 0, s[4:5]
	s_waitcnt vmcnt(0)
	global_load_dword v1, v[2:3], off nt
	s_nop 0
	global_load_dword v2, v[4:5], off nt
	global_load_dword v3, v[6:7], off nt
	s_nop 0
	global_load_dword v4, v[8:9], off nt
	global_load_dword v5, v[10:11], off nt
	global_load_dword v6, v[12:13], off nt
	global_load_dword v7, v[14:15], off nt
	s_nop 0
	global_load_dword v8, v[16:17], off nt
	global_load_dword v9, v[18:19], off nt
	global_load_dword v10, v[20:21], off nt
	global_load_dword v11, v[22:23], off nt
	global_load_dword v12, v[24:25], off nt
	global_load_dword v13, v[26:27], off nt
	global_load_dword v14, v[28:29], off nt
	global_load_dword v15, v[30:31], off nt
	global_load_dword v16, v[32:33], off nt
	global_load_dword v17, v[34:35], off nt
	global_load_dword v18, v[36:37], off nt
	global_load_dword v19, v[42:43], off nt
	global_load_dword v20, v[44:45], off nt
	global_load_dword v21, v[46:47], off nt
	global_load_dword v22, v[48:49], off nt
	global_load_dword v23, v[50:51], off nt
	global_load_dword v24, v[52:53], off nt
	global_load_dword v25, v[54:55], off nt
	global_load_dword v26, v[56:57], off nt
	global_load_dword v27, v[58:59], off nt
	global_load_dword v28, v[60:61], off nt
	global_load_dword v29, v[62:63], off nt
	global_load_dword v30, v[64:65], off nt
	global_load_dword v31, v[66:67], off nt
	global_load_dword v32, v40, s[2:3] nt
	s_add_i32 s23, s20, s22
	s_cmp_gt_i32 s23, 0x24fff
	s_mov_b64 s[20:21], s[0:1]
	s_mov_b32 s73, s53
	s_mov_b32 s52, s50
	s_waitcnt lgkmcnt(0)
	v_mov_b32_e32 v79, v73
	s_mov_b32 s54, s51
	s_cbranch_scc1 .LBB0_1721
	s_cmpk_gt_i32 s23, 0x17ff
	s_cbranch_scc0 .LBB0_1672
	s_cmpk_gt_u32 s23, 0x1fff
	s_cbranch_scc0 .LBB0_1675
	s_cmpk_gt_u32 s23, 0x35ff
	s_cbranch_scc0 .LBB0_1676
	s_cmpk_gt_u32 s23, 0x4bff
	s_cbranch_scc0 .LBB0_1677
	s_cmpk_gt_u32 s23, 0x61ff
	s_cbranch_scc0 .LBB0_1678
	s_cmpk_gt_u32 s23, 0x79ff
	s_cbranch_scc0 .LBB0_1679
	s_cmpk_gt_u32 s23, 0x81ff
	s_cbranch_scc0 .LBB0_1680
	s_cmp_gt_u32 s23, 0x161ff
	s_cbranch_scc0 .LBB0_1681
	s_cmp_gt_u32 s23, 0x241ff
	s_mov_b64 s[16:17], -1
	s_cbranch_scc0 .LBB0_1682
	s_add_i32 s2, s23, 0xbe00
	s_bfe_u32 s3, s2, 0x6000a
	s_mulk_i32 s3, 0x2493
	s_lshr_b32 s10, s3, 16
	s_mul_i32 s3, s10, 0x1c00
	s_sub_i32 s2, s2, s3
	s_and_b32 s4, s2, 0xffff
	s_bfe_u32 s3, s2, 0xb0005
	s_lshl_b32 s2, s4, 6
	s_and_b32 s2, s2, 0x7c0
	s_mul_i32 s4, s10, 0x3800000
	v_readlane_b32 s24, v254, 0
	v_readlane_b32 s25, v254, 1
	s_add_u32 s4, s24, s4
	s_addc_u32 s5, s25, 0
	s_add_u32 s8, s96, 0x24a00000
	s_mov_b32 s13, 0
	v_readlane_b32 s26, v254, 2
	v_readlane_b32 s27, v254, 3
	s_addc_u32 s9, s97, 0
	s_mul_i32 s12, s10, 0xe00000
	s_mov_b64 s[10:11], 0
	s_branch .LBB0_1683

.LBB0_1720:
	s_lshl_b32 s16, s3, 5
	s_ashr_i32 s3, s24, 8
	s_ashr_i32 s17, s3, 31
	s_mul_i32 s15, s3, s15
	s_mul_hi_u32 s18, s3, s14
	s_add_i32 s15, s18, s15
	s_mul_i32 s17, s17, s14
	s_add_i32 s15, s15, s17
	s_mul_i32 s14, s3, s14
	s_lshl_b64 s[14:15], s[14:15], 8
	s_add_u32 s3, s14, s12
	s_addc_u32 s12, s15, s13
	s_mul_i32 s12, s12, s26
	s_mul_hi_u32 s13, s3, s26
	s_add_i32 s13, s13, s12
	s_mul_i32 s3, s3, s26
	s_add_u32 s3, s8, s3
	s_addc_u32 s8, s9, s13
	s_lshl_b32 s9, s24, 5
	s_and_b32 s9, s9, 0x1fe0
	s_add_u32 s20, s3, s9
	s_addc_u32 s21, s8, 0
	s_ashr_i32 s3, s16, 31
	s_mul_i32 s3, s10, s3
	s_mul_hi_u32 s8, s10, s16
	s_add_i32 s3, s8, s3
	s_mul_i32 s8, s11, s16
	s_add_i32 s9, s3, s8
	s_mul_i32 s8, s10, s16
	s_lshl_b64 s[8:9], s[8:9], 2
	s_add_u32 s4, s4, s8
	s_addc_u32 s5, s5, s9
	s_ashr_i32 s3, s2, 31
	s_lshl_b64 s[2:3], s[2:3], 2
	s_add_u32 s2, s4, s2
	s_addc_u32 s3, s5, s3
	v_mov_b32_e32 v41, 0
	v_lshl_add_u64 v[34:35], s[2:3], 0, v[40:41]
	s_waitcnt vmcnt(0)
	global_load_dword v80, v40, s[2:3] nt
	s_lshl_b64 s[2:3], s[10:11], 2
	v_lshl_add_u64 v[34:35], v[34:35], 0, s[2:3]
	v_lshl_add_u64 v[36:37], v[34:35], 0, s[2:3]
	v_lshl_add_u64 v[42:43], v[36:37], 0, s[2:3]
	v_lshl_add_u64 v[44:45], v[42:43], 0, s[2:3]
	v_lshl_add_u64 v[46:47], v[44:45], 0, s[2:3]
	v_lshl_add_u64 v[48:49], v[46:47], 0, s[2:3]
	v_lshl_add_u64 v[50:51], v[48:49], 0, s[2:3]
	global_load_dword v81, v[34:35], off nt
	global_load_dword v82, v[36:37], off nt
	global_load_dword v83, v[42:43], off nt
	global_load_dword v84, v[44:45], off nt
	global_load_dword v85, v[46:47], off nt
	global_load_dword v86, v[48:49], off nt
	global_load_dword v87, v[50:51], off nt
	v_lshl_add_u64 v[34:35], v[50:51], 0, s[2:3]
	global_load_dword v88, v[34:35], off nt
	v_lshl_add_u64 v[34:35], v[34:35], 0, s[2:3]
	global_load_dword v89, v[34:35], off nt
	v_lshl_add_u64 v[34:35], v[34:35], 0, s[2:3]
	global_load_dword v90, v[34:35], off nt
	v_lshl_add_u64 v[34:35], v[34:35], 0, s[2:3]
	global_load_dword v91, v[34:35], off nt
	v_lshl_add_u64 v[34:35], v[34:35], 0, s[2:3]
	global_load_dword v92, v[34:35], off nt
	v_lshl_add_u64 v[34:35], v[34:35], 0, s[2:3]
	global_load_dword v93, v[34:35], off nt
	v_lshl_add_u64 v[34:35], v[34:35], 0, s[2:3]
	global_load_dword v94, v[34:35], off nt
	v_lshl_add_u64 v[34:35], v[34:35], 0, s[2:3]
	global_load_dword v95, v[34:35], off nt
	v_lshl_add_u64 v[34:35], v[34:35], 0, s[2:3]
	global_load_dword v96, v[34:35], off nt
	v_lshl_add_u64 v[34:35], v[34:35], 0, s[2:3]
	global_load_dword v97, v[34:35], off nt
	v_lshl_add_u64 v[34:35], v[34:35], 0, s[2:3]
	global_load_dword v98, v[34:35], off nt
	v_lshl_add_u64 v[34:35], v[34:35], 0, s[2:3]
	global_load_dword v99, v[34:35], off nt
	v_lshl_add_u64 v[34:35], v[34:35], 0, s[2:3]
	global_load_dword v100, v[34:35], off nt
	v_lshl_add_u64 v[34:35], v[34:35], 0, s[2:3]
	global_load_dword v101, v[34:35], off nt
	v_lshl_add_u64 v[34:35], v[34:35], 0, s[2:3]
	global_load_dword v102, v[34:35], off nt
	v_lshl_add_u64 v[34:35], v[34:35], 0, s[2:3]
	global_load_dword v103, v[34:35], off nt
	v_lshl_add_u64 v[34:35], v[34:35], 0, s[2:3]
	global_load_dword v104, v[34:35], off nt
	v_lshl_add_u64 v[34:35], v[34:35], 0, s[2:3]
	global_load_dword v105, v[34:35], off nt
	v_lshl_add_u64 v[34:35], v[34:35], 0, s[2:3]
	global_load_dword v106, v[34:35], off nt
	v_lshl_add_u64 v[34:35], v[34:35], 0, s[2:3]
	global_load_dword v107, v[34:35], off nt
	v_lshl_add_u64 v[34:35], v[34:35], 0, s[2:3]
	global_load_dword v108, v[34:35], off nt
	v_lshl_add_u64 v[34:35], v[34:35], 0, s[2:3]
	global_load_dword v109, v[34:35], off nt
	v_lshl_add_u64 v[34:35], v[34:35], 0, s[2:3]
	global_load_dword v110, v[34:35], off nt
	v_lshl_add_u64 v[34:35], v[34:35], 0, s[2:3]
	global_load_dword v111, v[34:35], off nt
	s_mul_i32 s73, s16, s26

.LBB0_1774:
	s_ashr_i32 s27, s76, 8
	s_ashr_i32 s34, s27, 31
	s_mul_i32 s23, s27, s23
	s_mul_hi_u32 s35, s27, s22
	s_add_i32 s23, s35, s23
	s_mul_i32 s34, s34, s22
	s_add_i32 s23, s23, s34
	s_mul_i32 s22, s27, s22
	s_lshl_b32 s40, s74, 5
	s_lshl_b64 s[22:23], s[22:23], 8
	s_add_u32 s22, s22, s36
	s_addc_u32 s23, s23, s37
	s_mul_i32 s23, s23, s18
	s_mul_hi_u32 s27, s22, s18
	s_add_i32 s27, s27, s23
	s_mul_i32 s22, s22, s18
	s_add_u32 s22, s38, s22
	s_addc_u32 s23, s39, s27
	s_lshl_b32 s27, s76, 5
	s_and_b32 s27, s27, 0x1fe0
	s_add_u32 s22, s22, s27
	s_addc_u32 s23, s23, 0
	s_ashr_i32 s27, s40, 31
	s_mul_i32 s27, s30, s27
	s_mul_hi_u32 s34, s30, s40
	s_add_i32 s27, s34, s27
	s_mul_i32 s34, s31, s40
	s_add_i32 s35, s27, s34
	s_mul_i32 s34, s30, s40
	s_lshl_b64 s[34:35], s[34:35], 2
	s_add_u32 s28, s28, s34
	s_addc_u32 s29, s29, s35
	s_ashr_i32 s27, s26, 31
	s_lshl_b64 s[26:27], s[26:27], 2
	s_add_u32 s26, s28, s26
	s_addc_u32 s27, s29, s27
	v_lshl_add_u64 v[34:35], s[26:27], 0, v[40:41]
	s_waitcnt vmcnt(0)
	global_load_dword v42, v40, s[26:27] nt
	s_lshl_b64 s[26:27], s[30:31], 2
	v_lshl_add_u64 v[34:35], v[34:35], 0, s[26:27]
	v_lshl_add_u64 v[36:37], v[34:35], 0, s[26:27]
	s_waitcnt vmcnt(26)
	v_lshl_add_u64 v[46:47], v[36:37], 0, s[26:27]
	s_waitcnt vmcnt(23)
	v_lshl_add_u64 v[48:49], v[46:47], 0, s[26:27]
	s_waitcnt vmcnt(22)
	v_lshl_add_u64 v[50:51], v[48:49], 0, s[26:27]
	s_waitcnt vmcnt(19)
	v_lshl_add_u64 v[52:53], v[50:51], 0, s[26:27]
	s_waitcnt vmcnt(18)
	v_lshl_add_u64 v[54:55], v[52:53], 0, s[26:27]
	global_load_dword v44, v[34:35], off nt
	global_load_dword v33, v[36:37], off nt
	global_load_dword v43, v[46:47], off nt
	s_nop 0
	global_load_dword v46, v[48:49], off nt
	s_nop 0
	global_load_dword v48, v[50:51], off nt
	global_load_dword v45, v[52:53], off nt
	global_load_dword v47, v[54:55], off nt
	v_lshl_add_u64 v[34:35], v[54:55], 0, s[26:27]
	global_load_dword v50, v[34:35], off nt
	v_lshl_add_u64 v[34:35], v[34:35], 0, s[26:27]
	global_load_dword v52, v[34:35], off nt
	v_lshl_add_u64 v[34:35], v[34:35], 0, s[26:27]
	global_load_dword v49, v[34:35], off nt
	v_lshl_add_u64 v[34:35], v[34:35], 0, s[26:27]
	global_load_dword v51, v[34:35], off nt
	v_lshl_add_u64 v[34:35], v[34:35], 0, s[26:27]
	global_load_dword v54, v[34:35], off nt
	v_lshl_add_u64 v[34:35], v[34:35], 0, s[26:27]
	global_load_dword v56, v[34:35], off nt
	v_lshl_add_u64 v[34:35], v[34:35], 0, s[26:27]
	global_load_dword v53, v[34:35], off nt
	v_lshl_add_u64 v[34:35], v[34:35], 0, s[26:27]
	global_load_dword v55, v[34:35], off nt
	v_lshl_add_u64 v[34:35], v[34:35], 0, s[26:27]
	global_load_dword v58, v[34:35], off nt
	v_lshl_add_u64 v[34:35], v[34:35], 0, s[26:27]
	global_load_dword v60, v[34:35], off nt
	v_lshl_add_u64 v[34:35], v[34:35], 0, s[26:27]
	global_load_dword v57, v[34:35], off nt
	v_lshl_add_u64 v[34:35], v[34:35], 0, s[26:27]
	global_load_dword v59, v[34:35], off nt
	v_lshl_add_u64 v[34:35], v[34:35], 0, s[26:27]
	global_load_dword v62, v[34:35], off nt
	v_lshl_add_u64 v[34:35], v[34:35], 0, s[26:27]
	global_load_dword v64, v[34:35], off nt
	v_lshl_add_u64 v[34:35], v[34:35], 0, s[26:27]
	global_load_dword v61, v[34:35], off nt
	v_lshl_add_u64 v[34:35], v[34:35], 0, s[26:27]
	global_load_dword v63, v[34:35], off nt
	v_lshl_add_u64 v[34:35], v[34:35], 0, s[26:27]
	global_load_dword v66, v[34:35], off nt
	v_lshl_add_u64 v[34:35], v[34:35], 0, s[26:27]
	global_load_dword v68, v[34:35], off nt
	v_lshl_add_u64 v[34:35], v[34:35], 0, s[26:27]
	global_load_dword v65, v[34:35], off nt
	v_lshl_add_u64 v[34:35], v[34:35], 0, s[26:27]
	global_load_dword v67, v[34:35], off nt
	v_lshl_add_u64 v[34:35], v[34:35], 0, s[26:27]
	global_load_dword v70, v[34:35], off nt
	v_lshl_add_u64 v[34:35], v[34:35], 0, s[26:27]
	global_load_dword v72, v[34:35], off nt
	v_lshl_add_u64 v[34:35], v[34:35], 0, s[26:27]
	global_load_dword v69, v[34:35], off nt
	v_lshl_add_u64 v[34:35], v[34:35], 0, s[26:27]
	global_load_dword v71, v[34:35], off nt
	s_mul_i32 s74, s40, s18

.LBB0_1839:
	s_ashr_i32 s34, s76, 8
	s_ashr_i32 s35, s34, 31
	s_mul_i32 s1, s34, s1
	s_mul_hi_u32 s40, s34, s0
	s_add_i32 s1, s40, s1
	s_mul_i32 s35, s35, s0
	s_add_i32 s1, s1, s35
	s_mul_i32 s0, s34, s0
	s_lshl_b32 s27, s53, 5
	s_lshl_b64 s[0:1], s[0:1], 8
	s_add_u32 s0, s0, s36
	s_addc_u32 s1, s1, s37
	s_mul_i32 s1, s1, s18
	s_mul_hi_u32 s34, s0, s18
	s_add_i32 s34, s34, s1
	s_mul_i32 s0, s0, s18
	s_add_u32 s0, s38, s0
	s_mul_i32 s53, s27, s18
	s_addc_u32 s1, s39, s34
	s_lshl_b32 s18, s76, 5
	s_and_b32 s18, s18, 0x1fe0
	s_add_u32 s0, s0, s18
	s_addc_u32 s1, s1, 0
	s_ashr_i32 s18, s27, 31
	s_mul_i32 s18, s30, s18
	s_mul_hi_u32 s34, s30, s27
	s_add_i32 s18, s34, s18
	s_mul_i32 s34, s31, s27
	s_add_i32 s35, s18, s34
	s_mul_i32 s34, s30, s27
	s_lshl_b64 s[34:35], s[34:35], 2
	s_add_u32 s18, s28, s34
	s_addc_u32 s28, s29, s35
	s_ashr_i32 s27, s26, 31
	s_lshl_b64 s[26:27], s[26:27], 2
	s_add_u32 s26, s18, s26
	s_addc_u32 s27, s28, s27
	s_waitcnt vmcnt(30)
	v_lshl_add_u64 v[2:3], s[26:27], 0, v[40:41]
	s_lshl_b64 s[28:29], s[30:31], 2
	v_lshl_add_u64 v[2:3], v[2:3], 0, s[28:29]
	s_waitcnt vmcnt(28)
	v_lshl_add_u64 v[4:5], v[2:3], 0, s[28:29]
	s_waitcnt vmcnt(26)
	v_lshl_add_u64 v[6:7], v[4:5], 0, s[28:29]
	s_waitcnt vmcnt(24)
	v_lshl_add_u64 v[8:9], v[6:7], 0, s[28:29]
	s_waitcnt vmcnt(22)
	v_lshl_add_u64 v[10:11], v[8:9], 0, s[28:29]
	s_waitcnt vmcnt(20)
	v_lshl_add_u64 v[12:13], v[10:11], 0, s[28:29]
	s_waitcnt vmcnt(18)
	v_lshl_add_u64 v[14:15], v[12:13], 0, s[28:29]
	s_waitcnt vmcnt(16)
	v_lshl_add_u64 v[16:17], v[14:15], 0, s[28:29]
	s_waitcnt vmcnt(14)
	v_lshl_add_u64 v[18:19], v[16:17], 0, s[28:29]
	s_waitcnt vmcnt(12)
	v_lshl_add_u64 v[20:21], v[18:19], 0, s[28:29]
	s_waitcnt vmcnt(10)
	v_lshl_add_u64 v[22:23], v[20:21], 0, s[28:29]
	s_waitcnt vmcnt(8)
	v_lshl_add_u64 v[24:25], v[22:23], 0, s[28:29]
	s_waitcnt vmcnt(6)
	v_lshl_add_u64 v[26:27], v[24:25], 0, s[28:29]
	s_waitcnt vmcnt(4)
	v_lshl_add_u64 v[28:29], v[26:27], 0, s[28:29]
	s_waitcnt vmcnt(2)
	v_lshl_add_u64 v[30:31], v[28:29], 0, s[28:29]
	v_lshl_add_u64 v[34:35], v[30:31], 0, s[28:29]
	v_lshl_add_u64 v[36:37], v[34:35], 0, s[28:29]
	v_lshl_add_u64 v[74:75], v[36:37], 0, s[28:29]
	v_lshl_add_u64 v[114:115], v[74:75], 0, s[28:29]
	v_lshl_add_u64 v[116:117], v[114:115], 0, s[28:29]
	v_lshl_add_u64 v[118:119], v[116:117], 0, s[28:29]
	v_lshl_add_u64 v[120:121], v[118:119], 0, s[28:29]
	v_lshl_add_u64 v[122:123], v[120:121], 0, s[28:29]
	v_lshl_add_u64 v[124:125], v[122:123], 0, s[28:29]
	v_lshl_add_u64 v[126:127], v[124:125], 0, s[28:29]
	v_lshl_add_u64 v[128:129], v[126:127], 0, s[28:29]
	v_lshl_add_u64 v[130:131], v[128:129], 0, s[28:29]
	v_lshl_add_u64 v[132:133], v[130:131], 0, s[28:29]
	v_lshl_add_u64 v[134:135], v[132:133], 0, s[28:29]
	v_lshl_add_u64 v[136:137], v[134:135], 0, s[28:29]
	v_lshl_add_u64 v[138:139], v[136:137], 0, s[28:29]
	s_waitcnt vmcnt(0)
	global_load_dword v1, v[2:3], off nt
	s_nop 0
	global_load_dword v2, v[4:5], off nt
	global_load_dword v3, v[6:7], off nt
	s_nop 0
	global_load_dword v4, v[8:9], off nt
	global_load_dword v5, v[10:11], off nt
	global_load_dword v6, v[12:13], off nt
	global_load_dword v7, v[14:15], off nt
	s_nop 0
	global_load_dword v8, v[16:17], off nt
	global_load_dword v9, v[18:19], off nt
	global_load_dword v10, v[20:21], off nt
	global_load_dword v11, v[22:23], off nt
	global_load_dword v12, v[24:25], off nt
	global_load_dword v13, v[26:27], off nt
	global_load_dword v14, v[28:29], off nt
	global_load_dword v15, v[30:31], off nt
	global_load_dword v16, v[34:35], off nt
	global_load_dword v17, v[36:37], off nt
	global_load_dword v18, v[74:75], off nt
	global_load_dword v19, v[114:115], off nt
	global_load_dword v20, v[116:117], off nt
	global_load_dword v21, v[118:119], off nt
	global_load_dword v22, v[120:121], off nt
	global_load_dword v23, v[122:123], off nt
	global_load_dword v24, v[124:125], off nt
	global_load_dword v25, v[126:127], off nt
	global_load_dword v26, v[128:129], off nt
	global_load_dword v27, v[130:131], off nt
	global_load_dword v28, v[132:133], off nt
	global_load_dword v29, v[134:135], off nt
	global_load_dword v30, v[136:137], off nt
	global_load_dword v31, v[138:139], off nt
	global_load_dword v32, v40, s[26:27] nt

.LBB0_1905:
	s_ashr_i32 s25, s73, 8
	s_ashr_i32 s30, s25, 31
	s_mul_i32 s21, s25, s21
	s_mul_hi_u32 s31, s25, s20
	s_add_i32 s21, s31, s21
	s_mul_i32 s30, s30, s20
	s_add_i32 s21, s21, s30
	s_mul_i32 s20, s25, s20
	s_lshl_b32 s38, s42, 5
	s_lshl_b64 s[20:21], s[20:21], 8
	s_add_u32 s20, s20, s34
	s_addc_u32 s21, s21, s35
	s_mul_i32 s21, s21, s18
	s_mul_hi_u32 s25, s20, s18
	s_add_i32 s25, s25, s21
	s_mul_i32 s20, s20, s18
	s_add_u32 s20, s36, s20
	s_addc_u32 s21, s37, s25
	s_lshl_b32 s25, s73, 5
	s_and_b32 s25, s25, 0x1fe0
	s_add_u32 s20, s20, s25
	s_addc_u32 s21, s21, 0
	s_ashr_i32 s25, s38, 31
	s_mul_i32 s25, s28, s25
	s_mul_hi_u32 s30, s28, s38
	s_add_i32 s25, s30, s25
	s_mul_i32 s30, s29, s38
	s_add_i32 s31, s25, s30
	s_mul_i32 s30, s28, s38
	s_lshl_b64 s[30:31], s[30:31], 2
	s_add_u32 s26, s26, s30
	s_addc_u32 s27, s27, s31
	s_ashr_i32 s25, s24, 31
	s_lshl_b64 s[24:25], s[24:25], 2
	s_add_u32 s24, s26, s24
	s_addc_u32 s25, s27, s25
	v_lshl_add_u64 v[34:35], s[24:25], 0, v[40:41]
	s_waitcnt vmcnt(0)
	global_load_dword v80, v40, s[24:25] nt
	s_lshl_b64 s[24:25], s[28:29], 2
	v_lshl_add_u64 v[34:35], v[34:35], 0, s[24:25]
	v_lshl_add_u64 v[36:37], v[34:35], 0, s[24:25]
	v_lshl_add_u64 v[74:75], v[36:37], 0, s[24:25]
	s_waitcnt vmcnt(29)
	v_lshl_add_u64 v[84:85], v[74:75], 0, s[24:25]
	s_waitcnt vmcnt(27)
	v_lshl_add_u64 v[86:87], v[84:85], 0, s[24:25]
	s_waitcnt vmcnt(25)
	v_lshl_add_u64 v[88:89], v[86:87], 0, s[24:25]
	s_waitcnt vmcnt(23)
	v_lshl_add_u64 v[90:91], v[88:89], 0, s[24:25]
	global_load_dword v81, v[34:35], off nt
	global_load_dword v82, v[36:37], off nt
	global_load_dword v83, v[74:75], off nt
	s_nop 0
	global_load_dword v84, v[84:85], off nt
	s_nop 0
	global_load_dword v85, v[86:87], off nt
	s_nop 0
	global_load_dword v86, v[88:89], off nt
	global_load_dword v87, v[90:91], off nt
	v_lshl_add_u64 v[34:35], v[90:91], 0, s[24:25]
	global_load_dword v88, v[34:35], off nt
	v_lshl_add_u64 v[34:35], v[34:35], 0, s[24:25]
	global_load_dword v89, v[34:35], off nt
	v_lshl_add_u64 v[34:35], v[34:35], 0, s[24:25]
	global_load_dword v90, v[34:35], off nt
	v_lshl_add_u64 v[34:35], v[34:35], 0, s[24:25]
	global_load_dword v91, v[34:35], off nt
	v_lshl_add_u64 v[34:35], v[34:35], 0, s[24:25]
	global_load_dword v92, v[34:35], off nt
	v_lshl_add_u64 v[34:35], v[34:35], 0, s[24:25]
	global_load_dword v93, v[34:35], off nt
	v_lshl_add_u64 v[34:35], v[34:35], 0, s[24:25]
	global_load_dword v94, v[34:35], off nt
	v_lshl_add_u64 v[34:35], v[34:35], 0, s[24:25]
	global_load_dword v95, v[34:35], off nt
	v_lshl_add_u64 v[34:35], v[34:35], 0, s[24:25]
	global_load_dword v96, v[34:35], off nt
	v_lshl_add_u64 v[34:35], v[34:35], 0, s[24:25]
	global_load_dword v97, v[34:35], off nt
	v_lshl_add_u64 v[34:35], v[34:35], 0, s[24:25]
	global_load_dword v98, v[34:35], off nt
	v_lshl_add_u64 v[34:35], v[34:35], 0, s[24:25]
	global_load_dword v99, v[34:35], off nt
	v_lshl_add_u64 v[34:35], v[34:35], 0, s[24:25]
	global_load_dword v100, v[34:35], off nt
	v_lshl_add_u64 v[34:35], v[34:35], 0, s[24:25]
	global_load_dword v101, v[34:35], off nt
	v_lshl_add_u64 v[34:35], v[34:35], 0, s[24:25]
	global_load_dword v102, v[34:35], off nt
	v_lshl_add_u64 v[34:35], v[34:35], 0, s[24:25]
	global_load_dword v103, v[34:35], off nt
	v_lshl_add_u64 v[34:35], v[34:35], 0, s[24:25]
	global_load_dword v104, v[34:35], off nt
	v_lshl_add_u64 v[34:35], v[34:35], 0, s[24:25]
	global_load_dword v105, v[34:35], off nt
	v_lshl_add_u64 v[34:35], v[34:35], 0, s[24:25]
	global_load_dword v106, v[34:35], off nt
	v_lshl_add_u64 v[34:35], v[34:35], 0, s[24:25]
	global_load_dword v107, v[34:35], off nt
	v_lshl_add_u64 v[34:35], v[34:35], 0, s[24:25]
	global_load_dword v108, v[34:35], off nt
	v_lshl_add_u64 v[34:35], v[34:35], 0, s[24:25]
	global_load_dword v109, v[34:35], off nt
	v_lshl_add_u64 v[34:35], v[34:35], 0, s[24:25]
	global_load_dword v110, v[34:35], off nt
	v_lshl_add_u64 v[34:35], v[34:35], 0, s[24:25]
	global_load_dword v111, v[34:35], off nt
	s_mul_i32 s73, s38, s18

.LBB0_2229:
	s_ashr_i32 s18, s25, 8
	s_ashr_i32 s19, s18, 31
	s_mul_i32 s17, s18, s17
	s_mul_hi_u32 s20, s18, s16
	s_add_i32 s17, s20, s17
	s_mul_i32 s19, s19, s16
	s_add_i32 s17, s17, s19
	s_mul_i32 s16, s18, s16
	s_lshl_b32 s26, s94, 3
	s_lshl_b32 s3, s3, 5
	s_lshl_b64 s[16:17], s[16:17], 8
	s_add_u32 s14, s16, s14
	s_addc_u32 s15, s17, s15
	s_mul_i32 s15, s15, s27
	s_mul_hi_u32 s16, s14, s27
	s_add_i32 s16, s16, s15
	s_mul_i32 s14, s14, s27
	s_add_u32 s0, s0, s14
	s_addc_u32 s1, s1, s16
	s_lshl_b32 s14, s25, 5
	s_and_b32 s14, s14, 0x1fe0
	s_add_u32 s0, s0, s14
	s_addc_u32 s1, s1, 0
	s_ashr_i32 s14, s3, 31
	s_mul_i32 s14, s12, s14
	s_mul_hi_u32 s15, s12, s3
	s_add_i32 s14, s15, s14
	s_mul_i32 s15, s13, s3
	s_add_i32 s15, s14, s15
	s_mul_i32 s14, s12, s3
	s_lshl_b64 s[14:15], s[14:15], 2
	s_add_u32 s10, s10, s14
	s_mul_i32 s54, s3, s27
	s_addc_u32 s11, s11, s15
	s_ashr_i32 s3, s2, 31
	s_lshl_b64 s[2:3], s[2:3], 2
	v_and_b32_e32 v38, 63, v2
	s_add_u32 s2, s10, s2
	v_mov_b32_e32 v39, 0
	s_addc_u32 s3, s11, s3
	v_lshlrev_b32_e32 v40, 2, v38
	v_mov_b32_e32 v41, v39
	v_lshl_add_u64 v[2:3], s[2:3], 0, v[40:41]
	s_lshl_b64 s[10:11], s[12:13], 2
	v_lshl_add_u64 v[2:3], v[2:3], 0, s[10:11]
	v_lshl_add_u64 v[4:5], v[2:3], 0, s[10:11]
	v_lshl_add_u64 v[6:7], v[4:5], 0, s[10:11]
	v_lshl_add_u64 v[8:9], v[6:7], 0, s[10:11]
	v_lshl_add_u64 v[10:11], v[8:9], 0, s[10:11]
	v_lshl_add_u64 v[12:13], v[10:11], 0, s[10:11]
	v_lshl_add_u64 v[14:15], v[12:13], 0, s[10:11]
	v_lshl_add_u64 v[16:17], v[14:15], 0, s[10:11]
	v_lshl_add_u64 v[18:19], v[16:17], 0, s[10:11]
	v_lshl_add_u64 v[20:21], v[18:19], 0, s[10:11]
	v_lshl_add_u64 v[22:23], v[20:21], 0, s[10:11]
	v_lshl_add_u64 v[24:25], v[22:23], 0, s[10:11]
	v_lshl_add_u64 v[26:27], v[24:25], 0, s[10:11]
	v_lshl_add_u64 v[28:29], v[26:27], 0, s[10:11]
	v_lshl_add_u64 v[30:31], v[28:29], 0, s[10:11]
	v_lshl_add_u64 v[32:33], v[30:31], 0, s[10:11]
	v_lshl_add_u64 v[34:35], v[32:33], 0, s[10:11]
	v_lshl_add_u64 v[36:37], v[34:35], 0, s[10:11]
	v_lshl_add_u64 v[42:43], v[36:37], 0, s[10:11]
	v_lshl_add_u64 v[44:45], v[42:43], 0, s[10:11]
	v_lshl_add_u64 v[46:47], v[44:45], 0, s[10:11]
	v_lshl_add_u64 v[48:49], v[46:47], 0, s[10:11]
	v_lshl_add_u64 v[50:51], v[48:49], 0, s[10:11]
	v_lshl_add_u64 v[52:53], v[50:51], 0, s[10:11]
	v_lshl_add_u64 v[54:55], v[52:53], 0, s[10:11]
	v_lshl_add_u64 v[56:57], v[54:55], 0, s[10:11]
	v_lshl_add_u64 v[58:59], v[56:57], 0, s[10:11]
	v_lshl_add_u64 v[60:61], v[58:59], 0, s[10:11]
	v_lshl_add_u64 v[62:63], v[60:61], 0, s[10:11]
	v_lshl_add_u64 v[64:65], v[62:63], 0, s[10:11]
	v_lshl_add_u64 v[66:67], v[64:65], 0, s[10:11]
	s_waitcnt vmcnt(0)
	global_load_dword v1, v[2:3], off nt
	s_nop 0
	global_load_dword v2, v[4:5], off nt
	global_load_dword v3, v[6:7], off nt
	s_nop 0
	global_load_dword v4, v[8:9], off nt
	global_load_dword v5, v[10:11], off nt
	global_load_dword v6, v[12:13], off nt
	global_load_dword v7, v[14:15], off nt
	s_nop 0
	global_load_dword v8, v[16:17], off nt
	global_load_dword v9, v[18:19], off nt
	global_load_dword v10, v[20:21], off nt
	global_load_dword v11, v[22:23], off nt
	global_load_dword v12, v[24:25], off nt
	global_load_dword v13, v[26:27], off nt
	global_load_dword v14, v[28:29], off nt
	global_load_dword v15, v[30:31], off nt
	global_load_dword v16, v[32:33], off nt
	global_load_dword v17, v[34:35], off nt
	global_load_dword v18, v[36:37], off nt
	global_load_dword v19, v[42:43], off nt
	global_load_dword v20, v[44:45], off nt
	global_load_dword v21, v[46:47], off nt
	global_load_dword v22, v[48:49], off nt
	global_load_dword v23, v[50:51], off nt
	global_load_dword v24, v[52:53], off nt
	global_load_dword v25, v[54:55], off nt
	global_load_dword v26, v[56:57], off nt
	global_load_dword v27, v[58:59], off nt
	global_load_dword v28, v[60:61], off nt
	global_load_dword v29, v[62:63], off nt
	global_load_dword v30, v[64:65], off nt
	global_load_dword v31, v[66:67], off nt
	global_load_dword v32, v40, s[2:3] nt
	s_add_i32 s27, s24, s26
	s_cmp_gt_i32 s27, 0x2c1ff
	s_mov_b64 s[24:25], s[0:1]
	s_mov_b32 s74, s54
	s_mov_b32 s53, s51
	s_waitcnt lgkmcnt(0)
	v_mov_b32_e32 v79, v73
	s_mov_b32 s55, s52
	s_cbranch_scc1 .LBB0_2289
	s_cmpk_gt_i32 s27, 0x17ff
	s_cbranch_scc0 .LBB0_2240
	s_cmpk_gt_u32 s27, 0x1fff
	s_cbranch_scc0 .LBB0_2243
	s_cmpk_gt_u32 s27, 0x35ff
	s_cbranch_scc0 .LBB0_2244
	s_cmpk_gt_u32 s27, 0x4bff
	s_cbranch_scc0 .LBB0_2245
	s_cmpk_gt_u32 s27, 0x61ff
	s_cbranch_scc0 .LBB0_2246
	s_cmpk_gt_u32 s27, 0x79ff
	s_cbranch_scc0 .LBB0_2247
	s_cmpk_gt_u32 s27, 0x81ff
	s_cbranch_scc0 .LBB0_2248
	s_cmp_gt_u32 s27, 0x161ff
	s_cbranch_scc0 .LBB0_2249
	s_cmp_gt_u32 s27, 0x241ff
	s_mov_b64 s[20:21], -1
	s_cbranch_scc0 .LBB0_2250
	s_add_i32 s2, s27, 0xbe00
	s_bfe_u32 s3, s2, 0x6000a
	s_mulk_i32 s3, 0x2493
	s_lshr_b32 s14, s3, 16
	s_mul_i32 s3, s14, 0x1c00
	s_sub_i32 s2, s2, s3
	s_and_b32 s10, s2, 0xffff
	s_bfe_u32 s3, s2, 0xb0005
	s_lshl_b32 s2, s10, 6
	s_and_b32 s2, s2, 0x7c0
	s_mul_i32 s10, s14, 0x3800000
	v_readlane_b32 s28, v254, 0
	v_readlane_b32 s29, v254, 1
	s_add_u32 s10, s28, s10
	s_addc_u32 s11, s29, 0
	s_add_u32 s12, s96, 0x24a00000
	s_mov_b32 s17, 0
	v_readlane_b32 s30, v254, 2
	v_readlane_b32 s31, v254, 3
	s_addc_u32 s13, s97, 0
	s_mul_i32 s16, s14, 0xe00000
	s_mov_b64 s[14:15], 0
	s_branch .LBB0_2251

.LBB0_2288:
	s_lshl_b32 s20, s3, 5
	s_ashr_i32 s3, s28, 8
	s_ashr_i32 s21, s3, 31
	s_mul_i32 s19, s3, s19
	s_mul_hi_u32 s22, s3, s18
	s_add_i32 s19, s22, s19
	s_mul_i32 s21, s21, s18
	s_add_i32 s19, s19, s21
	s_mul_i32 s18, s3, s18
	s_lshl_b64 s[18:19], s[18:19], 8
	s_add_u32 s3, s18, s16
	s_addc_u32 s16, s19, s17
	s_mul_i32 s16, s16, s30
	s_mul_hi_u32 s17, s3, s30
	s_add_i32 s17, s17, s16
	s_mul_i32 s3, s3, s30
	s_add_u32 s3, s12, s3
	s_addc_u32 s12, s13, s17
	s_lshl_b32 s13, s28, 5
	s_and_b32 s13, s13, 0x1fe0
	s_add_u32 s24, s3, s13
	s_addc_u32 s25, s12, 0
	s_ashr_i32 s3, s20, 31
	s_mul_i32 s3, s14, s3
	s_mul_hi_u32 s12, s14, s20
	s_add_i32 s3, s12, s3
	s_mul_i32 s12, s15, s20
	s_add_i32 s13, s3, s12
	s_mul_i32 s12, s14, s20
	s_lshl_b64 s[12:13], s[12:13], 2
	s_add_u32 s10, s10, s12
	s_addc_u32 s11, s11, s13
	s_ashr_i32 s3, s2, 31
	s_lshl_b64 s[2:3], s[2:3], 2
	s_add_u32 s2, s10, s2
	s_addc_u32 s3, s11, s3
	v_mov_b32_e32 v41, 0
	v_lshl_add_u64 v[34:35], s[2:3], 0, v[40:41]
	s_waitcnt vmcnt(0)
	global_load_dword v80, v40, s[2:3] nt
	s_lshl_b64 s[2:3], s[14:15], 2
	v_lshl_add_u64 v[34:35], v[34:35], 0, s[2:3]
	v_lshl_add_u64 v[36:37], v[34:35], 0, s[2:3]
	v_lshl_add_u64 v[42:43], v[36:37], 0, s[2:3]
	v_lshl_add_u64 v[44:45], v[42:43], 0, s[2:3]
	v_lshl_add_u64 v[46:47], v[44:45], 0, s[2:3]
	v_lshl_add_u64 v[48:49], v[46:47], 0, s[2:3]
	v_lshl_add_u64 v[50:51], v[48:49], 0, s[2:3]
	global_load_dword v81, v[34:35], off nt
	global_load_dword v82, v[36:37], off nt
	global_load_dword v83, v[42:43], off nt
	global_load_dword v84, v[44:45], off nt
	global_load_dword v85, v[46:47], off nt
	global_load_dword v86, v[48:49], off nt
	global_load_dword v87, v[50:51], off nt
	v_lshl_add_u64 v[34:35], v[50:51], 0, s[2:3]
	global_load_dword v88, v[34:35], off nt
	v_lshl_add_u64 v[34:35], v[34:35], 0, s[2:3]
	global_load_dword v89, v[34:35], off nt
	v_lshl_add_u64 v[34:35], v[34:35], 0, s[2:3]
	global_load_dword v90, v[34:35], off nt
	v_lshl_add_u64 v[34:35], v[34:35], 0, s[2:3]
	global_load_dword v91, v[34:35], off nt
	v_lshl_add_u64 v[34:35], v[34:35], 0, s[2:3]
	global_load_dword v92, v[34:35], off nt
	v_lshl_add_u64 v[34:35], v[34:35], 0, s[2:3]
	global_load_dword v93, v[34:35], off nt
	v_lshl_add_u64 v[34:35], v[34:35], 0, s[2:3]
	global_load_dword v94, v[34:35], off nt
	v_lshl_add_u64 v[34:35], v[34:35], 0, s[2:3]
	global_load_dword v95, v[34:35], off nt
	v_lshl_add_u64 v[34:35], v[34:35], 0, s[2:3]
	global_load_dword v96, v[34:35], off nt
	v_lshl_add_u64 v[34:35], v[34:35], 0, s[2:3]
	global_load_dword v97, v[34:35], off nt
	v_lshl_add_u64 v[34:35], v[34:35], 0, s[2:3]
	global_load_dword v98, v[34:35], off nt
	v_lshl_add_u64 v[34:35], v[34:35], 0, s[2:3]
	global_load_dword v99, v[34:35], off nt
	v_lshl_add_u64 v[34:35], v[34:35], 0, s[2:3]
	global_load_dword v100, v[34:35], off nt
	v_lshl_add_u64 v[34:35], v[34:35], 0, s[2:3]
	global_load_dword v101, v[34:35], off nt
	v_lshl_add_u64 v[34:35], v[34:35], 0, s[2:3]
	global_load_dword v102, v[34:35], off nt
	v_lshl_add_u64 v[34:35], v[34:35], 0, s[2:3]
	global_load_dword v103, v[34:35], off nt
	v_lshl_add_u64 v[34:35], v[34:35], 0, s[2:3]
	global_load_dword v104, v[34:35], off nt
	v_lshl_add_u64 v[34:35], v[34:35], 0, s[2:3]
	global_load_dword v105, v[34:35], off nt
	v_lshl_add_u64 v[34:35], v[34:35], 0, s[2:3]
	global_load_dword v106, v[34:35], off nt
	v_lshl_add_u64 v[34:35], v[34:35], 0, s[2:3]
	global_load_dword v107, v[34:35], off nt
	v_lshl_add_u64 v[34:35], v[34:35], 0, s[2:3]
	global_load_dword v108, v[34:35], off nt
	v_lshl_add_u64 v[34:35], v[34:35], 0, s[2:3]
	global_load_dword v109, v[34:35], off nt
	v_lshl_add_u64 v[34:35], v[34:35], 0, s[2:3]
	global_load_dword v110, v[34:35], off nt
	v_lshl_add_u64 v[34:35], v[34:35], 0, s[2:3]
	global_load_dword v111, v[34:35], off nt
	s_mul_i32 s74, s20, s30

.LBB0_2342:
	s_ashr_i32 s31, s77, 8
	s_ashr_i32 s38, s31, 31
	s_mul_i32 s27, s31, s27
	s_mul_hi_u32 s39, s31, s26
	s_add_i32 s27, s39, s27
	s_mul_i32 s38, s38, s26
	s_add_i32 s27, s27, s38
	s_mul_i32 s26, s31, s26
	s_lshl_b32 s44, s75, 5
	s_lshl_b64 s[26:27], s[26:27], 8
	s_add_u32 s26, s26, s40
	s_addc_u32 s27, s27, s41
	s_mul_i32 s27, s27, s22
	s_mul_hi_u32 s31, s26, s22
	s_add_i32 s31, s31, s27
	s_mul_i32 s26, s26, s22
	s_add_u32 s26, s42, s26
	s_addc_u32 s27, s43, s31
	s_lshl_b32 s31, s77, 5
	s_and_b32 s31, s31, 0x1fe0
	s_add_u32 s26, s26, s31
	s_addc_u32 s27, s27, 0
	s_ashr_i32 s31, s44, 31
	s_mul_i32 s31, s36, s31
	s_mul_hi_u32 s38, s36, s44
	s_add_i32 s31, s38, s31
	s_mul_i32 s38, s37, s44
	s_add_i32 s39, s31, s38
	s_mul_i32 s38, s36, s44
	s_lshl_b64 s[38:39], s[38:39], 2
	s_add_u32 s34, s34, s38
	s_addc_u32 s35, s35, s39
	s_ashr_i32 s31, s30, 31
	s_lshl_b64 s[30:31], s[30:31], 2
	s_add_u32 s30, s34, s30
	s_addc_u32 s31, s35, s31
	v_lshl_add_u64 v[34:35], s[30:31], 0, v[40:41]
	s_waitcnt vmcnt(0)
	global_load_dword v42, v40, s[30:31] nt
	s_lshl_b64 s[30:31], s[36:37], 2
	v_lshl_add_u64 v[34:35], v[34:35], 0, s[30:31]
	v_lshl_add_u64 v[36:37], v[34:35], 0, s[30:31]
	s_waitcnt vmcnt(26)
	v_lshl_add_u64 v[46:47], v[36:37], 0, s[30:31]
	s_waitcnt vmcnt(23)
	v_lshl_add_u64 v[48:49], v[46:47], 0, s[30:31]
	s_waitcnt vmcnt(22)
	v_lshl_add_u64 v[50:51], v[48:49], 0, s[30:31]
	s_waitcnt vmcnt(19)
	v_lshl_add_u64 v[52:53], v[50:51], 0, s[30:31]
	s_waitcnt vmcnt(18)
	v_lshl_add_u64 v[54:55], v[52:53], 0, s[30:31]
	global_load_dword v44, v[34:35], off nt
	global_load_dword v33, v[36:37], off nt
	global_load_dword v43, v[46:47], off nt
	s_nop 0
	global_load_dword v46, v[48:49], off nt
	s_nop 0
	global_load_dword v48, v[50:51], off nt
	global_load_dword v45, v[52:53], off nt
	global_load_dword v47, v[54:55], off nt
	v_lshl_add_u64 v[34:35], v[54:55], 0, s[30:31]
	global_load_dword v50, v[34:35], off nt
	v_lshl_add_u64 v[34:35], v[34:35], 0, s[30:31]
	global_load_dword v52, v[34:35], off nt
	v_lshl_add_u64 v[34:35], v[34:35], 0, s[30:31]
	global_load_dword v49, v[34:35], off nt
	v_lshl_add_u64 v[34:35], v[34:35], 0, s[30:31]
	global_load_dword v51, v[34:35], off nt
	v_lshl_add_u64 v[34:35], v[34:35], 0, s[30:31]
	global_load_dword v54, v[34:35], off nt
	v_lshl_add_u64 v[34:35], v[34:35], 0, s[30:31]
	global_load_dword v56, v[34:35], off nt
	v_lshl_add_u64 v[34:35], v[34:35], 0, s[30:31]
	global_load_dword v53, v[34:35], off nt
	v_lshl_add_u64 v[34:35], v[34:35], 0, s[30:31]
	global_load_dword v55, v[34:35], off nt
	v_lshl_add_u64 v[34:35], v[34:35], 0, s[30:31]
	global_load_dword v58, v[34:35], off nt
	v_lshl_add_u64 v[34:35], v[34:35], 0, s[30:31]
	global_load_dword v60, v[34:35], off nt
	v_lshl_add_u64 v[34:35], v[34:35], 0, s[30:31]
	global_load_dword v57, v[34:35], off nt
	v_lshl_add_u64 v[34:35], v[34:35], 0, s[30:31]
	global_load_dword v59, v[34:35], off nt
	v_lshl_add_u64 v[34:35], v[34:35], 0, s[30:31]
	global_load_dword v62, v[34:35], off nt
	v_lshl_add_u64 v[34:35], v[34:35], 0, s[30:31]
	global_load_dword v64, v[34:35], off nt
	v_lshl_add_u64 v[34:35], v[34:35], 0, s[30:31]
	global_load_dword v61, v[34:35], off nt
	v_lshl_add_u64 v[34:35], v[34:35], 0, s[30:31]
	global_load_dword v63, v[34:35], off nt
	v_lshl_add_u64 v[34:35], v[34:35], 0, s[30:31]
	global_load_dword v66, v[34:35], off nt
	v_lshl_add_u64 v[34:35], v[34:35], 0, s[30:31]
	global_load_dword v68, v[34:35], off nt
	v_lshl_add_u64 v[34:35], v[34:35], 0, s[30:31]
	global_load_dword v65, v[34:35], off nt
	v_lshl_add_u64 v[34:35], v[34:35], 0, s[30:31]
	global_load_dword v67, v[34:35], off nt
	v_lshl_add_u64 v[34:35], v[34:35], 0, s[30:31]
	global_load_dword v70, v[34:35], off nt
	v_lshl_add_u64 v[34:35], v[34:35], 0, s[30:31]
	global_load_dword v72, v[34:35], off nt
	v_lshl_add_u64 v[34:35], v[34:35], 0, s[30:31]
	global_load_dword v69, v[34:35], off nt
	v_lshl_add_u64 v[34:35], v[34:35], 0, s[30:31]
	global_load_dword v71, v[34:35], off nt
	s_mul_i32 s75, s44, s22

.LBB0_2407:
	s_ashr_i32 s38, s77, 8
	s_ashr_i32 s39, s38, 31
	s_mul_i32 s1, s38, s1
	s_mul_hi_u32 s44, s38, s0
	s_add_i32 s1, s44, s1
	s_mul_i32 s39, s39, s0
	s_add_i32 s1, s1, s39
	s_mul_i32 s0, s38, s0
	s_lshl_b32 s31, s54, 5
	s_lshl_b64 s[0:1], s[0:1], 8
	s_add_u32 s0, s0, s40
	s_addc_u32 s1, s1, s41
	s_mul_i32 s1, s1, s22
	s_mul_hi_u32 s38, s0, s22
	s_add_i32 s38, s38, s1
	s_mul_i32 s0, s0, s22
	s_add_u32 s0, s42, s0
	s_mul_i32 s54, s31, s22
	s_addc_u32 s1, s43, s38
	s_lshl_b32 s22, s77, 5
	s_and_b32 s22, s22, 0x1fe0
	s_add_u32 s0, s0, s22
	s_addc_u32 s1, s1, 0
	s_ashr_i32 s22, s31, 31
	s_mul_i32 s22, s36, s22
	s_mul_hi_u32 s38, s36, s31
	s_add_i32 s22, s38, s22
	s_mul_i32 s38, s37, s31
	s_add_i32 s39, s22, s38
	s_mul_i32 s38, s36, s31
	s_lshl_b64 s[38:39], s[38:39], 2
	s_add_u32 s22, s34, s38
	s_addc_u32 s34, s35, s39
	s_ashr_i32 s31, s30, 31
	s_lshl_b64 s[30:31], s[30:31], 2
	s_add_u32 s30, s22, s30
	s_addc_u32 s31, s34, s31
	s_waitcnt vmcnt(30)
	v_lshl_add_u64 v[2:3], s[30:31], 0, v[40:41]
	s_lshl_b64 s[34:35], s[36:37], 2
	v_lshl_add_u64 v[2:3], v[2:3], 0, s[34:35]
	s_waitcnt vmcnt(28)
	v_lshl_add_u64 v[4:5], v[2:3], 0, s[34:35]
	s_waitcnt vmcnt(26)
	v_lshl_add_u64 v[6:7], v[4:5], 0, s[34:35]
	s_waitcnt vmcnt(24)
	v_lshl_add_u64 v[8:9], v[6:7], 0, s[34:35]
	s_waitcnt vmcnt(22)
	v_lshl_add_u64 v[10:11], v[8:9], 0, s[34:35]
	s_waitcnt vmcnt(20)
	v_lshl_add_u64 v[12:13], v[10:11], 0, s[34:35]
	s_waitcnt vmcnt(18)
	v_lshl_add_u64 v[14:15], v[12:13], 0, s[34:35]
	s_waitcnt vmcnt(16)
	v_lshl_add_u64 v[16:17], v[14:15], 0, s[34:35]
	s_waitcnt vmcnt(14)
	v_lshl_add_u64 v[18:19], v[16:17], 0, s[34:35]
	s_waitcnt vmcnt(12)
	v_lshl_add_u64 v[20:21], v[18:19], 0, s[34:35]
	s_waitcnt vmcnt(10)
	v_lshl_add_u64 v[22:23], v[20:21], 0, s[34:35]
	s_waitcnt vmcnt(8)
	v_lshl_add_u64 v[24:25], v[22:23], 0, s[34:35]
	s_waitcnt vmcnt(6)
	v_lshl_add_u64 v[26:27], v[24:25], 0, s[34:35]
	s_waitcnt vmcnt(4)
	v_lshl_add_u64 v[28:29], v[26:27], 0, s[34:35]
	s_waitcnt vmcnt(2)
	v_lshl_add_u64 v[30:31], v[28:29], 0, s[34:35]
	v_lshl_add_u64 v[34:35], v[30:31], 0, s[34:35]
	v_lshl_add_u64 v[36:37], v[34:35], 0, s[34:35]
	v_lshl_add_u64 v[74:75], v[36:37], 0, s[34:35]
	v_lshl_add_u64 v[114:115], v[74:75], 0, s[34:35]
	v_lshl_add_u64 v[116:117], v[114:115], 0, s[34:35]
	v_lshl_add_u64 v[118:119], v[116:117], 0, s[34:35]
	v_lshl_add_u64 v[120:121], v[118:119], 0, s[34:35]
	v_lshl_add_u64 v[122:123], v[120:121], 0, s[34:35]
	v_lshl_add_u64 v[124:125], v[122:123], 0, s[34:35]
	v_lshl_add_u64 v[126:127], v[124:125], 0, s[34:35]
	v_lshl_add_u64 v[128:129], v[126:127], 0, s[34:35]
	v_lshl_add_u64 v[130:131], v[128:129], 0, s[34:35]
	v_lshl_add_u64 v[132:133], v[130:131], 0, s[34:35]
	v_lshl_add_u64 v[134:135], v[132:133], 0, s[34:35]
	v_lshl_add_u64 v[136:137], v[134:135], 0, s[34:35]
	v_lshl_add_u64 v[138:139], v[136:137], 0, s[34:35]
	s_waitcnt vmcnt(0)
	global_load_dword v1, v[2:3], off nt
	s_nop 0
	global_load_dword v2, v[4:5], off nt
	global_load_dword v3, v[6:7], off nt
	s_nop 0
	global_load_dword v4, v[8:9], off nt
	global_load_dword v5, v[10:11], off nt
	global_load_dword v6, v[12:13], off nt
	global_load_dword v7, v[14:15], off nt
	s_nop 0
	global_load_dword v8, v[16:17], off nt
	global_load_dword v9, v[18:19], off nt
	global_load_dword v10, v[20:21], off nt
	global_load_dword v11, v[22:23], off nt
	global_load_dword v12, v[24:25], off nt
	global_load_dword v13, v[26:27], off nt
	global_load_dword v14, v[28:29], off nt
	global_load_dword v15, v[30:31], off nt
	global_load_dword v16, v[34:35], off nt
	global_load_dword v17, v[36:37], off nt
	global_load_dword v18, v[74:75], off nt
	global_load_dword v19, v[114:115], off nt
	global_load_dword v20, v[116:117], off nt
	global_load_dword v21, v[118:119], off nt
	global_load_dword v22, v[120:121], off nt
	global_load_dword v23, v[122:123], off nt
	global_load_dword v24, v[124:125], off nt
	global_load_dword v25, v[126:127], off nt
	global_load_dword v26, v[128:129], off nt
	global_load_dword v27, v[130:131], off nt
	global_load_dword v28, v[132:133], off nt
	global_load_dword v29, v[134:135], off nt
	global_load_dword v30, v[136:137], off nt
	global_load_dword v31, v[138:139], off nt
	global_load_dword v32, v40, s[30:31] nt

.LBB0_2473:
	s_ashr_i32 s29, s74, 8
	s_ashr_i32 s36, s29, 31
	s_mul_i32 s25, s29, s25
	s_mul_hi_u32 s37, s29, s24
	s_add_i32 s25, s37, s25
	s_mul_i32 s36, s36, s24
	s_add_i32 s25, s25, s36
	s_mul_i32 s24, s29, s24
	s_lshl_b32 s42, s46, 5
	s_lshl_b64 s[24:25], s[24:25], 8
	s_add_u32 s24, s24, s38
	s_addc_u32 s25, s25, s39
	s_mul_i32 s25, s25, s22
	s_mul_hi_u32 s29, s24, s22
	s_add_i32 s29, s29, s25
	s_mul_i32 s24, s24, s22
	s_add_u32 s24, s40, s24
	s_addc_u32 s25, s41, s29
	s_lshl_b32 s29, s74, 5
	s_and_b32 s29, s29, 0x1fe0
	s_add_u32 s24, s24, s29
	s_addc_u32 s25, s25, 0
	s_ashr_i32 s29, s42, 31
	s_mul_i32 s29, s34, s29
	s_mul_hi_u32 s36, s34, s42
	s_add_i32 s29, s36, s29
	s_mul_i32 s36, s35, s42
	s_add_i32 s37, s29, s36
	s_mul_i32 s36, s34, s42
	s_lshl_b64 s[36:37], s[36:37], 2
	s_add_u32 s30, s30, s36
	s_addc_u32 s31, s31, s37
	s_ashr_i32 s29, s28, 31
	s_lshl_b64 s[28:29], s[28:29], 2
	s_add_u32 s28, s30, s28
	s_addc_u32 s29, s31, s29
	v_lshl_add_u64 v[34:35], s[28:29], 0, v[40:41]
	s_waitcnt vmcnt(0)
	global_load_dword v80, v40, s[28:29] nt
	s_lshl_b64 s[28:29], s[34:35], 2
	v_lshl_add_u64 v[34:35], v[34:35], 0, s[28:29]
	v_lshl_add_u64 v[36:37], v[34:35], 0, s[28:29]
	v_lshl_add_u64 v[74:75], v[36:37], 0, s[28:29]
	s_waitcnt vmcnt(29)
	v_lshl_add_u64 v[84:85], v[74:75], 0, s[28:29]
	s_waitcnt vmcnt(27)
	v_lshl_add_u64 v[86:87], v[84:85], 0, s[28:29]
	s_waitcnt vmcnt(25)
	v_lshl_add_u64 v[88:89], v[86:87], 0, s[28:29]
	s_waitcnt vmcnt(23)
	v_lshl_add_u64 v[90:91], v[88:89], 0, s[28:29]
	global_load_dword v81, v[34:35], off nt
	global_load_dword v82, v[36:37], off nt
	global_load_dword v83, v[74:75], off nt
	s_nop 0
	global_load_dword v84, v[84:85], off nt
	s_nop 0
	global_load_dword v85, v[86:87], off nt
	s_nop 0
	global_load_dword v86, v[88:89], off nt
	global_load_dword v87, v[90:91], off nt
	v_lshl_add_u64 v[34:35], v[90:91], 0, s[28:29]
	global_load_dword v88, v[34:35], off nt
	v_lshl_add_u64 v[34:35], v[34:35], 0, s[28:29]
	global_load_dword v89, v[34:35], off nt
	v_lshl_add_u64 v[34:35], v[34:35], 0, s[28:29]
	global_load_dword v90, v[34:35], off nt
	v_lshl_add_u64 v[34:35], v[34:35], 0, s[28:29]
	global_load_dword v91, v[34:35], off nt
	v_lshl_add_u64 v[34:35], v[34:35], 0, s[28:29]
	global_load_dword v92, v[34:35], off nt
	v_lshl_add_u64 v[34:35], v[34:35], 0, s[28:29]
	global_load_dword v93, v[34:35], off nt
	v_lshl_add_u64 v[34:35], v[34:35], 0, s[28:29]
	global_load_dword v94, v[34:35], off nt
	v_lshl_add_u64 v[34:35], v[34:35], 0, s[28:29]
	global_load_dword v95, v[34:35], off nt
	v_lshl_add_u64 v[34:35], v[34:35], 0, s[28:29]
	global_load_dword v96, v[34:35], off nt
	v_lshl_add_u64 v[34:35], v[34:35], 0, s[28:29]
	global_load_dword v97, v[34:35], off nt
	v_lshl_add_u64 v[34:35], v[34:35], 0, s[28:29]
	global_load_dword v98, v[34:35], off nt
	v_lshl_add_u64 v[34:35], v[34:35], 0, s[28:29]
	global_load_dword v99, v[34:35], off nt
	v_lshl_add_u64 v[34:35], v[34:35], 0, s[28:29]
	global_load_dword v100, v[34:35], off nt
	v_lshl_add_u64 v[34:35], v[34:35], 0, s[28:29]
	global_load_dword v101, v[34:35], off nt
	v_lshl_add_u64 v[34:35], v[34:35], 0, s[28:29]
	global_load_dword v102, v[34:35], off nt
	v_lshl_add_u64 v[34:35], v[34:35], 0, s[28:29]
	global_load_dword v103, v[34:35], off nt
	v_lshl_add_u64 v[34:35], v[34:35], 0, s[28:29]
	global_load_dword v104, v[34:35], off nt
	v_lshl_add_u64 v[34:35], v[34:35], 0, s[28:29]
	global_load_dword v105, v[34:35], off nt
	v_lshl_add_u64 v[34:35], v[34:35], 0, s[28:29]
	global_load_dword v106, v[34:35], off nt
	v_lshl_add_u64 v[34:35], v[34:35], 0, s[28:29]
	global_load_dword v107, v[34:35], off nt
	v_lshl_add_u64 v[34:35], v[34:35], 0, s[28:29]
	global_load_dword v108, v[34:35], off nt
	v_lshl_add_u64 v[34:35], v[34:35], 0, s[28:29]
	global_load_dword v109, v[34:35], off nt
	v_lshl_add_u64 v[34:35], v[34:35], 0, s[28:29]
	global_load_dword v110, v[34:35], off nt
	v_lshl_add_u64 v[34:35], v[34:35], 0, s[28:29]
	global_load_dword v111, v[34:35], off nt
	s_mul_i32 s74, s42, s22

.LBB0_2949:
	s_ashr_i32 s12, s19, 8
	s_ashr_i32 s13, s12, 31
	s_mul_i32 s11, s12, s11
	s_mul_hi_u32 s14, s12, s10
	s_add_i32 s11, s14, s11
	s_mul_i32 s13, s13, s10
	s_add_i32 s11, s11, s13
	s_mul_i32 s10, s12, s10
	s_lshl_b32 s22, s94, 3
	s_lshl_b32 s3, s3, 5
	s_lshl_b64 s[10:11], s[10:11], 8
	s_add_u32 s8, s10, s8
	s_addc_u32 s9, s11, s9
	s_mul_i32 s9, s9, s21
	s_mul_hi_u32 s10, s8, s21
	s_add_i32 s10, s10, s9
	s_mul_i32 s8, s8, s21
	s_add_u32 s0, s0, s8
	s_addc_u32 s1, s1, s10
	s_lshl_b32 s8, s19, 5
	s_and_b32 s8, s8, 0x1fe0
	s_add_u32 s0, s0, s8
	s_addc_u32 s1, s1, 0
	s_ashr_i32 s8, s3, 31
	s_mul_i32 s8, s6, s8
	s_mul_hi_u32 s9, s6, s3
	s_add_i32 s8, s9, s8
	s_mul_i32 s9, s7, s3
	s_add_i32 s9, s8, s9
	s_mul_i32 s8, s6, s3
	s_lshl_b64 s[8:9], s[8:9], 2
	s_add_u32 s4, s4, s8
	s_mul_i32 s48, s3, s21
	s_addc_u32 s5, s5, s9
	s_ashr_i32 s3, s2, 31
	s_lshl_b64 s[2:3], s[2:3], 2
	v_and_b32_e32 v38, 63, v2
	s_add_u32 s2, s4, s2
	v_mov_b32_e32 v39, 0
	s_addc_u32 s3, s5, s3
	v_lshlrev_b32_e32 v40, 2, v38
	v_mov_b32_e32 v41, v39
	v_lshl_add_u64 v[2:3], s[2:3], 0, v[40:41]
	s_lshl_b64 s[4:5], s[6:7], 2
	v_lshl_add_u64 v[2:3], v[2:3], 0, s[4:5]
	v_lshl_add_u64 v[4:5], v[2:3], 0, s[4:5]
	v_lshl_add_u64 v[6:7], v[4:5], 0, s[4:5]
	v_lshl_add_u64 v[8:9], v[6:7], 0, s[4:5]
	v_lshl_add_u64 v[10:11], v[8:9], 0, s[4:5]
	v_lshl_add_u64 v[12:13], v[10:11], 0, s[4:5]
	v_lshl_add_u64 v[14:15], v[12:13], 0, s[4:5]
	v_lshl_add_u64 v[16:17], v[14:15], 0, s[4:5]
	v_lshl_add_u64 v[18:19], v[16:17], 0, s[4:5]
	v_lshl_add_u64 v[20:21], v[18:19], 0, s[4:5]
	v_lshl_add_u64 v[22:23], v[20:21], 0, s[4:5]
	v_lshl_add_u64 v[24:25], v[22:23], 0, s[4:5]
	v_lshl_add_u64 v[26:27], v[24:25], 0, s[4:5]
	v_lshl_add_u64 v[28:29], v[26:27], 0, s[4:5]
	v_lshl_add_u64 v[30:31], v[28:29], 0, s[4:5]
	v_lshl_add_u64 v[32:33], v[30:31], 0, s[4:5]
	v_lshl_add_u64 v[34:35], v[32:33], 0, s[4:5]
	v_lshl_add_u64 v[36:37], v[34:35], 0, s[4:5]
	v_lshl_add_u64 v[42:43], v[36:37], 0, s[4:5]
	v_lshl_add_u64 v[44:45], v[42:43], 0, s[4:5]
	v_lshl_add_u64 v[46:47], v[44:45], 0, s[4:5]
	v_lshl_add_u64 v[48:49], v[46:47], 0, s[4:5]
	v_lshl_add_u64 v[50:51], v[48:49], 0, s[4:5]
	v_lshl_add_u64 v[52:53], v[50:51], 0, s[4:5]
	v_lshl_add_u64 v[54:55], v[52:53], 0, s[4:5]
	v_lshl_add_u64 v[56:57], v[54:55], 0, s[4:5]
	v_lshl_add_u64 v[58:59], v[56:57], 0, s[4:5]
	v_lshl_add_u64 v[60:61], v[58:59], 0, s[4:5]
	v_lshl_add_u64 v[62:63], v[60:61], 0, s[4:5]
	v_lshl_add_u64 v[64:65], v[62:63], 0, s[4:5]
	v_lshl_add_u64 v[66:67], v[64:65], 0, s[4:5]
	s_waitcnt vmcnt(0)
	global_load_dword v1, v[2:3], off nt
	s_nop 0
	global_load_dword v2, v[4:5], off nt
	global_load_dword v3, v[6:7], off nt
	s_nop 0
	global_load_dword v4, v[8:9], off nt
	global_load_dword v5, v[10:11], off nt
	global_load_dword v6, v[12:13], off nt
	global_load_dword v7, v[14:15], off nt
	s_nop 0
	global_load_dword v8, v[16:17], off nt
	global_load_dword v9, v[18:19], off nt
	global_load_dword v10, v[20:21], off nt
	global_load_dword v11, v[22:23], off nt
	global_load_dword v12, v[24:25], off nt
	global_load_dword v13, v[26:27], off nt
	global_load_dword v14, v[28:29], off nt
	global_load_dword v15, v[30:31], off nt
	global_load_dword v16, v[32:33], off nt
	global_load_dword v17, v[34:35], off nt
	global_load_dword v18, v[36:37], off nt
	global_load_dword v19, v[42:43], off nt
	global_load_dword v20, v[44:45], off nt
	global_load_dword v21, v[46:47], off nt
	global_load_dword v22, v[48:49], off nt
	global_load_dword v23, v[50:51], off nt
	global_load_dword v24, v[52:53], off nt
	global_load_dword v25, v[54:55], off nt
	global_load_dword v26, v[56:57], off nt
	global_load_dword v27, v[58:59], off nt
	global_load_dword v28, v[60:61], off nt
	global_load_dword v29, v[62:63], off nt
	global_load_dword v30, v[64:65], off nt
	global_load_dword v31, v[66:67], off nt
	global_load_dword v32, v40, s[2:3] nt
	s_add_i32 s23, s18, s22
	s_cmp_gt_i32 s23, 0x321ff
	s_mov_b64 s[20:21], s[0:1]
	s_mov_b32 s68, s48
	s_mov_b32 s47, s45
	s_waitcnt lgkmcnt(0)
	v_mov_b32_e32 v79, v73
	s_mov_b32 s49, s46
	s_cbranch_scc1 .LBB0_3009
	s_cmpk_gt_i32 s23, 0x17ff
	s_cbranch_scc0 .LBB0_2960
	s_cmpk_gt_u32 s23, 0x1fff
	s_cbranch_scc0 .LBB0_2963
	s_cmpk_gt_u32 s23, 0x35ff
	s_cbranch_scc0 .LBB0_2964
	s_cmpk_gt_u32 s23, 0x4bff
	s_cbranch_scc0 .LBB0_2965
	s_cmpk_gt_u32 s23, 0x61ff
	s_cbranch_scc0 .LBB0_2966
	s_cmpk_gt_u32 s23, 0x79ff
	s_cbranch_scc0 .LBB0_2967
	s_cmpk_gt_u32 s23, 0x81ff
	s_cbranch_scc0 .LBB0_2968
	s_cmp_gt_u32 s23, 0x161ff
	s_cbranch_scc0 .LBB0_2969
	s_cmp_gt_u32 s23, 0x241ff
	s_mov_b64 s[14:15], -1
	s_cbranch_scc0 .LBB0_2970
	s_add_i32 s2, s23, 0xbe00
	s_bfe_u32 s3, s2, 0x6000a
	s_mulk_i32 s3, 0x2493
	s_lshr_b32 s8, s3, 16
	s_mul_i32 s3, s8, 0x1c00
	s_sub_i32 s2, s2, s3
	s_and_b32 s4, s2, 0xffff
	s_bfe_u32 s3, s2, 0xb0005
	s_lshl_b32 s2, s4, 6
	s_and_b32 s2, s2, 0x7c0
	s_mul_i32 s4, s8, 0x3800000
	v_readlane_b32 s16, v254, 0
	v_readlane_b32 s17, v254, 1
	s_add_u32 s4, s16, s4
	s_addc_u32 s5, s17, 0
	s_add_u32 s6, s96, 0x24a00000
	s_mov_b32 s11, 0
	v_readlane_b32 s18, v254, 2
	v_readlane_b32 s19, v254, 3
	s_addc_u32 s7, s97, 0
	s_mul_i32 s10, s8, 0xe00000
	s_mov_b64 s[8:9], 0
	s_branch .LBB0_2971

.LBB0_3008:
	s_lshl_b32 s14, s3, 5
	s_ashr_i32 s3, s20, 8
	s_ashr_i32 s15, s3, 31
	s_mul_i32 s13, s3, s13
	s_mul_hi_u32 s16, s3, s12
	s_add_i32 s13, s16, s13
	s_mul_i32 s15, s15, s12
	s_add_i32 s13, s13, s15
	s_mul_i32 s12, s3, s12
	s_lshl_b64 s[12:13], s[12:13], 8
	s_add_u32 s3, s12, s10
	s_addc_u32 s10, s13, s11
	s_mul_i32 s10, s10, s24
	s_mul_hi_u32 s11, s3, s24
	s_add_i32 s11, s11, s10
	s_mul_i32 s3, s3, s24
	s_add_u32 s3, s6, s3
	s_addc_u32 s6, s7, s11
	s_lshl_b32 s7, s20, 5
	s_and_b32 s7, s7, 0x1fe0
	s_add_u32 s20, s3, s7
	s_addc_u32 s21, s6, 0
	s_ashr_i32 s3, s14, 31
	s_mul_i32 s3, s8, s3
	s_mul_hi_u32 s6, s8, s14
	s_add_i32 s3, s6, s3
	s_mul_i32 s6, s9, s14
	s_add_i32 s7, s3, s6
	s_mul_i32 s6, s8, s14
	s_lshl_b64 s[6:7], s[6:7], 2
	s_add_u32 s4, s4, s6
	s_addc_u32 s5, s5, s7
	s_ashr_i32 s3, s2, 31
	s_lshl_b64 s[2:3], s[2:3], 2
	s_add_u32 s2, s4, s2
	s_addc_u32 s3, s5, s3
	v_mov_b32_e32 v41, 0
	v_lshl_add_u64 v[34:35], s[2:3], 0, v[40:41]
	s_waitcnt vmcnt(0)
	global_load_dword v80, v40, s[2:3] nt
	s_lshl_b64 s[2:3], s[8:9], 2
	v_lshl_add_u64 v[34:35], v[34:35], 0, s[2:3]
	v_lshl_add_u64 v[36:37], v[34:35], 0, s[2:3]
	v_lshl_add_u64 v[42:43], v[36:37], 0, s[2:3]
	v_lshl_add_u64 v[44:45], v[42:43], 0, s[2:3]
	v_lshl_add_u64 v[46:47], v[44:45], 0, s[2:3]
	v_lshl_add_u64 v[48:49], v[46:47], 0, s[2:3]
	v_lshl_add_u64 v[50:51], v[48:49], 0, s[2:3]
	global_load_dword v81, v[34:35], off nt
	global_load_dword v82, v[36:37], off nt
	global_load_dword v83, v[42:43], off nt
	global_load_dword v84, v[44:45], off nt
	global_load_dword v85, v[46:47], off nt
	global_load_dword v86, v[48:49], off nt
	global_load_dword v87, v[50:51], off nt
	v_lshl_add_u64 v[34:35], v[50:51], 0, s[2:3]
	global_load_dword v88, v[34:35], off nt
	v_lshl_add_u64 v[34:35], v[34:35], 0, s[2:3]
	global_load_dword v89, v[34:35], off nt
	v_lshl_add_u64 v[34:35], v[34:35], 0, s[2:3]
	global_load_dword v90, v[34:35], off nt
	v_lshl_add_u64 v[34:35], v[34:35], 0, s[2:3]
	global_load_dword v91, v[34:35], off nt
	v_lshl_add_u64 v[34:35], v[34:35], 0, s[2:3]
	global_load_dword v92, v[34:35], off nt
	v_lshl_add_u64 v[34:35], v[34:35], 0, s[2:3]
	global_load_dword v93, v[34:35], off nt
	v_lshl_add_u64 v[34:35], v[34:35], 0, s[2:3]
	global_load_dword v94, v[34:35], off nt
	v_lshl_add_u64 v[34:35], v[34:35], 0, s[2:3]
	global_load_dword v95, v[34:35], off nt
	v_lshl_add_u64 v[34:35], v[34:35], 0, s[2:3]
	global_load_dword v96, v[34:35], off nt
	v_lshl_add_u64 v[34:35], v[34:35], 0, s[2:3]
	global_load_dword v97, v[34:35], off nt
	v_lshl_add_u64 v[34:35], v[34:35], 0, s[2:3]
	global_load_dword v98, v[34:35], off nt
	v_lshl_add_u64 v[34:35], v[34:35], 0, s[2:3]
	global_load_dword v99, v[34:35], off nt
	v_lshl_add_u64 v[34:35], v[34:35], 0, s[2:3]
	global_load_dword v100, v[34:35], off nt
	v_lshl_add_u64 v[34:35], v[34:35], 0, s[2:3]
	global_load_dword v101, v[34:35], off nt
	v_lshl_add_u64 v[34:35], v[34:35], 0, s[2:3]
	global_load_dword v102, v[34:35], off nt
	v_lshl_add_u64 v[34:35], v[34:35], 0, s[2:3]
	global_load_dword v103, v[34:35], off nt
	v_lshl_add_u64 v[34:35], v[34:35], 0, s[2:3]
	global_load_dword v104, v[34:35], off nt
	v_lshl_add_u64 v[34:35], v[34:35], 0, s[2:3]
	global_load_dword v105, v[34:35], off nt
	v_lshl_add_u64 v[34:35], v[34:35], 0, s[2:3]
	global_load_dword v106, v[34:35], off nt
	v_lshl_add_u64 v[34:35], v[34:35], 0, s[2:3]
	global_load_dword v107, v[34:35], off nt
	v_lshl_add_u64 v[34:35], v[34:35], 0, s[2:3]
	global_load_dword v108, v[34:35], off nt
	v_lshl_add_u64 v[34:35], v[34:35], 0, s[2:3]
	global_load_dword v109, v[34:35], off nt
	v_lshl_add_u64 v[34:35], v[34:35], 0, s[2:3]
	global_load_dword v110, v[34:35], off nt
	v_lshl_add_u64 v[34:35], v[34:35], 0, s[2:3]
	global_load_dword v111, v[34:35], off nt
	s_mul_i32 s68, s14, s24

.LBB0_3062:
	s_ashr_i32 s27, s71, 8
	s_ashr_i32 s34, s27, 31
	s_mul_i32 s23, s27, s23
	s_mul_hi_u32 s35, s27, s22
	s_add_i32 s23, s35, s23
	s_mul_i32 s34, s34, s22
	s_add_i32 s23, s23, s34
	s_mul_i32 s22, s27, s22
	s_lshl_b32 s40, s69, 5
	s_lshl_b64 s[22:23], s[22:23], 8
	s_add_u32 s22, s22, s36
	s_addc_u32 s23, s23, s37
	s_mul_i32 s23, s23, s18
	s_mul_hi_u32 s27, s22, s18
	s_add_i32 s27, s27, s23
	s_mul_i32 s22, s22, s18
	s_add_u32 s22, s38, s22
	s_addc_u32 s23, s39, s27
	s_lshl_b32 s27, s71, 5
	s_and_b32 s27, s27, 0x1fe0
	s_add_u32 s22, s22, s27
	s_addc_u32 s23, s23, 0
	s_ashr_i32 s27, s40, 31
	s_mul_i32 s27, s30, s27
	s_mul_hi_u32 s34, s30, s40
	s_add_i32 s27, s34, s27
	s_mul_i32 s34, s31, s40
	s_add_i32 s35, s27, s34
	s_mul_i32 s34, s30, s40
	s_lshl_b64 s[34:35], s[34:35], 2
	s_add_u32 s28, s28, s34
	s_addc_u32 s29, s29, s35
	s_ashr_i32 s27, s26, 31
	s_lshl_b64 s[26:27], s[26:27], 2
	s_add_u32 s26, s28, s26
	s_addc_u32 s27, s29, s27
	v_lshl_add_u64 v[34:35], s[26:27], 0, v[40:41]
	s_waitcnt vmcnt(0)
	global_load_dword v42, v40, s[26:27] nt
	s_lshl_b64 s[26:27], s[30:31], 2
	v_lshl_add_u64 v[34:35], v[34:35], 0, s[26:27]
	v_lshl_add_u64 v[36:37], v[34:35], 0, s[26:27]
	s_waitcnt vmcnt(26)
	v_lshl_add_u64 v[46:47], v[36:37], 0, s[26:27]
	s_waitcnt vmcnt(23)
	v_lshl_add_u64 v[48:49], v[46:47], 0, s[26:27]
	s_waitcnt vmcnt(22)
	v_lshl_add_u64 v[50:51], v[48:49], 0, s[26:27]
	s_waitcnt vmcnt(19)
	v_lshl_add_u64 v[52:53], v[50:51], 0, s[26:27]
	s_waitcnt vmcnt(18)
	v_lshl_add_u64 v[54:55], v[52:53], 0, s[26:27]
	global_load_dword v44, v[34:35], off nt
	global_load_dword v33, v[36:37], off nt
	global_load_dword v43, v[46:47], off nt
	s_nop 0
	global_load_dword v46, v[48:49], off nt
	s_nop 0
	global_load_dword v48, v[50:51], off nt
	global_load_dword v45, v[52:53], off nt
	global_load_dword v47, v[54:55], off nt
	v_lshl_add_u64 v[34:35], v[54:55], 0, s[26:27]
	global_load_dword v50, v[34:35], off nt
	v_lshl_add_u64 v[34:35], v[34:35], 0, s[26:27]
	global_load_dword v52, v[34:35], off nt
	v_lshl_add_u64 v[34:35], v[34:35], 0, s[26:27]
	global_load_dword v49, v[34:35], off nt
	v_lshl_add_u64 v[34:35], v[34:35], 0, s[26:27]
	global_load_dword v51, v[34:35], off nt
	v_lshl_add_u64 v[34:35], v[34:35], 0, s[26:27]
	global_load_dword v54, v[34:35], off nt
	v_lshl_add_u64 v[34:35], v[34:35], 0, s[26:27]
	global_load_dword v56, v[34:35], off nt
	v_lshl_add_u64 v[34:35], v[34:35], 0, s[26:27]
	global_load_dword v53, v[34:35], off nt
	v_lshl_add_u64 v[34:35], v[34:35], 0, s[26:27]
	global_load_dword v55, v[34:35], off nt
	v_lshl_add_u64 v[34:35], v[34:35], 0, s[26:27]
	global_load_dword v58, v[34:35], off nt
	v_lshl_add_u64 v[34:35], v[34:35], 0, s[26:27]
	global_load_dword v60, v[34:35], off nt
	v_lshl_add_u64 v[34:35], v[34:35], 0, s[26:27]
	global_load_dword v57, v[34:35], off nt
	v_lshl_add_u64 v[34:35], v[34:35], 0, s[26:27]
	global_load_dword v59, v[34:35], off nt
	v_lshl_add_u64 v[34:35], v[34:35], 0, s[26:27]
	global_load_dword v62, v[34:35], off nt
	v_lshl_add_u64 v[34:35], v[34:35], 0, s[26:27]
	global_load_dword v64, v[34:35], off nt
	v_lshl_add_u64 v[34:35], v[34:35], 0, s[26:27]
	global_load_dword v61, v[34:35], off nt
	v_lshl_add_u64 v[34:35], v[34:35], 0, s[26:27]
	global_load_dword v63, v[34:35], off nt
	v_lshl_add_u64 v[34:35], v[34:35], 0, s[26:27]
	global_load_dword v66, v[34:35], off nt
	v_lshl_add_u64 v[34:35], v[34:35], 0, s[26:27]
	global_load_dword v68, v[34:35], off nt
	v_lshl_add_u64 v[34:35], v[34:35], 0, s[26:27]
	global_load_dword v65, v[34:35], off nt
	v_lshl_add_u64 v[34:35], v[34:35], 0, s[26:27]
	global_load_dword v67, v[34:35], off nt
	v_lshl_add_u64 v[34:35], v[34:35], 0, s[26:27]
	global_load_dword v70, v[34:35], off nt
	v_lshl_add_u64 v[34:35], v[34:35], 0, s[26:27]
	global_load_dword v72, v[34:35], off nt
	v_lshl_add_u64 v[34:35], v[34:35], 0, s[26:27]
	global_load_dword v69, v[34:35], off nt
	v_lshl_add_u64 v[34:35], v[34:35], 0, s[26:27]
	global_load_dword v71, v[34:35], off nt
	s_mul_i32 s69, s40, s18

.LBB0_3127:
	s_ashr_i32 s34, s71, 8
	s_ashr_i32 s35, s34, 31
	s_mul_i32 s1, s34, s1
	s_mul_hi_u32 s40, s34, s0
	s_add_i32 s1, s40, s1
	s_mul_i32 s35, s35, s0
	s_add_i32 s1, s1, s35
	s_mul_i32 s0, s34, s0
	s_lshl_b32 s27, s48, 5
	s_lshl_b64 s[0:1], s[0:1], 8
	s_add_u32 s0, s0, s36
	s_addc_u32 s1, s1, s37
	s_mul_i32 s1, s1, s18
	s_mul_hi_u32 s34, s0, s18
	s_add_i32 s34, s34, s1
	s_mul_i32 s0, s0, s18
	s_add_u32 s0, s38, s0
	s_mul_i32 s48, s27, s18
	s_addc_u32 s1, s39, s34
	s_lshl_b32 s18, s71, 5
	s_and_b32 s18, s18, 0x1fe0
	s_add_u32 s0, s0, s18
	s_addc_u32 s1, s1, 0
	s_ashr_i32 s18, s27, 31
	s_mul_i32 s18, s30, s18
	s_mul_hi_u32 s34, s30, s27
	s_add_i32 s18, s34, s18
	s_mul_i32 s34, s31, s27
	s_add_i32 s35, s18, s34
	s_mul_i32 s34, s30, s27
	s_lshl_b64 s[34:35], s[34:35], 2
	s_add_u32 s18, s28, s34
	s_addc_u32 s28, s29, s35
	s_ashr_i32 s27, s26, 31
	s_lshl_b64 s[26:27], s[26:27], 2
	s_add_u32 s26, s18, s26
	s_addc_u32 s27, s28, s27
	s_waitcnt vmcnt(30)
	v_lshl_add_u64 v[2:3], s[26:27], 0, v[40:41]
	s_lshl_b64 s[28:29], s[30:31], 2
	v_lshl_add_u64 v[2:3], v[2:3], 0, s[28:29]
	s_waitcnt vmcnt(28)
	v_lshl_add_u64 v[4:5], v[2:3], 0, s[28:29]
	s_waitcnt vmcnt(26)
	v_lshl_add_u64 v[6:7], v[4:5], 0, s[28:29]
	s_waitcnt vmcnt(24)
	v_lshl_add_u64 v[8:9], v[6:7], 0, s[28:29]
	s_waitcnt vmcnt(22)
	v_lshl_add_u64 v[10:11], v[8:9], 0, s[28:29]
	s_waitcnt vmcnt(20)
	v_lshl_add_u64 v[12:13], v[10:11], 0, s[28:29]
	s_waitcnt vmcnt(18)
	v_lshl_add_u64 v[14:15], v[12:13], 0, s[28:29]
	s_waitcnt vmcnt(16)
	v_lshl_add_u64 v[16:17], v[14:15], 0, s[28:29]
	s_waitcnt vmcnt(14)
	v_lshl_add_u64 v[18:19], v[16:17], 0, s[28:29]
	s_waitcnt vmcnt(12)
	v_lshl_add_u64 v[20:21], v[18:19], 0, s[28:29]
	s_waitcnt vmcnt(10)
	v_lshl_add_u64 v[22:23], v[20:21], 0, s[28:29]
	s_waitcnt vmcnt(8)
	v_lshl_add_u64 v[24:25], v[22:23], 0, s[28:29]
	s_waitcnt vmcnt(6)
	v_lshl_add_u64 v[26:27], v[24:25], 0, s[28:29]
	s_waitcnt vmcnt(4)
	v_lshl_add_u64 v[28:29], v[26:27], 0, s[28:29]
	s_waitcnt vmcnt(2)
	v_lshl_add_u64 v[30:31], v[28:29], 0, s[28:29]
	v_lshl_add_u64 v[34:35], v[30:31], 0, s[28:29]
	v_lshl_add_u64 v[36:37], v[34:35], 0, s[28:29]
	v_lshl_add_u64 v[74:75], v[36:37], 0, s[28:29]
	v_lshl_add_u64 v[114:115], v[74:75], 0, s[28:29]
	v_lshl_add_u64 v[116:117], v[114:115], 0, s[28:29]
	v_lshl_add_u64 v[118:119], v[116:117], 0, s[28:29]
	v_lshl_add_u64 v[120:121], v[118:119], 0, s[28:29]
	v_lshl_add_u64 v[122:123], v[120:121], 0, s[28:29]
	v_lshl_add_u64 v[124:125], v[122:123], 0, s[28:29]
	v_lshl_add_u64 v[126:127], v[124:125], 0, s[28:29]
	v_lshl_add_u64 v[128:129], v[126:127], 0, s[28:29]
	v_lshl_add_u64 v[130:131], v[128:129], 0, s[28:29]
	v_lshl_add_u64 v[132:133], v[130:131], 0, s[28:29]
	v_lshl_add_u64 v[134:135], v[132:133], 0, s[28:29]
	v_lshl_add_u64 v[136:137], v[134:135], 0, s[28:29]
	v_lshl_add_u64 v[138:139], v[136:137], 0, s[28:29]
	s_waitcnt vmcnt(0)
	global_load_dword v1, v[2:3], off nt
	s_nop 0
	global_load_dword v2, v[4:5], off nt
	global_load_dword v3, v[6:7], off nt
	s_nop 0
	global_load_dword v4, v[8:9], off nt
	global_load_dword v5, v[10:11], off nt
	global_load_dword v6, v[12:13], off nt
	global_load_dword v7, v[14:15], off nt
	s_nop 0
	global_load_dword v8, v[16:17], off nt
	global_load_dword v9, v[18:19], off nt
	global_load_dword v10, v[20:21], off nt
	global_load_dword v11, v[22:23], off nt
	global_load_dword v12, v[24:25], off nt
	global_load_dword v13, v[26:27], off nt
	global_load_dword v14, v[28:29], off nt
	global_load_dword v15, v[30:31], off nt
	global_load_dword v16, v[34:35], off nt
	global_load_dword v17, v[36:37], off nt
	global_load_dword v18, v[74:75], off nt
	global_load_dword v19, v[114:115], off nt
	global_load_dword v20, v[116:117], off nt
	global_load_dword v21, v[118:119], off nt
	global_load_dword v22, v[120:121], off nt
	global_load_dword v23, v[122:123], off nt
	global_load_dword v24, v[124:125], off nt
	global_load_dword v25, v[126:127], off nt
	global_load_dword v26, v[128:129], off nt
	global_load_dword v27, v[130:131], off nt
	global_load_dword v28, v[132:133], off nt
	global_load_dword v29, v[134:135], off nt
	global_load_dword v30, v[136:137], off nt
	global_load_dword v31, v[138:139], off nt
	global_load_dword v32, v40, s[26:27] nt

.LBB0_3193:
	s_ashr_i32 s25, s68, 8
	s_ashr_i32 s30, s25, 31
	s_mul_i32 s21, s25, s21
	s_mul_hi_u32 s31, s25, s20
	s_add_i32 s21, s31, s21
	s_mul_i32 s30, s30, s20
	s_add_i32 s21, s21, s30
	s_mul_i32 s20, s25, s20
	s_lshl_b32 s38, s42, 5
	s_lshl_b64 s[20:21], s[20:21], 8
	s_add_u32 s20, s20, s34
	s_addc_u32 s21, s21, s35
	s_mul_i32 s21, s21, s18
	s_mul_hi_u32 s25, s20, s18
	s_add_i32 s25, s25, s21
	s_mul_i32 s20, s20, s18
	s_add_u32 s20, s36, s20
	s_addc_u32 s21, s37, s25
	s_lshl_b32 s25, s68, 5
	s_and_b32 s25, s25, 0x1fe0
	s_add_u32 s20, s20, s25
	s_addc_u32 s21, s21, 0
	s_ashr_i32 s25, s38, 31
	s_mul_i32 s25, s28, s25
	s_mul_hi_u32 s30, s28, s38
	s_add_i32 s25, s30, s25
	s_mul_i32 s30, s29, s38
	s_add_i32 s31, s25, s30
	s_mul_i32 s30, s28, s38
	s_lshl_b64 s[30:31], s[30:31], 2
	s_add_u32 s26, s26, s30
	s_addc_u32 s27, s27, s31
	s_ashr_i32 s25, s24, 31
	s_lshl_b64 s[24:25], s[24:25], 2
	s_add_u32 s24, s26, s24
	s_addc_u32 s25, s27, s25
	v_lshl_add_u64 v[34:35], s[24:25], 0, v[40:41]
	s_waitcnt vmcnt(0)
	global_load_dword v80, v40, s[24:25] nt
	s_lshl_b64 s[24:25], s[28:29], 2
	v_lshl_add_u64 v[34:35], v[34:35], 0, s[24:25]
	v_lshl_add_u64 v[36:37], v[34:35], 0, s[24:25]
	v_lshl_add_u64 v[74:75], v[36:37], 0, s[24:25]
	s_waitcnt vmcnt(29)
	v_lshl_add_u64 v[84:85], v[74:75], 0, s[24:25]
	s_waitcnt vmcnt(27)
	v_lshl_add_u64 v[86:87], v[84:85], 0, s[24:25]
	s_waitcnt vmcnt(25)
	v_lshl_add_u64 v[88:89], v[86:87], 0, s[24:25]
	s_waitcnt vmcnt(23)
	v_lshl_add_u64 v[90:91], v[88:89], 0, s[24:25]
	global_load_dword v81, v[34:35], off nt
	global_load_dword v82, v[36:37], off nt
	global_load_dword v83, v[74:75], off nt
	s_nop 0
	global_load_dword v84, v[84:85], off nt
	s_nop 0
	global_load_dword v85, v[86:87], off nt
	s_nop 0
	global_load_dword v86, v[88:89], off nt
	global_load_dword v87, v[90:91], off nt
	v_lshl_add_u64 v[34:35], v[90:91], 0, s[24:25]
	global_load_dword v88, v[34:35], off nt
	v_lshl_add_u64 v[34:35], v[34:35], 0, s[24:25]
	global_load_dword v89, v[34:35], off nt
	v_lshl_add_u64 v[34:35], v[34:35], 0, s[24:25]
	global_load_dword v90, v[34:35], off nt
	v_lshl_add_u64 v[34:35], v[34:35], 0, s[24:25]
	global_load_dword v91, v[34:35], off nt
	v_lshl_add_u64 v[34:35], v[34:35], 0, s[24:25]
	global_load_dword v92, v[34:35], off nt
	v_lshl_add_u64 v[34:35], v[34:35], 0, s[24:25]
	global_load_dword v93, v[34:35], off nt
	v_lshl_add_u64 v[34:35], v[34:35], 0, s[24:25]
	global_load_dword v94, v[34:35], off nt
	v_lshl_add_u64 v[34:35], v[34:35], 0, s[24:25]
	global_load_dword v95, v[34:35], off nt
	v_lshl_add_u64 v[34:35], v[34:35], 0, s[24:25]
	global_load_dword v96, v[34:35], off nt
	v_lshl_add_u64 v[34:35], v[34:35], 0, s[24:25]
	global_load_dword v97, v[34:35], off nt
	v_lshl_add_u64 v[34:35], v[34:35], 0, s[24:25]
	global_load_dword v98, v[34:35], off nt
	v_lshl_add_u64 v[34:35], v[34:35], 0, s[24:25]
	global_load_dword v99, v[34:35], off nt
	v_lshl_add_u64 v[34:35], v[34:35], 0, s[24:25]
	global_load_dword v100, v[34:35], off nt
	v_lshl_add_u64 v[34:35], v[34:35], 0, s[24:25]
	global_load_dword v101, v[34:35], off nt
	v_lshl_add_u64 v[34:35], v[34:35], 0, s[24:25]
	global_load_dword v102, v[34:35], off nt
	v_lshl_add_u64 v[34:35], v[34:35], 0, s[24:25]
	global_load_dword v103, v[34:35], off nt
	v_lshl_add_u64 v[34:35], v[34:35], 0, s[24:25]
	global_load_dword v104, v[34:35], off nt
	v_lshl_add_u64 v[34:35], v[34:35], 0, s[24:25]
	global_load_dword v105, v[34:35], off nt
	v_lshl_add_u64 v[34:35], v[34:35], 0, s[24:25]
	global_load_dword v106, v[34:35], off nt
	v_lshl_add_u64 v[34:35], v[34:35], 0, s[24:25]
	global_load_dword v107, v[34:35], off nt
	v_lshl_add_u64 v[34:35], v[34:35], 0, s[24:25]
	global_load_dword v108, v[34:35], off nt
	v_lshl_add_u64 v[34:35], v[34:35], 0, s[24:25]
	global_load_dword v109, v[34:35], off nt
	v_lshl_add_u64 v[34:35], v[34:35], 0, s[24:25]
	global_load_dword v110, v[34:35], off nt
	v_lshl_add_u64 v[34:35], v[34:35], 0, s[24:25]
	global_load_dword v111, v[34:35], off nt
	s_mul_i32 s68, s38, s18
